# v27: v26 + removed back-to-back prio 0/1 flips inside GEMM compute segments
# baseline (speedup 1.0000x reference)
; #define PG8_STAGE(bufoff, gbase, voff) do { _Pragma("unroll") for (int _i = 0; _i < 2; ++_i) \
;         __builtin_amdgcn_global_load_lds((const unsigned*)((const char*)(gbase) + (voff)[_i]), (PG8_LAS unsigned*)(lds + (bufoff) + ldsw + _i * 8192), 16, 0, 0); } while (0)
; #define PG8_LDA(dst, b, h) do { _Pragma("unroll") for (int m = 0; m < 4; ++m) _Pragma("unroll") for (int k = 0; k < 2; ++k) dst[m][k] = *(const PG8_LAS bf16x8*)(lds + PG8_SA(b, h) + aoff + m * 2048 + k * 1024); } while (0)
; #define PG8_LDB(dst, b, h) do { _Pragma("unroll") for (int n = 0; n < 2; ++n) _Pragma("unroll") for (int k = 0; k < 2; ++k) dst[n][k] = *(const PG8_LAS bf16x8*)(lds + PG8_SB(b, h) + boff + n * 2048 + k * 1024); } while (0)
; #define PG8_MMA(ai, bj, At, Bt) do { __builtin_amdgcn_s_setprio(1); _Pragma("unroll") for (int m = 0; m < 4; ++m) _Pragma("unroll") for (int n = 0; n < 2; ++n) _Pragma("unroll") for (int k = 0; k < 2; ++k) \
;         acc[ai][bj][m][n] = __builtin_amdgcn_mfma_f32_16x16x32_bf16(Bt[n][k], At[m][k], acc[ai][bj][m][n], 0, 0, 0); __builtin_amdgcn_s_setprio(0); } while (0)
; #define PG8_WAIT_V(n) asm volatile("s_waitcnt vmcnt(" #n ")" ::: "memory")
; #define PG8_WAIT_L(n) asm volatile("s_waitcnt lgkmcnt(" #n ")" ::: "memory")
; #define PG8_BAR __builtin_amdgcn_s_barrier()
; #define PG8_SCHED __builtin_amdgcn_sched_barrier(0)
; template <class Epi, class Sched, bool ALIGN_EPI = false, bool SP2 = false>
; __device__ __forceinline__ void gemm_phase(PG8_LAS unsigned char* lds, const Gemm g, const Sched& S, const Epi& E, const int wid) {
;     ...
;             if constexpr (SP2) {
;             PG8_LDB(B0, 0, 0); PG8_LDB(B1, 0, 1); PG8_SCHED; PG8_LDA(At, 0, 0); PG8_STAGE(PG8_SA(1, 1), a1 + hstepA, voffA);
;             PG8_WAIT_V(8); PG8_WAIT_L(0); PG8_BAR; PG8_MMA(0, 0, At, B0); PG8_MMA(0, 1, At, B1); PG8_BAR; PG8_SCHED;
;             PG8_LDA(At, 0, 1); PG8_STAGE(PG8_SB(0, 0), b2, voffB); PG8_STAGE(PG8_SB(0, 1), b2 + hstepB, voffB); PG8_STAGE(PG8_SA(0, 0), a2, voffA);
;             PG8_WAIT_V(8); PG8_WAIT_L(0); PG8_BAR; PG8_MMA(1, 0, At, B0); PG8_MMA(1, 1, At, B1); PG8_BAR; PG8_SCHED;
.LBB0_349:
	ds_read_b128 v[128:131], v183
	ds_read_b128 v[150:153], v183 offset:1024
	ds_read_b128 v[154:157], v183 offset:2048
	ds_read_b128 v[158:161], v183 offset:3072
	ds_read_b128 v[162:165], v184
	ds_read_b128 v[166:169], v184 offset:1024
	ds_read_b128 v[170:173], v184 offset:2048
	ds_read_b128 v[188:191], v184 offset:3072
	s_add_u32 s36, s8, 0xfffc0080
	s_addc_u32 s37, s9, -1
	s_cmp_eq_u32 s75, 12
	s_cselect_b32 s41, s7, s37
	s_cselect_b32 s40, s27, s36
	s_cselect_b32 s37, s25, s74
	s_cselect_b32 s36, s35, s73
	s_add_i32 m0, s46, 0xc000
	ds_read_b128 v[192:195], v185
	ds_read_b128 v[196:199], v185 offset:1024
	ds_read_b128 v[200:203], v185 offset:2048
	ds_read_b128 v[204:207], v185 offset:3072
	ds_read_b128 v[208:211], v185 offset:4096
	ds_read_b128 v[212:215], v185 offset:5120
	ds_read_b128 v[216:219], v185 offset:6144
	ds_read_b128 v[220:223], v185 offset:7168
	global_load_lds_dwordx4 v142, s[8:9]
	s_add_i32 m0, s46, 0xe000
	s_nop 0
	global_load_lds_dwordx4 v144, s[8:9]
	s_waitcnt vmcnt(8) lgkmcnt(0)
	s_barrier
	s_setprio 1
	v_mfma_f32_16x16x32_bf16 v[124:127], v[128:131], v[192:195], v[124:127]
	v_mfma_f32_16x16x32_bf16 v[120:123], v[154:157], v[192:195], v[120:123]
	v_mfma_f32_16x16x32_bf16 v[108:111], v[128:131], v[200:203], v[108:111]
	v_mfma_f32_16x16x32_bf16 v[104:107], v[154:157], v[200:203], v[104:107]
	v_mfma_f32_16x16x32_bf16 v[92:95], v[128:131], v[208:211], v[92:95]
	v_mfma_f32_16x16x32_bf16 v[88:91], v[154:157], v[208:211], v[88:91]
	v_mfma_f32_16x16x32_bf16 v[76:79], v[128:131], v[216:219], v[76:79]
	v_mfma_f32_16x16x32_bf16 v[72:75], v[154:157], v[216:219], v[72:75]
	v_mfma_f32_16x16x32_bf16 v[124:127], v[150:153], v[196:199], v[124:127]
	v_mfma_f32_16x16x32_bf16 v[120:123], v[158:161], v[196:199], v[120:123]
	v_mfma_f32_16x16x32_bf16 v[108:111], v[150:153], v[204:207], v[108:111]
	v_mfma_f32_16x16x32_bf16 v[104:107], v[158:161], v[204:207], v[104:107]
	v_mfma_f32_16x16x32_bf16 v[92:95], v[150:153], v[212:215], v[92:95]
	v_mfma_f32_16x16x32_bf16 v[88:91], v[158:161], v[212:215], v[88:91]
	v_mfma_f32_16x16x32_bf16 v[76:79], v[150:153], v[220:223], v[76:79]
	v_mfma_f32_16x16x32_bf16 v[72:75], v[158:161], v[220:223], v[72:75]
	v_mfma_f32_16x16x32_bf16 v[116:119], v[162:165], v[192:195], v[116:119]
	v_mfma_f32_16x16x32_bf16 v[112:115], v[170:173], v[192:195], v[112:115]
	v_mfma_f32_16x16x32_bf16 v[100:103], v[162:165], v[200:203], v[100:103]
	v_mfma_f32_16x16x32_bf16 v[96:99], v[170:173], v[200:203], v[96:99]
	v_mfma_f32_16x16x32_bf16 v[84:87], v[162:165], v[208:211], v[84:87]
	v_mfma_f32_16x16x32_bf16 v[80:83], v[170:173], v[208:211], v[80:83]
	v_mfma_f32_16x16x32_bf16 v[68:71], v[162:165], v[216:219], v[68:71]
	v_mfma_f32_16x16x32_bf16 v[64:67], v[170:173], v[216:219], v[64:67]
	v_mfma_f32_16x16x32_bf16 v[116:119], v[166:169], v[196:199], v[116:119]
	v_mfma_f32_16x16x32_bf16 v[112:115], v[188:191], v[196:199], v[112:115]
	v_mfma_f32_16x16x32_bf16 v[100:103], v[166:169], v[204:207], v[100:103]
	v_mfma_f32_16x16x32_bf16 v[96:99], v[188:191], v[204:207], v[96:99]
	v_mfma_f32_16x16x32_bf16 v[84:87], v[166:169], v[212:215], v[84:87]
	v_mfma_f32_16x16x32_bf16 v[80:83], v[188:191], v[212:215], v[80:83]
	v_mfma_f32_16x16x32_bf16 v[68:71], v[166:169], v[220:223], v[68:71]
	v_mfma_f32_16x16x32_bf16 v[64:67], v[188:191], v[220:223], v[64:67]
	s_setprio 0
	s_barrier
	s_add_i32 s76, s69, s45
	v_lshl_add_u64 v[174:175], s[36:37], 0, v[134:135]
	s_mov_b32 m0, s76
	ds_read_b128 v[192:195], v185 offset:16384
	ds_read_b128 v[196:199], v185 offset:17408
	ds_read_b128 v[200:203], v185 offset:18432
	ds_read_b128 v[204:207], v185 offset:19456
	ds_read_b128 v[208:211], v185 offset:20480
	ds_read_b128 v[212:215], v185 offset:21504
	ds_read_b128 v[216:219], v185 offset:22528
	ds_read_b128 v[220:223], v185 offset:23552
	global_load_lds_dwordx4 v134, s[36:37]
	s_add_i32 m0, s76, 0x2000
	s_add_u32 s76, s36, 0x40000
	v_lshl_add_u64 v[224:225], s[36:37], 0, v[138:139]
	s_addc_u32 s77, s37, 0
	s_add_i32 s78, s70, s45
	global_load_lds_dwordx4 v138, s[36:37]
	s_mov_b32 m0, s78
	v_lshl_add_u64 v[228:229], s[40:41], 0, v[136:137]
	global_load_lds_dwordx4 v134, s[76:77]
	s_add_i32 m0, s78, 0x2000
	s_nop 0
	global_load_lds_dwordx4 v138, s[76:77]
	v_lshl_add_u64 v[226:227], s[40:41], 0, v[132:133]
	s_mov_b32 m0, s46
	s_nop 0
	global_load_lds_dwordx4 v132, s[40:41]
	s_mov_b32 m0, s47
	s_nop 0
	global_load_lds_dwordx4 v136, s[40:41]
	s_waitcnt vmcnt(8) lgkmcnt(0)
	s_barrier
	s_setprio 1
	v_mfma_f32_16x16x32_bf16 v[60:63], v[128:131], v[192:195], v[60:63]
	v_mfma_f32_16x16x32_bf16 v[56:59], v[154:157], v[192:195], v[56:59]
	v_mfma_f32_16x16x32_bf16 v[44:47], v[128:131], v[200:203], v[44:47]
	v_mfma_f32_16x16x32_bf16 v[40:43], v[154:157], v[200:203], v[40:43]
	v_mfma_f32_16x16x32_bf16 v[28:31], v[128:131], v[208:211], v[28:31]
	v_mfma_f32_16x16x32_bf16 v[24:27], v[154:157], v[208:211], v[24:27]
	v_mfma_f32_16x16x32_bf16 v[12:15], v[128:131], v[216:219], v[12:15]
	v_mfma_f32_16x16x32_bf16 v[8:11], v[154:157], v[216:219], v[8:11]
	v_mfma_f32_16x16x32_bf16 v[60:63], v[150:153], v[196:199], v[60:63]
	v_mfma_f32_16x16x32_bf16 v[56:59], v[158:161], v[196:199], v[56:59]
	v_mfma_f32_16x16x32_bf16 v[44:47], v[150:153], v[204:207], v[44:47]
	v_mfma_f32_16x16x32_bf16 v[40:43], v[158:161], v[204:207], v[40:43]
	v_mfma_f32_16x16x32_bf16 v[28:31], v[150:153], v[212:215], v[28:31]
	v_mfma_f32_16x16x32_bf16 v[24:27], v[158:161], v[212:215], v[24:27]
	v_mfma_f32_16x16x32_bf16 v[12:15], v[150:153], v[220:223], v[12:15]
	v_mfma_f32_16x16x32_bf16 v[8:11], v[158:161], v[220:223], v[8:11]
	v_mfma_f32_16x16x32_bf16 v[52:55], v[162:165], v[192:195], v[52:55]
	v_mfma_f32_16x16x32_bf16 v[48:51], v[170:173], v[192:195], v[48:51]
	v_mfma_f32_16x16x32_bf16 v[36:39], v[162:165], v[200:203], v[36:39]
	v_mfma_f32_16x16x32_bf16 v[32:35], v[170:173], v[200:203], v[32:35]
	v_mfma_f32_16x16x32_bf16 v[20:23], v[162:165], v[208:211], v[20:23]
	v_mfma_f32_16x16x32_bf16 v[16:19], v[170:173], v[208:211], v[16:19]
	v_mfma_f32_16x16x32_bf16 v[4:7], v[162:165], v[216:219], v[4:7]
	v_mfma_f32_16x16x32_bf16 v[0:3], v[170:173], v[216:219], v[0:3]
	v_mfma_f32_16x16x32_bf16 v[52:55], v[166:169], v[196:199], v[52:55]
	v_mfma_f32_16x16x32_bf16 v[48:51], v[188:191], v[196:199], v[48:51]
	v_mfma_f32_16x16x32_bf16 v[36:39], v[166:169], v[204:207], v[36:39]
	v_mfma_f32_16x16x32_bf16 v[32:35], v[188:191], v[204:207], v[32:35]
	v_mfma_f32_16x16x32_bf16 v[20:23], v[166:169], v[212:215], v[20:23]
	v_mfma_f32_16x16x32_bf16 v[16:19], v[188:191], v[212:215], v[16:19]
	v_mfma_f32_16x16x32_bf16 v[4:7], v[166:169], v[220:223], v[4:7]
	v_mfma_f32_16x16x32_bf16 v[0:3], v[188:191], v[220:223], v[0:3]
	s_setprio 0
	s_barrier
; #define PG8_STAGE(bufoff, gbase, voff) do { _Pragma("unroll") for (int _i = 0; _i < 2; ++_i) \
;         __builtin_amdgcn_global_load_lds((const unsigned*)((const char*)(gbase) + (voff)[_i]), (PG8_LAS unsigned*)(lds + (bufoff) + ldsw + _i * 8192), 16, 0, 0); } while (0)
; #define PG8_LDA(dst, b, h) do { _Pragma("unroll") for (int m = 0; m < 4; ++m) _Pragma("unroll") for (int k = 0; k < 2; ++k) dst[m][k] = *(const PG8_LAS bf16x8*)(lds + PG8_SA(b, h) + aoff + m * 2048 + k * 1024); } while (0)
; #define PG8_WAIT_V(n) asm volatile("s_waitcnt vmcnt(" #n ")" ::: "memory")
; #define PG8_WAIT_L(n) asm volatile("s_waitcnt lgkmcnt(" #n ")" ::: "memory")
; #define PG8_BAR __builtin_amdgcn_s_barrier()
; template <class Epi, class Sched, bool ALIGN_EPI = false, bool SP2 = false>
; __device__ __forceinline__ void gemm_phase(PG8_LAS unsigned char* lds, const Gemm g, const Sched& S, const Epi& E, const int wid) {
;     ...
;         for (int t = 0; t < nt; t += 2) {
;             const bool last = (t == nt - 2);
;             const char* a1 = cA + (size_t)(t + 1) * kstep;
;             const char* a2 = last ? nA : cA + (size_t)(t + 2) * kstep; const char* b2 = last ? nB : cB + (size_t)(t + 2) * kstep;
;             const char* a3 = a2 + kstep; const char* b3 = b2 + kstep;
;             if (last && has_next) S.a_ready(nxt);
;             if constexpr (SP2) {
;             PG8_LDB(B0, 0, 0); PG8_LDB(B1, 0, 1); PG8_SCHED; PG8_LDA(At, 0, 0); PG8_STAGE(PG8_SA(1, 1), a1 + hstepA, voffA);
;             PG8_WAIT_V(8); PG8_WAIT_L(0); PG8_BAR; PG8_MMA(0, 0, At, B0); PG8_MMA(0, 1, At, B1); PG8_BAR; PG8_SCHED;
;             PG8_LDA(At, 0, 1); PG8_STAGE(PG8_SB(0, 0), b2, voffB); PG8_STAGE(PG8_SB(0, 1), b2 + hstepB, voffB); PG8_STAGE(PG8_SA(0, 0), a2, voffA);
;             PG8_WAIT_V(8); PG8_WAIT_L(0); PG8_BAR; PG8_MMA(1, 0, At, B0); PG8_MMA(1, 1, At, B1); PG8_BAR; PG8_SCHED;
;             PG8_LDB(B0, 1, 0); PG8_LDB(B1, 1, 1); PG8_SCHED; PG8_LDA(At, 1, 0); PG8_STAGE(PG8_SA(0, 1), a2 + hstepA, voffA);
;             PG8_WAIT_V(8); PG8_WAIT_L(0); PG8_BAR; PG8_MMA(0, 0, At, B0); PG8_MMA(0, 1, At, B1); PG8_BAR; PG8_SCHED;
;             PG8_LDA(At, 1, 1); PG8_STAGE(PG8_SB(1, 0), b3, voffB); PG8_STAGE(PG8_SB(1, 1), b3 + hstepB, voffB); PG8_STAGE(PG8_SA(1, 0), a3, voffA);
;             PG8_WAIT_V(8); PG8_WAIT_L(0); PG8_BAR; PG8_MMA(1, 0, At, B0); PG8_MMA(1, 1, At, B1); PG8_BAR; PG8_SCHED;
	s_add_i32 s76, 0, 0x18000
	s_add_i32 s77, 0, 0x1c000
	v_add_u32_e32 v158, s76, v178
	v_add_u32_e32 v188, s77, v178
	ds_read_b128 v[128:131], v158
	ds_read_b128 v[150:153], v158 offset:1024
	ds_read_b128 v[154:157], v158 offset:2048
	ds_read_b128 v[158:161], v158 offset:3072
	ds_read_b128 v[162:165], v188
	ds_read_b128 v[166:169], v188 offset:1024
	ds_read_b128 v[170:173], v188 offset:2048
	ds_read_b128 v[188:191], v188 offset:3072
	s_add_u32 s40, s40, 0x40000
	s_addc_u32 s41, s41, 0
	s_mov_b32 m0, s48
	ds_read_b128 v[192:195], v185 offset:32768
	ds_read_b128 v[196:199], v185 offset:33792
	ds_read_b128 v[200:203], v185 offset:34816
	ds_read_b128 v[204:207], v185 offset:35840
	ds_read_b128 v[208:211], v185 offset:36864
	ds_read_b128 v[212:215], v185 offset:37888
	ds_read_b128 v[216:219], v185 offset:38912
	ds_read_b128 v[220:223], v185 offset:39936
	global_load_lds_dwordx4 v132, s[40:41]
	s_mov_b32 m0, s49
	s_nop 0
	global_load_lds_dwordx4 v136, s[40:41]
	s_waitcnt vmcnt(8) lgkmcnt(0)
	s_barrier
	s_setprio 1
	v_mfma_f32_16x16x32_bf16 v[124:127], v[128:131], v[192:195], v[124:127]
	v_mfma_f32_16x16x32_bf16 v[120:123], v[154:157], v[192:195], v[120:123]
	v_mfma_f32_16x16x32_bf16 v[108:111], v[128:131], v[200:203], v[108:111]
	v_mfma_f32_16x16x32_bf16 v[104:107], v[154:157], v[200:203], v[104:107]
	v_mfma_f32_16x16x32_bf16 v[92:95], v[128:131], v[208:211], v[92:95]
	v_mfma_f32_16x16x32_bf16 v[88:91], v[154:157], v[208:211], v[88:91]
	v_mfma_f32_16x16x32_bf16 v[76:79], v[128:131], v[216:219], v[76:79]
	v_mfma_f32_16x16x32_bf16 v[72:75], v[154:157], v[216:219], v[72:75]
	v_mfma_f32_16x16x32_bf16 v[124:127], v[150:153], v[196:199], v[124:127]
	v_mfma_f32_16x16x32_bf16 v[120:123], v[158:161], v[196:199], v[120:123]
	v_mfma_f32_16x16x32_bf16 v[108:111], v[150:153], v[204:207], v[108:111]
	v_mfma_f32_16x16x32_bf16 v[104:107], v[158:161], v[204:207], v[104:107]
	v_mfma_f32_16x16x32_bf16 v[92:95], v[150:153], v[212:215], v[92:95]
	v_mfma_f32_16x16x32_bf16 v[88:91], v[158:161], v[212:215], v[88:91]
	v_mfma_f32_16x16x32_bf16 v[76:79], v[150:153], v[220:223], v[76:79]
	v_mfma_f32_16x16x32_bf16 v[72:75], v[158:161], v[220:223], v[72:75]
	v_mfma_f32_16x16x32_bf16 v[116:119], v[162:165], v[192:195], v[116:119]
	v_mfma_f32_16x16x32_bf16 v[112:115], v[170:173], v[192:195], v[112:115]
	v_mfma_f32_16x16x32_bf16 v[100:103], v[162:165], v[200:203], v[100:103]
	v_mfma_f32_16x16x32_bf16 v[96:99], v[170:173], v[200:203], v[96:99]
	v_mfma_f32_16x16x32_bf16 v[84:87], v[162:165], v[208:211], v[84:87]
	v_mfma_f32_16x16x32_bf16 v[80:83], v[170:173], v[208:211], v[80:83]
	v_mfma_f32_16x16x32_bf16 v[68:71], v[162:165], v[216:219], v[68:71]
	v_mfma_f32_16x16x32_bf16 v[64:67], v[170:173], v[216:219], v[64:67]
	v_mfma_f32_16x16x32_bf16 v[116:119], v[166:169], v[196:199], v[116:119]
	v_mfma_f32_16x16x32_bf16 v[112:115], v[188:191], v[196:199], v[112:115]
	v_mfma_f32_16x16x32_bf16 v[100:103], v[166:169], v[204:207], v[100:103]
	v_mfma_f32_16x16x32_bf16 v[96:99], v[188:191], v[204:207], v[96:99]
	v_mfma_f32_16x16x32_bf16 v[84:87], v[166:169], v[212:215], v[84:87]
	v_mfma_f32_16x16x32_bf16 v[80:83], v[188:191], v[212:215], v[80:83]
	v_mfma_f32_16x16x32_bf16 v[68:71], v[166:169], v[220:223], v[68:71]
	v_mfma_f32_16x16x32_bf16 v[64:67], v[188:191], v[220:223], v[64:67]
	s_setprio 0
	s_barrier
	s_add_i32 s40, s76, s45
	v_lshl_add_u64 v[174:175], v[174:175], 0, s[18:19]
	s_mov_b32 m0, s40
	ds_read_b128 v[192:195], v185 offset:49152
	ds_read_b128 v[196:199], v185 offset:50176
	ds_read_b128 v[200:203], v185 offset:51200
	ds_read_b128 v[204:207], v185 offset:52224
	ds_read_b128 v[208:211], v185 offset:53248
	ds_read_b128 v[212:215], v185 offset:54272
	ds_read_b128 v[216:219], v185 offset:55296
	ds_read_b128 v[220:223], v185 offset:56320
	global_load_lds_dwordx4 v[174:175], off
	s_add_i32 m0, s40, 0x2000
	s_add_u32 s36, s36, 0x40080
	v_lshl_add_u64 v[174:175], v[224:225], 0, s[18:19]
	s_addc_u32 s37, s37, 0
	s_add_i32 s40, s77, s45
	global_load_lds_dwordx4 v[174:175], off
	s_mov_b32 m0, s40
	s_nop 0
	global_load_lds_dwordx4 v134, s[36:37]
	v_lshl_add_u64 v[174:175], s[36:37], 0, v[138:139]
	s_add_i32 m0, s40, 0x2000
	s_nop 0
	global_load_lds_dwordx4 v138, s[36:37]
	v_lshl_add_u64 v[174:175], v[226:227], 0, s[18:19]
	s_mov_b32 m0, s64
	s_nop 0
	global_load_lds_dwordx4 v[174:175], off
	v_lshl_add_u64 v[174:175], v[228:229], 0, s[18:19]
	s_mov_b32 m0, s65
	s_nop 0
	global_load_lds_dwordx4 v[174:175], off
	s_waitcnt vmcnt(8) lgkmcnt(0)
	s_barrier
	s_setprio 1
	v_mfma_f32_16x16x32_bf16 v[60:63], v[128:131], v[192:195], v[60:63]
	v_mfma_f32_16x16x32_bf16 v[56:59], v[154:157], v[192:195], v[56:59]
	v_mfma_f32_16x16x32_bf16 v[44:47], v[128:131], v[200:203], v[44:47]
	v_mfma_f32_16x16x32_bf16 v[40:43], v[154:157], v[200:203], v[40:43]
	v_mfma_f32_16x16x32_bf16 v[28:31], v[128:131], v[208:211], v[28:31]
	v_mfma_f32_16x16x32_bf16 v[24:27], v[154:157], v[208:211], v[24:27]
	v_mfma_f32_16x16x32_bf16 v[12:15], v[128:131], v[216:219], v[12:15]
	v_mfma_f32_16x16x32_bf16 v[8:11], v[154:157], v[216:219], v[8:11]
	v_mfma_f32_16x16x32_bf16 v[60:63], v[150:153], v[196:199], v[60:63]
	v_mfma_f32_16x16x32_bf16 v[56:59], v[158:161], v[196:199], v[56:59]
	v_mfma_f32_16x16x32_bf16 v[44:47], v[150:153], v[204:207], v[44:47]
	v_mfma_f32_16x16x32_bf16 v[40:43], v[158:161], v[204:207], v[40:43]
	v_mfma_f32_16x16x32_bf16 v[28:31], v[150:153], v[212:215], v[28:31]
	v_mfma_f32_16x16x32_bf16 v[24:27], v[158:161], v[212:215], v[24:27]
	v_mfma_f32_16x16x32_bf16 v[12:15], v[150:153], v[220:223], v[12:15]
	v_mfma_f32_16x16x32_bf16 v[8:11], v[158:161], v[220:223], v[8:11]
	v_mfma_f32_16x16x32_bf16 v[52:55], v[162:165], v[192:195], v[52:55]
	v_mfma_f32_16x16x32_bf16 v[48:51], v[170:173], v[192:195], v[48:51]
	v_mfma_f32_16x16x32_bf16 v[36:39], v[162:165], v[200:203], v[36:39]
	v_mfma_f32_16x16x32_bf16 v[32:35], v[170:173], v[200:203], v[32:35]
	v_mfma_f32_16x16x32_bf16 v[20:23], v[162:165], v[208:211], v[20:23]
	v_mfma_f32_16x16x32_bf16 v[16:19], v[170:173], v[208:211], v[16:19]
	v_mfma_f32_16x16x32_bf16 v[4:7], v[162:165], v[216:219], v[4:7]
	v_mfma_f32_16x16x32_bf16 v[0:3], v[170:173], v[216:219], v[0:3]
	v_mfma_f32_16x16x32_bf16 v[52:55], v[166:169], v[196:199], v[52:55]
	v_mfma_f32_16x16x32_bf16 v[48:51], v[188:191], v[196:199], v[48:51]
	v_mfma_f32_16x16x32_bf16 v[36:39], v[166:169], v[204:207], v[36:39]
	v_mfma_f32_16x16x32_bf16 v[32:35], v[188:191], v[204:207], v[32:35]
	v_mfma_f32_16x16x32_bf16 v[20:23], v[166:169], v[212:215], v[20:23]
	v_mfma_f32_16x16x32_bf16 v[16:19], v[188:191], v[212:215], v[16:19]
	v_mfma_f32_16x16x32_bf16 v[4:7], v[166:169], v[220:223], v[4:7]
	v_mfma_f32_16x16x32_bf16 v[0:3], v[188:191], v[220:223], v[0:3]
	s_setprio 0
	s_barrier
	s_add_i32 s75, s75, 2
	s_add_u32 s8, s8, 0x100
	s_addc_u32 s9, s9, 0
	s_add_u32 s73, s73, 0x100
	s_addc_u32 s74, s74, 0
	s_cmp_gt_u32 s75, 13
	s_cbranch_scc0 .LBB0_349
	s_and_b64 vcc, exec, s[20:21]
	s_cbranch_vccz .LBB0_352
	s_barrier

; #define PG8_STAGE(bufoff, gbase, voff) do { _Pragma("unroll") for (int _i = 0; _i < 2; ++_i) \
;         __builtin_amdgcn_global_load_lds((const unsigned*)((const char*)(gbase) + (voff)[_i]), (PG8_LAS unsigned*)(lds + (bufoff) + ldsw + _i * 8192), 16, 0, 0); } while (0)
; #define PG8_LDA(dst, b, h) do { _Pragma("unroll") for (int m = 0; m < 4; ++m) _Pragma("unroll") for (int k = 0; k < 2; ++k) dst[m][k] = *(const PG8_LAS bf16x8*)(lds + PG8_SA(b, h) + aoff + m * 2048 + k * 1024); } while (0)
; #define PG8_LDB(dst, b, h) do { _Pragma("unroll") for (int n = 0; n < 2; ++n) _Pragma("unroll") for (int k = 0; k < 2; ++k) dst[n][k] = *(const PG8_LAS bf16x8*)(lds + PG8_SB(b, h) + boff + n * 2048 + k * 1024); } while (0)
; #define PG8_MMA(ai, bj, At, Bt) do { __builtin_amdgcn_s_setprio(1); _Pragma("unroll") for (int m = 0; m < 4; ++m) _Pragma("unroll") for (int n = 0; n < 2; ++n) _Pragma("unroll") for (int k = 0; k < 2; ++k) \
;         acc[ai][bj][m][n] = __builtin_amdgcn_mfma_f32_16x16x32_bf16(Bt[n][k], At[m][k], acc[ai][bj][m][n], 0, 0, 0); __builtin_amdgcn_s_setprio(0); } while (0)
; #define PG8_WAIT_V(n) asm volatile("s_waitcnt vmcnt(" #n ")" ::: "memory")
; #define PG8_WAIT_L(n) asm volatile("s_waitcnt lgkmcnt(" #n ")" ::: "memory")
; #define PG8_BAR __builtin_amdgcn_s_barrier()
; #define PG8_SCHED __builtin_amdgcn_sched_barrier(0)
; template <class Epi, class Sched, bool ALIGN_EPI = false, bool SP2 = false>
; __device__ __forceinline__ void gemm_phase(PG8_LAS unsigned char* lds, const Gemm g, const Sched& S, const Epi& E, const int wid) {
;     ...
;             if constexpr (SP2) {
;             PG8_LDB(B0, 0, 0); PG8_LDB(B1, 0, 1); PG8_SCHED; PG8_LDA(At, 0, 0); PG8_STAGE(PG8_SA(1, 1), a1 + hstepA, voffA);
;             PG8_WAIT_V(8); PG8_WAIT_L(0); PG8_BAR; PG8_MMA(0, 0, At, B0); PG8_MMA(0, 1, At, B1); PG8_BAR; PG8_SCHED;
;             PG8_LDA(At, 0, 1); PG8_STAGE(PG8_SB(0, 0), b2, voffB); PG8_STAGE(PG8_SB(0, 1), b2 + hstepB, voffB); PG8_STAGE(PG8_SA(0, 0), a2, voffA);
;             PG8_WAIT_V(8); PG8_WAIT_L(0); PG8_BAR; PG8_MMA(1, 0, At, B0); PG8_MMA(1, 1, At, B1); PG8_BAR; PG8_SCHED;
.LBB0_1780:
	ds_read_b128 v[128:131], v190
	ds_read_b128 v[132:135], v190 offset:1024
	ds_read_b128 v[136:139], v190 offset:2048
	ds_read_b128 v[140:143], v190 offset:3072
	ds_read_b128 v[144:147], v191
	ds_read_b128 v[148:151], v191 offset:1024
	ds_read_b128 v[172:175], v191 offset:2048
	ds_read_b128 v[176:179], v191 offset:3072
	s_add_u32 s34, s30, 0xfffc0080
	s_addc_u32 s35, s31, -1
	s_cmp_eq_u32 s70, 12
	s_cselect_b32 s37, s21, s35
	s_cselect_b32 s36, s27, s34
	s_cselect_b32 s35, s19, s69
	s_cselect_b32 s34, s29, s68
	s_add_i32 m0, s40, 0xc000
	ds_read_b128 v[180:183], v192
	ds_read_b128 v[184:187], v192 offset:1024
	ds_read_b128 v[194:197], v192 offset:2048
	ds_read_b128 v[198:201], v192 offset:3072
	ds_read_b128 v[202:205], v192 offset:4096
	ds_read_b128 v[206:209], v192 offset:5120
	ds_read_b128 v[210:213], v192 offset:6144
	ds_read_b128 v[214:217], v192 offset:7168
	global_load_lds_dwordx4 v164, s[30:31]
	s_add_i32 m0, s40, 0xe000
	s_nop 0
	global_load_lds_dwordx4 v166, s[30:31]
	s_waitcnt vmcnt(8) lgkmcnt(0)
	s_barrier
	s_setprio 1
	v_mfma_f32_16x16x32_bf16 v[124:127], v[128:131], v[180:183], v[124:127]
	v_mfma_f32_16x16x32_bf16 v[120:123], v[136:139], v[180:183], v[120:123]
	v_mfma_f32_16x16x32_bf16 v[108:111], v[128:131], v[194:197], v[108:111]
	v_mfma_f32_16x16x32_bf16 v[104:107], v[136:139], v[194:197], v[104:107]
	v_mfma_f32_16x16x32_bf16 v[92:95], v[128:131], v[202:205], v[92:95]
	v_mfma_f32_16x16x32_bf16 v[88:91], v[136:139], v[202:205], v[88:91]
	v_mfma_f32_16x16x32_bf16 v[76:79], v[128:131], v[210:213], v[76:79]
	v_mfma_f32_16x16x32_bf16 v[72:75], v[136:139], v[210:213], v[72:75]
	v_mfma_f32_16x16x32_bf16 v[124:127], v[132:135], v[184:187], v[124:127]
	v_mfma_f32_16x16x32_bf16 v[120:123], v[140:143], v[184:187], v[120:123]
	v_mfma_f32_16x16x32_bf16 v[108:111], v[132:135], v[198:201], v[108:111]
	v_mfma_f32_16x16x32_bf16 v[104:107], v[140:143], v[198:201], v[104:107]
	v_mfma_f32_16x16x32_bf16 v[92:95], v[132:135], v[206:209], v[92:95]
	v_mfma_f32_16x16x32_bf16 v[88:91], v[140:143], v[206:209], v[88:91]
	v_mfma_f32_16x16x32_bf16 v[76:79], v[132:135], v[214:217], v[76:79]
	v_mfma_f32_16x16x32_bf16 v[72:75], v[140:143], v[214:217], v[72:75]
	v_mfma_f32_16x16x32_bf16 v[116:119], v[144:147], v[180:183], v[116:119]
	v_mfma_f32_16x16x32_bf16 v[112:115], v[172:175], v[180:183], v[112:115]
	v_mfma_f32_16x16x32_bf16 v[100:103], v[144:147], v[194:197], v[100:103]
	v_mfma_f32_16x16x32_bf16 v[96:99], v[172:175], v[194:197], v[96:99]
	v_mfma_f32_16x16x32_bf16 v[84:87], v[144:147], v[202:205], v[84:87]
	v_mfma_f32_16x16x32_bf16 v[80:83], v[172:175], v[202:205], v[80:83]
	v_mfma_f32_16x16x32_bf16 v[68:71], v[144:147], v[210:213], v[68:71]
	v_mfma_f32_16x16x32_bf16 v[64:67], v[172:175], v[210:213], v[64:67]
	v_mfma_f32_16x16x32_bf16 v[116:119], v[148:151], v[184:187], v[116:119]
	v_mfma_f32_16x16x32_bf16 v[112:115], v[176:179], v[184:187], v[112:115]
	v_mfma_f32_16x16x32_bf16 v[100:103], v[148:151], v[198:201], v[100:103]
	v_mfma_f32_16x16x32_bf16 v[96:99], v[176:179], v[198:201], v[96:99]
	v_mfma_f32_16x16x32_bf16 v[84:87], v[148:151], v[206:209], v[84:87]
	v_mfma_f32_16x16x32_bf16 v[80:83], v[176:179], v[206:209], v[80:83]
	v_mfma_f32_16x16x32_bf16 v[68:71], v[148:151], v[214:217], v[68:71]
	v_mfma_f32_16x16x32_bf16 v[64:67], v[176:179], v[214:217], v[64:67]
	s_setprio 0
	s_barrier
	s_add_i32 s71, s65, s39
	v_lshl_add_u64 v[218:219], s[34:35], 0, v[154:155]
	s_mov_b32 m0, s71
	ds_read_b128 v[180:183], v192 offset:16384
	ds_read_b128 v[184:187], v192 offset:17408
	ds_read_b128 v[194:197], v192 offset:18432
	ds_read_b128 v[198:201], v192 offset:19456
	ds_read_b128 v[202:205], v192 offset:20480
	ds_read_b128 v[206:209], v192 offset:21504
	ds_read_b128 v[210:213], v192 offset:22528
	ds_read_b128 v[214:217], v192 offset:23552
	global_load_lds_dwordx4 v154, s[34:35]
	s_add_i32 m0, s71, 0x2000
	s_add_u32 s72, s34, 0x40000
	v_lshl_add_u64 v[220:221], s[34:35], 0, v[158:159]
	s_addc_u32 s73, s35, 0
	s_add_i32 s71, s66, s39
	global_load_lds_dwordx4 v158, s[34:35]
	s_mov_b32 m0, s71
	v_lshl_add_u64 v[224:225], s[36:37], 0, v[156:157]
	global_load_lds_dwordx4 v154, s[72:73]
	s_add_i32 m0, s71, 0x2000
	s_nop 0
	global_load_lds_dwordx4 v158, s[72:73]
	v_lshl_add_u64 v[222:223], s[36:37], 0, v[152:153]
	s_mov_b32 m0, s40
	s_nop 0
	global_load_lds_dwordx4 v152, s[36:37]
	s_mov_b32 m0, s41
	s_nop 0
	global_load_lds_dwordx4 v156, s[36:37]
	s_waitcnt vmcnt(8) lgkmcnt(0)
	s_barrier
	s_setprio 1
	v_mfma_f32_16x16x32_bf16 v[60:63], v[128:131], v[180:183], v[60:63]
	v_mfma_f32_16x16x32_bf16 v[56:59], v[136:139], v[180:183], v[56:59]
	v_mfma_f32_16x16x32_bf16 v[44:47], v[128:131], v[194:197], v[44:47]
	v_mfma_f32_16x16x32_bf16 v[40:43], v[136:139], v[194:197], v[40:43]
	v_mfma_f32_16x16x32_bf16 v[28:31], v[128:131], v[202:205], v[28:31]
	v_mfma_f32_16x16x32_bf16 v[24:27], v[136:139], v[202:205], v[24:27]
	v_mfma_f32_16x16x32_bf16 v[12:15], v[128:131], v[210:213], v[12:15]
	v_mfma_f32_16x16x32_bf16 v[8:11], v[136:139], v[210:213], v[8:11]
	v_mfma_f32_16x16x32_bf16 v[60:63], v[132:135], v[184:187], v[60:63]
	v_mfma_f32_16x16x32_bf16 v[56:59], v[140:143], v[184:187], v[56:59]
	v_mfma_f32_16x16x32_bf16 v[44:47], v[132:135], v[198:201], v[44:47]
	v_mfma_f32_16x16x32_bf16 v[40:43], v[140:143], v[198:201], v[40:43]
	v_mfma_f32_16x16x32_bf16 v[28:31], v[132:135], v[206:209], v[28:31]
	v_mfma_f32_16x16x32_bf16 v[24:27], v[140:143], v[206:209], v[24:27]
	v_mfma_f32_16x16x32_bf16 v[12:15], v[132:135], v[214:217], v[12:15]
	v_mfma_f32_16x16x32_bf16 v[8:11], v[140:143], v[214:217], v[8:11]
	v_mfma_f32_16x16x32_bf16 v[52:55], v[144:147], v[180:183], v[52:55]
	v_mfma_f32_16x16x32_bf16 v[48:51], v[172:175], v[180:183], v[48:51]
	v_mfma_f32_16x16x32_bf16 v[36:39], v[144:147], v[194:197], v[36:39]
	v_mfma_f32_16x16x32_bf16 v[32:35], v[172:175], v[194:197], v[32:35]
	v_mfma_f32_16x16x32_bf16 v[20:23], v[144:147], v[202:205], v[20:23]
	v_mfma_f32_16x16x32_bf16 v[16:19], v[172:175], v[202:205], v[16:19]
	v_mfma_f32_16x16x32_bf16 v[4:7], v[144:147], v[210:213], v[4:7]
	v_mfma_f32_16x16x32_bf16 v[0:3], v[172:175], v[210:213], v[0:3]
	v_mfma_f32_16x16x32_bf16 v[52:55], v[148:151], v[184:187], v[52:55]
	v_mfma_f32_16x16x32_bf16 v[48:51], v[176:179], v[184:187], v[48:51]
	v_mfma_f32_16x16x32_bf16 v[36:39], v[148:151], v[198:201], v[36:39]
	v_mfma_f32_16x16x32_bf16 v[32:35], v[176:179], v[198:201], v[32:35]
	v_mfma_f32_16x16x32_bf16 v[20:23], v[148:151], v[206:209], v[20:23]
	v_mfma_f32_16x16x32_bf16 v[16:19], v[176:179], v[206:209], v[16:19]
	v_mfma_f32_16x16x32_bf16 v[4:7], v[148:151], v[214:217], v[4:7]
	v_mfma_f32_16x16x32_bf16 v[0:3], v[176:179], v[214:217], v[0:3]
	s_setprio 0
	s_barrier
; #define PG8_STAGE(bufoff, gbase, voff) do { _Pragma("unroll") for (int _i = 0; _i < 2; ++_i) \
;         __builtin_amdgcn_global_load_lds((const unsigned*)((const char*)(gbase) + (voff)[_i]), (PG8_LAS unsigned*)(lds + (bufoff) + ldsw + _i * 8192), 16, 0, 0); } while (0)
; #define PG8_LDA(dst, b, h) do { _Pragma("unroll") for (int m = 0; m < 4; ++m) _Pragma("unroll") for (int k = 0; k < 2; ++k) dst[m][k] = *(const PG8_LAS bf16x8*)(lds + PG8_SA(b, h) + aoff + m * 2048 + k * 1024); } while (0)
; #define PG8_LDB(dst, b, h) do { _Pragma("unroll") for (int n = 0; n < 2; ++n) _Pragma("unroll") for (int k = 0; k < 2; ++k) dst[n][k] = *(const PG8_LAS bf16x8*)(lds + PG8_SB(b, h) + boff + n * 2048 + k * 1024); } while (0)
; #define PG8_MMA(ai, bj, At, Bt) do { __builtin_amdgcn_s_setprio(1); _Pragma("unroll") for (int m = 0; m < 4; ++m) _Pragma("unroll") for (int n = 0; n < 2; ++n) _Pragma("unroll") for (int k = 0; k < 2; ++k) \
;         acc[ai][bj][m][n] = __builtin_amdgcn_mfma_f32_16x16x32_bf16(Bt[n][k], At[m][k], acc[ai][bj][m][n], 0, 0, 0); __builtin_amdgcn_s_setprio(0); } while (0)
; #define PG8_WAIT_V(n) asm volatile("s_waitcnt vmcnt(" #n ")" ::: "memory")
; #define PG8_WAIT_L(n) asm volatile("s_waitcnt lgkmcnt(" #n ")" ::: "memory")
; #define PG8_BAR __builtin_amdgcn_s_barrier()
; #define PG8_SCHED __builtin_amdgcn_sched_barrier(0)
; template <class Epi, class Sched, bool ALIGN_EPI = false, bool SP2 = false>
; __device__ __forceinline__ void gemm_phase(PG8_LAS unsigned char* lds, const Gemm g, const Sched& S, const Epi& E, const int wid) {
;     ...
;             PG8_LDB(B0, 1, 0); PG8_LDB(B1, 1, 1); PG8_SCHED; PG8_LDA(At, 1, 0); PG8_STAGE(PG8_SA(0, 1), a2 + hstepA, voffA);
;             PG8_WAIT_V(8); PG8_WAIT_L(0); PG8_BAR; PG8_MMA(0, 0, At, B0); PG8_MMA(0, 1, At, B1); PG8_BAR; PG8_SCHED;
;             PG8_LDA(At, 1, 1); PG8_STAGE(PG8_SB(1, 0), b3, voffB); PG8_STAGE(PG8_SB(1, 1), b3 + hstepB, voffB); PG8_STAGE(PG8_SA(1, 0), a3, voffA);
;             PG8_WAIT_V(8); PG8_WAIT_L(0); PG8_BAR; PG8_MMA(1, 0, At, B0); PG8_MMA(1, 1, At, B1); PG8_BAR; PG8_SCHED;
;     ...
;         if constexpr (ALIGN_EPI) { if (wr == 0) PG8_BAR; }
	s_add_i32 s71, 0, 0x18000
	s_add_i32 s72, 0, 0x1c000
	v_add_u32_e32 v140, s71, v189
	v_add_u32_e32 v176, s72, v189
	ds_read_b128 v[128:131], v140
	ds_read_b128 v[132:135], v140 offset:1024
	ds_read_b128 v[136:139], v140 offset:2048
	ds_read_b128 v[140:143], v140 offset:3072
	ds_read_b128 v[144:147], v176
	ds_read_b128 v[148:151], v176 offset:1024
	ds_read_b128 v[172:175], v176 offset:2048
	ds_read_b128 v[176:179], v176 offset:3072
	s_add_u32 s36, s36, 0x40000
	s_addc_u32 s37, s37, 0
	s_mov_b32 m0, s44
	ds_read_b128 v[180:183], v192 offset:32768
	ds_read_b128 v[184:187], v192 offset:33792
	ds_read_b128 v[194:197], v192 offset:34816
	ds_read_b128 v[198:201], v192 offset:35840
	ds_read_b128 v[202:205], v192 offset:36864
	ds_read_b128 v[206:209], v192 offset:37888
	ds_read_b128 v[210:213], v192 offset:38912
	ds_read_b128 v[214:217], v192 offset:39936
	global_load_lds_dwordx4 v152, s[36:37]
	s_mov_b32 m0, s45
	s_nop 0
	global_load_lds_dwordx4 v156, s[36:37]
	s_waitcnt vmcnt(8) lgkmcnt(0)
	s_barrier
	s_setprio 1
	v_mfma_f32_16x16x32_bf16 v[124:127], v[128:131], v[180:183], v[124:127]
	v_mfma_f32_16x16x32_bf16 v[120:123], v[136:139], v[180:183], v[120:123]
	v_mfma_f32_16x16x32_bf16 v[108:111], v[128:131], v[194:197], v[108:111]
	v_mfma_f32_16x16x32_bf16 v[104:107], v[136:139], v[194:197], v[104:107]
	v_mfma_f32_16x16x32_bf16 v[92:95], v[128:131], v[202:205], v[92:95]
	v_mfma_f32_16x16x32_bf16 v[88:91], v[136:139], v[202:205], v[88:91]
	v_mfma_f32_16x16x32_bf16 v[76:79], v[128:131], v[210:213], v[76:79]
	v_mfma_f32_16x16x32_bf16 v[72:75], v[136:139], v[210:213], v[72:75]
	v_mfma_f32_16x16x32_bf16 v[124:127], v[132:135], v[184:187], v[124:127]
	v_mfma_f32_16x16x32_bf16 v[120:123], v[140:143], v[184:187], v[120:123]
	v_mfma_f32_16x16x32_bf16 v[108:111], v[132:135], v[198:201], v[108:111]
	v_mfma_f32_16x16x32_bf16 v[104:107], v[140:143], v[198:201], v[104:107]
	v_mfma_f32_16x16x32_bf16 v[92:95], v[132:135], v[206:209], v[92:95]
	v_mfma_f32_16x16x32_bf16 v[88:91], v[140:143], v[206:209], v[88:91]
	v_mfma_f32_16x16x32_bf16 v[76:79], v[132:135], v[214:217], v[76:79]
	v_mfma_f32_16x16x32_bf16 v[72:75], v[140:143], v[214:217], v[72:75]
	v_mfma_f32_16x16x32_bf16 v[116:119], v[144:147], v[180:183], v[116:119]
	v_mfma_f32_16x16x32_bf16 v[112:115], v[172:175], v[180:183], v[112:115]
	v_mfma_f32_16x16x32_bf16 v[100:103], v[144:147], v[194:197], v[100:103]
	v_mfma_f32_16x16x32_bf16 v[96:99], v[172:175], v[194:197], v[96:99]
	v_mfma_f32_16x16x32_bf16 v[84:87], v[144:147], v[202:205], v[84:87]
	v_mfma_f32_16x16x32_bf16 v[80:83], v[172:175], v[202:205], v[80:83]
	v_mfma_f32_16x16x32_bf16 v[68:71], v[144:147], v[210:213], v[68:71]
	v_mfma_f32_16x16x32_bf16 v[64:67], v[172:175], v[210:213], v[64:67]
	v_mfma_f32_16x16x32_bf16 v[116:119], v[148:151], v[184:187], v[116:119]
	v_mfma_f32_16x16x32_bf16 v[112:115], v[176:179], v[184:187], v[112:115]
	v_mfma_f32_16x16x32_bf16 v[100:103], v[148:151], v[198:201], v[100:103]
	v_mfma_f32_16x16x32_bf16 v[96:99], v[176:179], v[198:201], v[96:99]
	v_mfma_f32_16x16x32_bf16 v[84:87], v[148:151], v[206:209], v[84:87]
	v_mfma_f32_16x16x32_bf16 v[80:83], v[176:179], v[206:209], v[80:83]
	v_mfma_f32_16x16x32_bf16 v[68:71], v[148:151], v[214:217], v[68:71]
	v_mfma_f32_16x16x32_bf16 v[64:67], v[176:179], v[214:217], v[64:67]
	s_setprio 0
	s_barrier
	s_add_i32 s36, s71, s39
	v_lshl_add_u64 v[218:219], v[218:219], 0, s[14:15]
	s_mov_b32 m0, s36
	ds_read_b128 v[180:183], v192 offset:49152
	ds_read_b128 v[184:187], v192 offset:50176
	ds_read_b128 v[194:197], v192 offset:51200
	ds_read_b128 v[198:201], v192 offset:52224
	ds_read_b128 v[202:205], v192 offset:53248
	ds_read_b128 v[206:209], v192 offset:54272
	ds_read_b128 v[210:213], v192 offset:55296
	ds_read_b128 v[214:217], v192 offset:56320
	global_load_lds_dwordx4 v[218:219], off
	s_add_i32 m0, s36, 0x2000
	s_add_u32 s34, s34, 0x40080
	v_lshl_add_u64 v[218:219], v[220:221], 0, s[14:15]
	s_addc_u32 s35, s35, 0
	s_add_i32 s36, s72, s39
	global_load_lds_dwordx4 v[218:219], off
	s_mov_b32 m0, s36
	s_nop 0
	global_load_lds_dwordx4 v154, s[34:35]
	v_lshl_add_u64 v[218:219], s[34:35], 0, v[158:159]
	s_add_i32 m0, s36, 0x2000
	s_nop 0
	global_load_lds_dwordx4 v158, s[34:35]
	v_lshl_add_u64 v[218:219], v[222:223], 0, s[14:15]
	s_mov_b32 m0, s47
	s_nop 0
	global_load_lds_dwordx4 v[218:219], off
	v_lshl_add_u64 v[218:219], v[224:225], 0, s[14:15]
	s_mov_b32 m0, s48
	s_nop 0
	global_load_lds_dwordx4 v[218:219], off
	s_waitcnt vmcnt(8) lgkmcnt(0)
	s_barrier
	s_setprio 1
	v_mfma_f32_16x16x32_bf16 v[60:63], v[128:131], v[180:183], v[60:63]
	v_mfma_f32_16x16x32_bf16 v[56:59], v[136:139], v[180:183], v[56:59]
	v_mfma_f32_16x16x32_bf16 v[44:47], v[128:131], v[194:197], v[44:47]
	v_mfma_f32_16x16x32_bf16 v[40:43], v[136:139], v[194:197], v[40:43]
	v_mfma_f32_16x16x32_bf16 v[28:31], v[128:131], v[202:205], v[28:31]
	v_mfma_f32_16x16x32_bf16 v[24:27], v[136:139], v[202:205], v[24:27]
	v_mfma_f32_16x16x32_bf16 v[12:15], v[128:131], v[210:213], v[12:15]
	v_mfma_f32_16x16x32_bf16 v[8:11], v[136:139], v[210:213], v[8:11]
	v_mfma_f32_16x16x32_bf16 v[60:63], v[132:135], v[184:187], v[60:63]
	v_mfma_f32_16x16x32_bf16 v[56:59], v[140:143], v[184:187], v[56:59]
	v_mfma_f32_16x16x32_bf16 v[44:47], v[132:135], v[198:201], v[44:47]
	v_mfma_f32_16x16x32_bf16 v[40:43], v[140:143], v[198:201], v[40:43]
	v_mfma_f32_16x16x32_bf16 v[28:31], v[132:135], v[206:209], v[28:31]
	v_mfma_f32_16x16x32_bf16 v[24:27], v[140:143], v[206:209], v[24:27]
	v_mfma_f32_16x16x32_bf16 v[12:15], v[132:135], v[214:217], v[12:15]
	v_mfma_f32_16x16x32_bf16 v[8:11], v[140:143], v[214:217], v[8:11]
	v_mfma_f32_16x16x32_bf16 v[52:55], v[144:147], v[180:183], v[52:55]
	v_mfma_f32_16x16x32_bf16 v[48:51], v[172:175], v[180:183], v[48:51]
	v_mfma_f32_16x16x32_bf16 v[36:39], v[144:147], v[194:197], v[36:39]
	v_mfma_f32_16x16x32_bf16 v[32:35], v[172:175], v[194:197], v[32:35]
	v_mfma_f32_16x16x32_bf16 v[20:23], v[144:147], v[202:205], v[20:23]
	v_mfma_f32_16x16x32_bf16 v[16:19], v[172:175], v[202:205], v[16:19]
	v_mfma_f32_16x16x32_bf16 v[4:7], v[144:147], v[210:213], v[4:7]
	v_mfma_f32_16x16x32_bf16 v[0:3], v[172:175], v[210:213], v[0:3]
	v_mfma_f32_16x16x32_bf16 v[52:55], v[148:151], v[184:187], v[52:55]
	v_mfma_f32_16x16x32_bf16 v[48:51], v[176:179], v[184:187], v[48:51]
	v_mfma_f32_16x16x32_bf16 v[36:39], v[148:151], v[198:201], v[36:39]
	v_mfma_f32_16x16x32_bf16 v[32:35], v[176:179], v[198:201], v[32:35]
	v_mfma_f32_16x16x32_bf16 v[20:23], v[148:151], v[206:209], v[20:23]
	v_mfma_f32_16x16x32_bf16 v[16:19], v[176:179], v[206:209], v[16:19]
	v_mfma_f32_16x16x32_bf16 v[4:7], v[148:151], v[214:217], v[4:7]
	v_mfma_f32_16x16x32_bf16 v[0:3], v[176:179], v[214:217], v[0:3]
	s_setprio 0
	s_barrier
	s_add_i32 s70, s70, 2
	s_add_u32 s30, s30, 0x100
	s_addc_u32 s31, s31, 0
	s_add_u32 s68, s68, 0x100
	s_addc_u32 s69, s69, 0
	s_cmp_gt_u32 s70, 13
	s_cbranch_scc0 .LBB0_1780
	s_and_b64 vcc, exec, s[16:17]
	s_cbranch_vccz .LBB0_1783
	s_barrier

; #define PG8_STAGE(bufoff, gbase, voff) do { _Pragma("unroll") for (int _i = 0; _i < 2; ++_i) \
;         __builtin_amdgcn_global_load_lds((const unsigned*)((const char*)(gbase) + (voff)[_i]), (PG8_LAS unsigned*)(lds + (bufoff) + ldsw + _i * 8192), 16, 0, 0); } while (0)
; #define PG8_LDA(dst, b, h) do { _Pragma("unroll") for (int m = 0; m < 4; ++m) _Pragma("unroll") for (int k = 0; k < 2; ++k) dst[m][k] = *(const PG8_LAS bf16x8*)(lds + PG8_SA(b, h) + aoff + m * 2048 + k * 1024); } while (0)
; #define PG8_LDB(dst, b, h) do { _Pragma("unroll") for (int n = 0; n < 2; ++n) _Pragma("unroll") for (int k = 0; k < 2; ++k) dst[n][k] = *(const PG8_LAS bf16x8*)(lds + PG8_SB(b, h) + boff + n * 2048 + k * 1024); } while (0)
; #define PG8_MMA(ai, bj, At, Bt) do { __builtin_amdgcn_s_setprio(1); _Pragma("unroll") for (int m = 0; m < 4; ++m) _Pragma("unroll") for (int n = 0; n < 2; ++n) _Pragma("unroll") for (int k = 0; k < 2; ++k) \
;         acc[ai][bj][m][n] = __builtin_amdgcn_mfma_f32_16x16x32_bf16(Bt[n][k], At[m][k], acc[ai][bj][m][n], 0, 0, 0); __builtin_amdgcn_s_setprio(0); } while (0)
; #define PG8_WAIT_V(n) asm volatile("s_waitcnt vmcnt(" #n ")" ::: "memory")
; #define PG8_WAIT_L(n) asm volatile("s_waitcnt lgkmcnt(" #n ")" ::: "memory")
; template <class Epi, class Sched, bool ALIGN_EPI = false, bool SP2 = false>
; __device__ __forceinline__ void gemm_phase(PG8_LAS unsigned char* lds, const Gemm g, const Sched& S, const Epi& E, const int wid) {
;     ...
;             const bool last = (t == nt - 2);
;             const char* a1 = cA + (size_t)(t + 1) * kstep;
;             const char* a2 = last ? nA : cA + (size_t)(t + 2) * kstep; const char* b2 = last ? nB : cB + (size_t)(t + 2) * kstep;
;             const char* a3 = a2 + kstep; const char* b3 = b2 + kstep;
;             if (last && has_next) S.a_ready(nxt);
;             if constexpr (SP2) {
;             PG8_LDB(B0, 0, 0); PG8_LDB(B1, 0, 1); PG8_SCHED; PG8_LDA(At, 0, 0); PG8_STAGE(PG8_SA(1, 1), a1 + hstepA, voffA);
;             PG8_WAIT_V(8); PG8_WAIT_L(0); PG8_BAR; PG8_MMA(0, 0, At, B0); PG8_MMA(0, 1, At, B1); PG8_BAR; PG8_SCHED;
;             PG8_LDA(At, 0, 1); PG8_STAGE(PG8_SB(0, 0), b2, voffB); PG8_STAGE(PG8_SB(0, 1), b2 + hstepB, voffB); PG8_STAGE(PG8_SA(0, 0), a2, voffA);
;             PG8_WAIT_V(8); PG8_WAIT_L(0); PG8_BAR; PG8_MMA(1, 0, At, B0); PG8_MMA(1, 1, At, B1); PG8_BAR; PG8_SCHED;
.LBB0_1867:
	ds_read_b128 v[148:151], v166
	ds_read_b128 v[152:155], v166 offset:1024
	ds_read_b128 v[156:159], v166 offset:2048
	ds_read_b128 v[160:163], v166 offset:3072
	ds_read_b128 v[172:175], v167
	ds_read_b128 v[176:179], v167 offset:1024
	ds_read_b128 v[180:183], v167 offset:2048
	ds_read_b128 v[184:187], v167 offset:3072
	s_add_u32 s26, s24, 0xfffc0080
	s_addc_u32 s27, s25, -1
	s_cmp_eq_u32 s67, 12
	s_cselect_b32 s29, s17, s27
	s_cselect_b32 s28, s49, s26
	s_cselect_b32 s27, s15, s66
	s_cselect_b32 s26, s64, s65
	s_add_i32 m0, s36, 0xc000
	ds_read_b128 v[188:191], v168
	ds_read_b128 v[192:195], v168 offset:1024
	ds_read_b128 v[196:199], v168 offset:2048
	ds_read_b128 v[200:203], v168 offset:3072
	ds_read_b128 v[204:207], v168 offset:4096
	ds_read_b128 v[208:211], v168 offset:5120
	ds_read_b128 v[212:215], v168 offset:6144
	ds_read_b128 v[216:219], v168 offset:7168
	global_load_lds_dwordx4 v140, s[24:25]
	s_add_i32 m0, s36, 0xe000
	s_nop 0
	global_load_lds_dwordx4 v142, s[24:25]
	s_waitcnt vmcnt(8) lgkmcnt(0)
	s_barrier
	s_setprio 1
	v_mfma_f32_16x16x32_bf16 v[124:127], v[148:151], v[188:191], v[124:127]
	v_mfma_f32_16x16x32_bf16 v[116:119], v[156:159], v[188:191], v[116:119]
	v_mfma_f32_16x16x32_bf16 v[108:111], v[148:151], v[196:199], v[108:111]
	v_mfma_f32_16x16x32_bf16 v[100:103], v[156:159], v[196:199], v[100:103]
	v_mfma_f32_16x16x32_bf16 v[92:95], v[148:151], v[204:207], v[92:95]
	v_mfma_f32_16x16x32_bf16 v[84:87], v[156:159], v[204:207], v[84:87]
	v_mfma_f32_16x16x32_bf16 v[76:79], v[148:151], v[212:215], v[76:79]
	v_mfma_f32_16x16x32_bf16 v[68:71], v[156:159], v[212:215], v[68:71]
	v_mfma_f32_16x16x32_bf16 v[124:127], v[152:155], v[192:195], v[124:127]
	v_mfma_f32_16x16x32_bf16 v[116:119], v[160:163], v[192:195], v[116:119]
	v_mfma_f32_16x16x32_bf16 v[108:111], v[152:155], v[200:203], v[108:111]
	v_mfma_f32_16x16x32_bf16 v[100:103], v[160:163], v[200:203], v[100:103]
	v_mfma_f32_16x16x32_bf16 v[92:95], v[152:155], v[208:211], v[92:95]
	v_mfma_f32_16x16x32_bf16 v[84:87], v[160:163], v[208:211], v[84:87]
	v_mfma_f32_16x16x32_bf16 v[76:79], v[152:155], v[216:219], v[76:79]
	v_mfma_f32_16x16x32_bf16 v[68:71], v[160:163], v[216:219], v[68:71]
	v_mfma_f32_16x16x32_bf16 v[120:123], v[172:175], v[188:191], v[120:123]
	v_mfma_f32_16x16x32_bf16 v[112:115], v[180:183], v[188:191], v[112:115]
	v_mfma_f32_16x16x32_bf16 v[104:107], v[172:175], v[196:199], v[104:107]
	v_mfma_f32_16x16x32_bf16 v[96:99], v[180:183], v[196:199], v[96:99]
	v_mfma_f32_16x16x32_bf16 v[88:91], v[172:175], v[204:207], v[88:91]
	v_mfma_f32_16x16x32_bf16 v[80:83], v[180:183], v[204:207], v[80:83]
	v_mfma_f32_16x16x32_bf16 v[72:75], v[172:175], v[212:215], v[72:75]
	v_mfma_f32_16x16x32_bf16 v[64:67], v[180:183], v[212:215], v[64:67]
	v_mfma_f32_16x16x32_bf16 v[120:123], v[176:179], v[192:195], v[120:123]
	v_mfma_f32_16x16x32_bf16 v[112:115], v[184:187], v[192:195], v[112:115]
	v_mfma_f32_16x16x32_bf16 v[104:107], v[176:179], v[200:203], v[104:107]
	v_mfma_f32_16x16x32_bf16 v[96:99], v[184:187], v[200:203], v[96:99]
	v_mfma_f32_16x16x32_bf16 v[88:91], v[176:179], v[208:211], v[88:91]
	v_mfma_f32_16x16x32_bf16 v[80:83], v[184:187], v[208:211], v[80:83]
	v_mfma_f32_16x16x32_bf16 v[72:75], v[176:179], v[216:219], v[72:75]
	v_mfma_f32_16x16x32_bf16 v[64:67], v[184:187], v[216:219], v[64:67]
	s_setprio 0
	s_barrier
	s_add_i32 s68, s45, s33
	v_lshl_add_u64 v[220:221], s[26:27], 0, v[132:133]
	s_mov_b32 m0, s68
	ds_read_b128 v[188:191], v168 offset:16384
	ds_read_b128 v[192:195], v168 offset:17408
	ds_read_b128 v[196:199], v168 offset:18432
	ds_read_b128 v[200:203], v168 offset:19456
	ds_read_b128 v[204:207], v168 offset:20480
	ds_read_b128 v[208:211], v168 offset:21504
	ds_read_b128 v[212:215], v168 offset:22528
	ds_read_b128 v[216:219], v168 offset:23552
	global_load_lds_dwordx4 v132, s[26:27]
	s_add_i32 m0, s68, 0x2000
	s_add_u32 s68, s26, 0x40000
	v_lshl_add_u64 v[222:223], s[26:27], 0, v[128:129]
	s_addc_u32 s69, s27, 0
	s_add_i32 s70, s46, s33
	global_load_lds_dwordx4 v128, s[26:27]
	s_mov_b32 m0, s70
	v_lshl_add_u64 v[226:227], s[28:29], 0, v[130:131]
	global_load_lds_dwordx4 v132, s[68:69]
	s_add_i32 m0, s70, 0x2000
	s_nop 0
	global_load_lds_dwordx4 v128, s[68:69]
	v_lshl_add_u64 v[224:225], s[28:29], 0, v[134:135]
	s_mov_b32 m0, s36
	s_nop 0
	global_load_lds_dwordx4 v134, s[28:29]
	s_mov_b32 m0, s37
	s_nop 0
	global_load_lds_dwordx4 v130, s[28:29]
	s_waitcnt vmcnt(8) lgkmcnt(0)
	s_barrier
	s_setprio 1
	v_mfma_f32_16x16x32_bf16 v[60:63], v[148:151], v[188:191], v[60:63]
	v_mfma_f32_16x16x32_bf16 v[52:55], v[156:159], v[188:191], v[52:55]
	v_mfma_f32_16x16x32_bf16 v[44:47], v[148:151], v[196:199], v[44:47]
	v_mfma_f32_16x16x32_bf16 v[36:39], v[156:159], v[196:199], v[36:39]
	v_mfma_f32_16x16x32_bf16 v[28:31], v[148:151], v[204:207], v[28:31]
	v_mfma_f32_16x16x32_bf16 v[20:23], v[156:159], v[204:207], v[20:23]
	v_mfma_f32_16x16x32_bf16 v[12:15], v[148:151], v[212:215], v[12:15]
	v_mfma_f32_16x16x32_bf16 v[4:7], v[156:159], v[212:215], v[4:7]
	v_mfma_f32_16x16x32_bf16 v[60:63], v[152:155], v[192:195], v[60:63]
	v_mfma_f32_16x16x32_bf16 v[52:55], v[160:163], v[192:195], v[52:55]
	v_mfma_f32_16x16x32_bf16 v[44:47], v[152:155], v[200:203], v[44:47]
	v_mfma_f32_16x16x32_bf16 v[36:39], v[160:163], v[200:203], v[36:39]
	v_mfma_f32_16x16x32_bf16 v[28:31], v[152:155], v[208:211], v[28:31]
	v_mfma_f32_16x16x32_bf16 v[20:23], v[160:163], v[208:211], v[20:23]
	v_mfma_f32_16x16x32_bf16 v[12:15], v[152:155], v[216:219], v[12:15]
	v_mfma_f32_16x16x32_bf16 v[4:7], v[160:163], v[216:219], v[4:7]
	v_mfma_f32_16x16x32_bf16 v[56:59], v[172:175], v[188:191], v[56:59]
	v_mfma_f32_16x16x32_bf16 v[48:51], v[180:183], v[188:191], v[48:51]
	v_mfma_f32_16x16x32_bf16 v[40:43], v[172:175], v[196:199], v[40:43]
	v_mfma_f32_16x16x32_bf16 v[32:35], v[180:183], v[196:199], v[32:35]
	v_mfma_f32_16x16x32_bf16 v[24:27], v[172:175], v[204:207], v[24:27]
	v_mfma_f32_16x16x32_bf16 v[16:19], v[180:183], v[204:207], v[16:19]
	v_mfma_f32_16x16x32_bf16 v[8:11], v[172:175], v[212:215], v[8:11]
	v_mfma_f32_16x16x32_bf16 v[0:3], v[180:183], v[212:215], v[0:3]
	v_mfma_f32_16x16x32_bf16 v[56:59], v[176:179], v[192:195], v[56:59]
	v_mfma_f32_16x16x32_bf16 v[48:51], v[184:187], v[192:195], v[48:51]
	v_mfma_f32_16x16x32_bf16 v[40:43], v[176:179], v[200:203], v[40:43]
	v_mfma_f32_16x16x32_bf16 v[32:35], v[184:187], v[200:203], v[32:35]
	v_mfma_f32_16x16x32_bf16 v[24:27], v[176:179], v[208:211], v[24:27]
	v_mfma_f32_16x16x32_bf16 v[16:19], v[184:187], v[208:211], v[16:19]
	v_mfma_f32_16x16x32_bf16 v[8:11], v[176:179], v[216:219], v[8:11]
	v_mfma_f32_16x16x32_bf16 v[0:3], v[184:187], v[216:219], v[0:3]
	s_setprio 0
	s_barrier
; #define PG8_STAGE(bufoff, gbase, voff) do { _Pragma("unroll") for (int _i = 0; _i < 2; ++_i) \
;         __builtin_amdgcn_global_load_lds((const unsigned*)((const char*)(gbase) + (voff)[_i]), (PG8_LAS unsigned*)(lds + (bufoff) + ldsw + _i * 8192), 16, 0, 0); } while (0)
; #define PG8_LDA(dst, b, h) do { _Pragma("unroll") for (int m = 0; m < 4; ++m) _Pragma("unroll") for (int k = 0; k < 2; ++k) dst[m][k] = *(const PG8_LAS bf16x8*)(lds + PG8_SA(b, h) + aoff + m * 2048 + k * 1024); } while (0)
; #define PG8_LDB(dst, b, h) do { _Pragma("unroll") for (int n = 0; n < 2; ++n) _Pragma("unroll") for (int k = 0; k < 2; ++k) dst[n][k] = *(const PG8_LAS bf16x8*)(lds + PG8_SB(b, h) + boff + n * 2048 + k * 1024); } while (0)
; #define PG8_MMA(ai, bj, At, Bt) do { __builtin_amdgcn_s_setprio(1); _Pragma("unroll") for (int m = 0; m < 4; ++m) _Pragma("unroll") for (int n = 0; n < 2; ++n) _Pragma("unroll") for (int k = 0; k < 2; ++k) \
;         acc[ai][bj][m][n] = __builtin_amdgcn_mfma_f32_16x16x32_bf16(Bt[n][k], At[m][k], acc[ai][bj][m][n], 0, 0, 0); __builtin_amdgcn_s_setprio(0); } while (0)
; #define PG8_WAIT_V(n) asm volatile("s_waitcnt vmcnt(" #n ")" ::: "memory")
; #define PG8_WAIT_L(n) asm volatile("s_waitcnt lgkmcnt(" #n ")" ::: "memory")
; #define PG8_BAR __builtin_amdgcn_s_barrier()
; #define PG8_SCHED __builtin_amdgcn_sched_barrier(0)
; template <class Epi, class Sched, bool ALIGN_EPI = false, bool SP2 = false>
; __device__ __forceinline__ void gemm_phase(PG8_LAS unsigned char* lds, const Gemm g, const Sched& S, const Epi& E, const int wid) {
;     ...
;             PG8_LDB(B0, 1, 0); PG8_LDB(B1, 1, 1); PG8_SCHED; PG8_LDA(At, 1, 0); PG8_STAGE(PG8_SA(0, 1), a2 + hstepA, voffA);
;             PG8_WAIT_V(8); PG8_WAIT_L(0); PG8_BAR; PG8_MMA(0, 0, At, B0); PG8_MMA(0, 1, At, B1); PG8_BAR; PG8_SCHED;
;             PG8_LDA(At, 1, 1); PG8_STAGE(PG8_SB(1, 0), b3, voffB); PG8_STAGE(PG8_SB(1, 1), b3 + hstepB, voffB); PG8_STAGE(PG8_SA(1, 0), a3, voffA);
;             PG8_WAIT_V(8); PG8_WAIT_L(0); PG8_BAR; PG8_MMA(1, 0, At, B0); PG8_MMA(1, 1, At, B1); PG8_BAR; PG8_SCHED;
;     ...
;         if constexpr (ALIGN_EPI) { if (wr == 0) PG8_BAR; }
	s_add_i32 s68, 0, 0x18000
	s_add_i32 s69, 0, 0x1c000
	v_add_u32_e32 v160, s68, v165
	v_add_u32_e32 v171, s69, v165
	ds_read_b128 v[148:151], v160
	ds_read_b128 v[152:155], v160 offset:1024
	ds_read_b128 v[156:159], v160 offset:2048
	ds_read_b128 v[160:163], v160 offset:3072
	ds_read_b128 v[172:175], v171
	ds_read_b128 v[176:179], v171 offset:1024
	ds_read_b128 v[180:183], v171 offset:2048
	ds_read_b128 v[184:187], v171 offset:3072
	s_add_u32 s28, s28, 0x40000
	s_addc_u32 s29, s29, 0
	s_mov_b32 m0, s38
	ds_read_b128 v[188:191], v168 offset:32768
	ds_read_b128 v[192:195], v168 offset:33792
	ds_read_b128 v[196:199], v168 offset:34816
	ds_read_b128 v[200:203], v168 offset:35840
	ds_read_b128 v[204:207], v168 offset:36864
	ds_read_b128 v[208:211], v168 offset:37888
	ds_read_b128 v[212:215], v168 offset:38912
	ds_read_b128 v[216:219], v168 offset:39936
	global_load_lds_dwordx4 v134, s[28:29]
	s_mov_b32 m0, s39
	s_nop 0
	global_load_lds_dwordx4 v130, s[28:29]
	s_waitcnt vmcnt(8) lgkmcnt(0)
	s_barrier
	s_setprio 1
	v_mfma_f32_16x16x32_bf16 v[124:127], v[148:151], v[188:191], v[124:127]
	v_mfma_f32_16x16x32_bf16 v[116:119], v[156:159], v[188:191], v[116:119]
	v_mfma_f32_16x16x32_bf16 v[108:111], v[148:151], v[196:199], v[108:111]
	v_mfma_f32_16x16x32_bf16 v[100:103], v[156:159], v[196:199], v[100:103]
	v_mfma_f32_16x16x32_bf16 v[92:95], v[148:151], v[204:207], v[92:95]
	v_mfma_f32_16x16x32_bf16 v[84:87], v[156:159], v[204:207], v[84:87]
	v_mfma_f32_16x16x32_bf16 v[76:79], v[148:151], v[212:215], v[76:79]
	v_mfma_f32_16x16x32_bf16 v[68:71], v[156:159], v[212:215], v[68:71]
	v_mfma_f32_16x16x32_bf16 v[124:127], v[152:155], v[192:195], v[124:127]
	v_mfma_f32_16x16x32_bf16 v[116:119], v[160:163], v[192:195], v[116:119]
	v_mfma_f32_16x16x32_bf16 v[108:111], v[152:155], v[200:203], v[108:111]
	v_mfma_f32_16x16x32_bf16 v[100:103], v[160:163], v[200:203], v[100:103]
	v_mfma_f32_16x16x32_bf16 v[92:95], v[152:155], v[208:211], v[92:95]
	v_mfma_f32_16x16x32_bf16 v[84:87], v[160:163], v[208:211], v[84:87]
	v_mfma_f32_16x16x32_bf16 v[76:79], v[152:155], v[216:219], v[76:79]
	v_mfma_f32_16x16x32_bf16 v[68:71], v[160:163], v[216:219], v[68:71]
	v_mfma_f32_16x16x32_bf16 v[120:123], v[172:175], v[188:191], v[120:123]
	v_mfma_f32_16x16x32_bf16 v[112:115], v[180:183], v[188:191], v[112:115]
	v_mfma_f32_16x16x32_bf16 v[104:107], v[172:175], v[196:199], v[104:107]
	v_mfma_f32_16x16x32_bf16 v[96:99], v[180:183], v[196:199], v[96:99]
	v_mfma_f32_16x16x32_bf16 v[88:91], v[172:175], v[204:207], v[88:91]
	v_mfma_f32_16x16x32_bf16 v[80:83], v[180:183], v[204:207], v[80:83]
	v_mfma_f32_16x16x32_bf16 v[72:75], v[172:175], v[212:215], v[72:75]
	v_mfma_f32_16x16x32_bf16 v[64:67], v[180:183], v[212:215], v[64:67]
	v_mfma_f32_16x16x32_bf16 v[120:123], v[176:179], v[192:195], v[120:123]
	v_mfma_f32_16x16x32_bf16 v[112:115], v[184:187], v[192:195], v[112:115]
	v_mfma_f32_16x16x32_bf16 v[104:107], v[176:179], v[200:203], v[104:107]
	v_mfma_f32_16x16x32_bf16 v[96:99], v[184:187], v[200:203], v[96:99]
	v_mfma_f32_16x16x32_bf16 v[88:91], v[176:179], v[208:211], v[88:91]
	v_mfma_f32_16x16x32_bf16 v[80:83], v[184:187], v[208:211], v[80:83]
	v_mfma_f32_16x16x32_bf16 v[72:75], v[176:179], v[216:219], v[72:75]
	v_mfma_f32_16x16x32_bf16 v[64:67], v[184:187], v[216:219], v[64:67]
	s_setprio 0
	s_barrier
	s_add_i32 s28, s68, s33
	v_lshl_add_u64 v[220:221], v[220:221], 0, s[10:11]
	s_mov_b32 m0, s28
	ds_read_b128 v[188:191], v168 offset:49152
	ds_read_b128 v[192:195], v168 offset:50176
	ds_read_b128 v[196:199], v168 offset:51200
	ds_read_b128 v[200:203], v168 offset:52224
	ds_read_b128 v[204:207], v168 offset:53248
	ds_read_b128 v[208:211], v168 offset:54272
	ds_read_b128 v[212:215], v168 offset:55296
	ds_read_b128 v[216:219], v168 offset:56320
	global_load_lds_dwordx4 v[220:221], off
	s_add_i32 m0, s28, 0x2000
	s_add_u32 s26, s26, 0x40080
	v_lshl_add_u64 v[220:221], v[222:223], 0, s[10:11]
	s_addc_u32 s27, s27, 0
	s_add_i32 s28, s69, s33
	global_load_lds_dwordx4 v[220:221], off
	s_mov_b32 m0, s28
	s_nop 0
	global_load_lds_dwordx4 v132, s[26:27]
	v_lshl_add_u64 v[220:221], s[26:27], 0, v[128:129]
	s_add_i32 m0, s28, 0x2000
	s_nop 0
	global_load_lds_dwordx4 v128, s[26:27]
	v_lshl_add_u64 v[220:221], v[224:225], 0, s[10:11]
	s_mov_b32 m0, s40
	s_nop 0
	global_load_lds_dwordx4 v[220:221], off
	v_lshl_add_u64 v[220:221], v[226:227], 0, s[10:11]
	s_mov_b32 m0, s41
	s_nop 0
	global_load_lds_dwordx4 v[220:221], off
	s_waitcnt vmcnt(8) lgkmcnt(0)
	s_barrier
	s_setprio 1
	v_mfma_f32_16x16x32_bf16 v[60:63], v[148:151], v[188:191], v[60:63]
	v_mfma_f32_16x16x32_bf16 v[52:55], v[156:159], v[188:191], v[52:55]
	v_mfma_f32_16x16x32_bf16 v[44:47], v[148:151], v[196:199], v[44:47]
	v_mfma_f32_16x16x32_bf16 v[36:39], v[156:159], v[196:199], v[36:39]
	v_mfma_f32_16x16x32_bf16 v[28:31], v[148:151], v[204:207], v[28:31]
	v_mfma_f32_16x16x32_bf16 v[20:23], v[156:159], v[204:207], v[20:23]
	v_mfma_f32_16x16x32_bf16 v[12:15], v[148:151], v[212:215], v[12:15]
	v_mfma_f32_16x16x32_bf16 v[4:7], v[156:159], v[212:215], v[4:7]
	v_mfma_f32_16x16x32_bf16 v[60:63], v[152:155], v[192:195], v[60:63]
	v_mfma_f32_16x16x32_bf16 v[52:55], v[160:163], v[192:195], v[52:55]
	v_mfma_f32_16x16x32_bf16 v[44:47], v[152:155], v[200:203], v[44:47]
	v_mfma_f32_16x16x32_bf16 v[36:39], v[160:163], v[200:203], v[36:39]
	v_mfma_f32_16x16x32_bf16 v[28:31], v[152:155], v[208:211], v[28:31]
	v_mfma_f32_16x16x32_bf16 v[20:23], v[160:163], v[208:211], v[20:23]
	v_mfma_f32_16x16x32_bf16 v[12:15], v[152:155], v[216:219], v[12:15]
	v_mfma_f32_16x16x32_bf16 v[4:7], v[160:163], v[216:219], v[4:7]
	v_mfma_f32_16x16x32_bf16 v[56:59], v[172:175], v[188:191], v[56:59]
	v_mfma_f32_16x16x32_bf16 v[48:51], v[180:183], v[188:191], v[48:51]
	v_mfma_f32_16x16x32_bf16 v[40:43], v[172:175], v[196:199], v[40:43]
	v_mfma_f32_16x16x32_bf16 v[32:35], v[180:183], v[196:199], v[32:35]
	v_mfma_f32_16x16x32_bf16 v[24:27], v[172:175], v[204:207], v[24:27]
	v_mfma_f32_16x16x32_bf16 v[16:19], v[180:183], v[204:207], v[16:19]
	v_mfma_f32_16x16x32_bf16 v[8:11], v[172:175], v[212:215], v[8:11]
	v_mfma_f32_16x16x32_bf16 v[0:3], v[180:183], v[212:215], v[0:3]
	v_mfma_f32_16x16x32_bf16 v[56:59], v[176:179], v[192:195], v[56:59]
	v_mfma_f32_16x16x32_bf16 v[48:51], v[184:187], v[192:195], v[48:51]
	v_mfma_f32_16x16x32_bf16 v[40:43], v[176:179], v[200:203], v[40:43]
	v_mfma_f32_16x16x32_bf16 v[32:35], v[184:187], v[200:203], v[32:35]
	v_mfma_f32_16x16x32_bf16 v[24:27], v[176:179], v[208:211], v[24:27]
	v_mfma_f32_16x16x32_bf16 v[16:19], v[184:187], v[208:211], v[16:19]
	v_mfma_f32_16x16x32_bf16 v[8:11], v[176:179], v[216:219], v[8:11]
	v_mfma_f32_16x16x32_bf16 v[0:3], v[184:187], v[216:219], v[0:3]
	s_setprio 0
	s_barrier
	s_add_i32 s67, s67, 2
	s_add_u32 s24, s24, 0x100
	s_addc_u32 s25, s25, 0
	s_add_u32 s65, s65, 0x100
	s_addc_u32 s66, s66, 0
	s_cmp_gt_u32 s67, 13
	s_cbranch_scc0 .LBB0_1867
	s_and_b64 vcc, exec, s[12:13]
	s_cbranch_vccz .LBB0_1870
	s_barrier

; #define PG8_STAGE(bufoff, gbase, voff) do { _Pragma("unroll") for (int _i = 0; _i < 2; ++_i) \
;         __builtin_amdgcn_global_load_lds((const unsigned*)((const char*)(gbase) + (voff)[_i]), (PG8_LAS unsigned*)(lds + (bufoff) + ldsw + _i * 8192), 16, 0, 0); } while (0)
; #define PG8_LDA(dst, b, h) do { _Pragma("unroll") for (int m = 0; m < 4; ++m) _Pragma("unroll") for (int k = 0; k < 2; ++k) dst[m][k] = *(const PG8_LAS bf16x8*)(lds + PG8_SA(b, h) + aoff + m * 2048 + k * 1024); } while (0)
; #define PG8_LDB(dst, b, h) do { _Pragma("unroll") for (int n = 0; n < 2; ++n) _Pragma("unroll") for (int k = 0; k < 2; ++k) dst[n][k] = *(const PG8_LAS bf16x8*)(lds + PG8_SB(b, h) + boff + n * 2048 + k * 1024); } while (0)
; #define PG8_MMA(ai, bj, At, Bt) do { __builtin_amdgcn_s_setprio(1); _Pragma("unroll") for (int m = 0; m < 4; ++m) _Pragma("unroll") for (int n = 0; n < 2; ++n) _Pragma("unroll") for (int k = 0; k < 2; ++k) \
;         acc[ai][bj][m][n] = __builtin_amdgcn_mfma_f32_16x16x32_bf16(Bt[n][k], At[m][k], acc[ai][bj][m][n], 0, 0, 0); __builtin_amdgcn_s_setprio(0); } while (0)
; #define PG8_WAIT_V(n) asm volatile("s_waitcnt vmcnt(" #n ")" ::: "memory")
; #define PG8_WAIT_L(n) asm volatile("s_waitcnt lgkmcnt(" #n ")" ::: "memory")
; template <class Epi, class Sched, bool ALIGN_EPI = false, bool SP2 = false>
; __device__ __forceinline__ void gemm_phase(PG8_LAS unsigned char* lds, const Gemm g, const Sched& S, const Epi& E, const int wid) {
;     ...
;             const bool last = (t == nt - 2);
;             const char* a1 = cA + (size_t)(t + 1) * kstep;
;             const char* a2 = last ? nA : cA + (size_t)(t + 2) * kstep; const char* b2 = last ? nB : cB + (size_t)(t + 2) * kstep;
;             const char* a3 = a2 + kstep; const char* b3 = b2 + kstep;
;             if (last && has_next) S.a_ready(nxt);
;             if constexpr (SP2) {
;             PG8_LDB(B0, 0, 0); PG8_LDB(B1, 0, 1); PG8_SCHED; PG8_LDA(At, 0, 0); PG8_STAGE(PG8_SA(1, 1), a1 + hstepA, voffA);
;             PG8_WAIT_V(8); PG8_WAIT_L(0); PG8_BAR; PG8_MMA(0, 0, At, B0); PG8_MMA(0, 1, At, B1); PG8_BAR; PG8_SCHED;
;             PG8_LDA(At, 0, 1); PG8_STAGE(PG8_SB(0, 0), b2, voffB); PG8_STAGE(PG8_SB(0, 1), b2 + hstepB, voffB); PG8_STAGE(PG8_SA(0, 0), a2, voffA);
;             PG8_WAIT_V(8); PG8_WAIT_L(0); PG8_BAR; PG8_MMA(1, 0, At, B0); PG8_MMA(1, 1, At, B1); PG8_BAR; PG8_SCHED;
.LBB0_1952:
	ds_read_b128 v[128:131], v190
	ds_read_b128 v[132:135], v190 offset:1024
	ds_read_b128 v[136:139], v190 offset:2048
	ds_read_b128 v[140:143], v190 offset:3072
	ds_read_b128 v[144:147], v191
	ds_read_b128 v[148:151], v191 offset:1024
	ds_read_b128 v[172:175], v191 offset:2048
	ds_read_b128 v[176:179], v191 offset:3072
	s_add_u32 s24, s22, 0x100
	s_addc_u32 s25, s23, 0
	s_cmp_eq_u32 s68, 40
	s_cselect_b32 s29, s7, s25
	s_cselect_b32 s28, s6, s24
	s_cselect_b32 s27, s21, s67
	s_cselect_b32 s26, s20, s66
	s_add_i32 m0, s34, 0xc000
	ds_read_b128 v[180:183], v192
	ds_read_b128 v[184:187], v192 offset:1024
	ds_read_b128 v[194:197], v192 offset:2048
	ds_read_b128 v[198:201], v192 offset:3072
	ds_read_b128 v[202:205], v192 offset:4096
	ds_read_b128 v[206:209], v192 offset:5120
	ds_read_b128 v[210:213], v192 offset:6144
	ds_read_b128 v[214:217], v192 offset:7168
	global_load_lds_dwordx4 v164, s[22:23]
	s_add_i32 m0, s34, 0xe000
	s_nop 0
	global_load_lds_dwordx4 v166, s[22:23]
	s_waitcnt vmcnt(8) lgkmcnt(0)
	s_barrier
	s_setprio 1
	v_mfma_f32_16x16x32_bf16 v[124:127], v[128:131], v[180:183], v[124:127]
	v_mfma_f32_16x16x32_bf16 v[120:123], v[136:139], v[180:183], v[120:123]
	v_mfma_f32_16x16x32_bf16 v[108:111], v[128:131], v[194:197], v[108:111]
	v_mfma_f32_16x16x32_bf16 v[104:107], v[136:139], v[194:197], v[104:107]
	v_mfma_f32_16x16x32_bf16 v[92:95], v[128:131], v[202:205], v[92:95]
	v_mfma_f32_16x16x32_bf16 v[88:91], v[136:139], v[202:205], v[88:91]
	v_mfma_f32_16x16x32_bf16 v[76:79], v[128:131], v[210:213], v[76:79]
	v_mfma_f32_16x16x32_bf16 v[72:75], v[136:139], v[210:213], v[72:75]
	v_mfma_f32_16x16x32_bf16 v[124:127], v[132:135], v[184:187], v[124:127]
	v_mfma_f32_16x16x32_bf16 v[120:123], v[140:143], v[184:187], v[120:123]
	v_mfma_f32_16x16x32_bf16 v[108:111], v[132:135], v[198:201], v[108:111]
	v_mfma_f32_16x16x32_bf16 v[104:107], v[140:143], v[198:201], v[104:107]
	v_mfma_f32_16x16x32_bf16 v[92:95], v[132:135], v[206:209], v[92:95]
	v_mfma_f32_16x16x32_bf16 v[88:91], v[140:143], v[206:209], v[88:91]
	v_mfma_f32_16x16x32_bf16 v[76:79], v[132:135], v[214:217], v[76:79]
	v_mfma_f32_16x16x32_bf16 v[72:75], v[140:143], v[214:217], v[72:75]
	v_mfma_f32_16x16x32_bf16 v[116:119], v[144:147], v[180:183], v[116:119]
	v_mfma_f32_16x16x32_bf16 v[112:115], v[172:175], v[180:183], v[112:115]
	v_mfma_f32_16x16x32_bf16 v[100:103], v[144:147], v[194:197], v[100:103]
	v_mfma_f32_16x16x32_bf16 v[96:99], v[172:175], v[194:197], v[96:99]
	v_mfma_f32_16x16x32_bf16 v[84:87], v[144:147], v[202:205], v[84:87]
	v_mfma_f32_16x16x32_bf16 v[80:83], v[172:175], v[202:205], v[80:83]
	v_mfma_f32_16x16x32_bf16 v[68:71], v[144:147], v[210:213], v[68:71]
	v_mfma_f32_16x16x32_bf16 v[64:67], v[172:175], v[210:213], v[64:67]
	v_mfma_f32_16x16x32_bf16 v[116:119], v[148:151], v[184:187], v[116:119]
	v_mfma_f32_16x16x32_bf16 v[112:115], v[176:179], v[184:187], v[112:115]
	v_mfma_f32_16x16x32_bf16 v[100:103], v[148:151], v[198:201], v[100:103]
	v_mfma_f32_16x16x32_bf16 v[96:99], v[176:179], v[198:201], v[96:99]
	v_mfma_f32_16x16x32_bf16 v[84:87], v[148:151], v[206:209], v[84:87]
	v_mfma_f32_16x16x32_bf16 v[80:83], v[176:179], v[206:209], v[80:83]
	v_mfma_f32_16x16x32_bf16 v[68:71], v[148:151], v[214:217], v[68:71]
	v_mfma_f32_16x16x32_bf16 v[64:67], v[176:179], v[214:217], v[64:67]
	s_setprio 0
	s_barrier
	s_add_i32 s22, s45, s33
	v_lshl_add_u64 v[218:219], s[26:27], 0, v[154:155]
	s_mov_b32 m0, s22
	ds_read_b128 v[180:183], v192 offset:16384
	ds_read_b128 v[184:187], v192 offset:17408
	ds_read_b128 v[194:197], v192 offset:18432
	ds_read_b128 v[198:201], v192 offset:19456
	ds_read_b128 v[202:205], v192 offset:20480
	ds_read_b128 v[206:209], v192 offset:21504
	ds_read_b128 v[210:213], v192 offset:22528
	ds_read_b128 v[214:217], v192 offset:23552
	global_load_lds_dwordx4 v154, s[26:27]
	s_add_i32 m0, s22, 0x2000
	s_add_u32 s22, s26, 0xb0000
	v_lshl_add_u64 v[220:221], s[26:27], 0, v[158:159]
	s_addc_u32 s23, s27, 0
	s_add_i32 s69, s46, s33
	global_load_lds_dwordx4 v158, s[26:27]
	s_mov_b32 m0, s69
	v_lshl_add_u64 v[224:225], s[28:29], 0, v[156:157]
	global_load_lds_dwordx4 v154, s[22:23]
	s_add_i32 m0, s69, 0x2000
	s_nop 0
	global_load_lds_dwordx4 v158, s[22:23]
	v_lshl_add_u64 v[222:223], s[28:29], 0, v[152:153]
	s_mov_b32 m0, s34
	s_nop 0
	global_load_lds_dwordx4 v152, s[28:29]
	s_mov_b32 m0, s35
	s_nop 0
	global_load_lds_dwordx4 v156, s[28:29]
	s_waitcnt vmcnt(8) lgkmcnt(0)
	s_barrier
	s_setprio 1
	v_mfma_f32_16x16x32_bf16 v[60:63], v[128:131], v[180:183], v[60:63]
	v_mfma_f32_16x16x32_bf16 v[56:59], v[136:139], v[180:183], v[56:59]
	v_mfma_f32_16x16x32_bf16 v[44:47], v[128:131], v[194:197], v[44:47]
	v_mfma_f32_16x16x32_bf16 v[40:43], v[136:139], v[194:197], v[40:43]
	v_mfma_f32_16x16x32_bf16 v[28:31], v[128:131], v[202:205], v[28:31]
	v_mfma_f32_16x16x32_bf16 v[24:27], v[136:139], v[202:205], v[24:27]
	v_mfma_f32_16x16x32_bf16 v[12:15], v[128:131], v[210:213], v[12:15]
	v_mfma_f32_16x16x32_bf16 v[8:11], v[136:139], v[210:213], v[8:11]
	v_mfma_f32_16x16x32_bf16 v[60:63], v[132:135], v[184:187], v[60:63]
	v_mfma_f32_16x16x32_bf16 v[56:59], v[140:143], v[184:187], v[56:59]
	v_mfma_f32_16x16x32_bf16 v[44:47], v[132:135], v[198:201], v[44:47]
	v_mfma_f32_16x16x32_bf16 v[40:43], v[140:143], v[198:201], v[40:43]
	v_mfma_f32_16x16x32_bf16 v[28:31], v[132:135], v[206:209], v[28:31]
	v_mfma_f32_16x16x32_bf16 v[24:27], v[140:143], v[206:209], v[24:27]
	v_mfma_f32_16x16x32_bf16 v[12:15], v[132:135], v[214:217], v[12:15]
	v_mfma_f32_16x16x32_bf16 v[8:11], v[140:143], v[214:217], v[8:11]
	v_mfma_f32_16x16x32_bf16 v[52:55], v[144:147], v[180:183], v[52:55]
	v_mfma_f32_16x16x32_bf16 v[48:51], v[172:175], v[180:183], v[48:51]
	v_mfma_f32_16x16x32_bf16 v[36:39], v[144:147], v[194:197], v[36:39]
	v_mfma_f32_16x16x32_bf16 v[32:35], v[172:175], v[194:197], v[32:35]
	v_mfma_f32_16x16x32_bf16 v[20:23], v[144:147], v[202:205], v[20:23]
	v_mfma_f32_16x16x32_bf16 v[16:19], v[172:175], v[202:205], v[16:19]
	v_mfma_f32_16x16x32_bf16 v[4:7], v[144:147], v[210:213], v[4:7]
	v_mfma_f32_16x16x32_bf16 v[0:3], v[172:175], v[210:213], v[0:3]
	v_mfma_f32_16x16x32_bf16 v[52:55], v[148:151], v[184:187], v[52:55]
	v_mfma_f32_16x16x32_bf16 v[48:51], v[176:179], v[184:187], v[48:51]
	v_mfma_f32_16x16x32_bf16 v[36:39], v[148:151], v[198:201], v[36:39]
	v_mfma_f32_16x16x32_bf16 v[32:35], v[176:179], v[198:201], v[32:35]
	v_mfma_f32_16x16x32_bf16 v[20:23], v[148:151], v[206:209], v[20:23]
	v_mfma_f32_16x16x32_bf16 v[16:19], v[176:179], v[206:209], v[16:19]
	v_mfma_f32_16x16x32_bf16 v[4:7], v[148:151], v[214:217], v[4:7]
	v_mfma_f32_16x16x32_bf16 v[0:3], v[176:179], v[214:217], v[0:3]
	s_setprio 0
	s_barrier
; #define PG8_STAGE(bufoff, gbase, voff) do { _Pragma("unroll") for (int _i = 0; _i < 2; ++_i) \
;         __builtin_amdgcn_global_load_lds((const unsigned*)((const char*)(gbase) + (voff)[_i]), (PG8_LAS unsigned*)(lds + (bufoff) + ldsw + _i * 8192), 16, 0, 0); } while (0)
; #define PG8_LDA(dst, b, h) do { _Pragma("unroll") for (int m = 0; m < 4; ++m) _Pragma("unroll") for (int k = 0; k < 2; ++k) dst[m][k] = *(const PG8_LAS bf16x8*)(lds + PG8_SA(b, h) + aoff + m * 2048 + k * 1024); } while (0)
; #define PG8_LDB(dst, b, h) do { _Pragma("unroll") for (int n = 0; n < 2; ++n) _Pragma("unroll") for (int k = 0; k < 2; ++k) dst[n][k] = *(const PG8_LAS bf16x8*)(lds + PG8_SB(b, h) + boff + n * 2048 + k * 1024); } while (0)
; #define PG8_MMA(ai, bj, At, Bt) do { __builtin_amdgcn_s_setprio(1); _Pragma("unroll") for (int m = 0; m < 4; ++m) _Pragma("unroll") for (int n = 0; n < 2; ++n) _Pragma("unroll") for (int k = 0; k < 2; ++k) \
;         acc[ai][bj][m][n] = __builtin_amdgcn_mfma_f32_16x16x32_bf16(Bt[n][k], At[m][k], acc[ai][bj][m][n], 0, 0, 0); __builtin_amdgcn_s_setprio(0); } while (0)
; #define PG8_WAIT_V(n) asm volatile("s_waitcnt vmcnt(" #n ")" ::: "memory")
; #define PG8_WAIT_L(n) asm volatile("s_waitcnt lgkmcnt(" #n ")" ::: "memory")
; #define PG8_BAR __builtin_amdgcn_s_barrier()
; #define PG8_SCHED __builtin_amdgcn_sched_barrier(0)
; template <class Epi, class Sched, bool ALIGN_EPI = false, bool SP2 = false>
; __device__ __forceinline__ void gemm_phase(PG8_LAS unsigned char* lds, const Gemm g, const Sched& S, const Epi& E, const int wid) {
;     ...
;             PG8_LDB(B0, 1, 0); PG8_LDB(B1, 1, 1); PG8_SCHED; PG8_LDA(At, 1, 0); PG8_STAGE(PG8_SA(0, 1), a2 + hstepA, voffA);
;             PG8_WAIT_V(8); PG8_WAIT_L(0); PG8_BAR; PG8_MMA(0, 0, At, B0); PG8_MMA(0, 1, At, B1); PG8_BAR; PG8_SCHED;
;             PG8_LDA(At, 1, 1); PG8_STAGE(PG8_SB(1, 0), b3, voffB); PG8_STAGE(PG8_SB(1, 1), b3 + hstepB, voffB); PG8_STAGE(PG8_SA(1, 0), a3, voffA);
;             PG8_WAIT_V(8); PG8_WAIT_L(0); PG8_BAR; PG8_MMA(1, 0, At, B0); PG8_MMA(1, 1, At, B1); PG8_BAR; PG8_SCHED;
;     ...
;         if constexpr (ALIGN_EPI) { if (wr == 0) PG8_BAR; }
	s_add_i32 s69, 0, 0x18000
	s_add_i32 s70, 0, 0x1c000
	v_add_u32_e32 v140, s69, v189
	v_add_u32_e32 v176, s70, v189
	ds_read_b128 v[128:131], v140
	ds_read_b128 v[132:135], v140 offset:1024
	ds_read_b128 v[136:139], v140 offset:2048
	ds_read_b128 v[140:143], v140 offset:3072
	ds_read_b128 v[144:147], v176
	ds_read_b128 v[148:151], v176 offset:1024
	ds_read_b128 v[172:175], v176 offset:2048
	ds_read_b128 v[176:179], v176 offset:3072
	s_add_u32 s22, s28, 0xb0000
	s_addc_u32 s23, s29, 0
	s_mov_b32 m0, s36
	ds_read_b128 v[180:183], v192 offset:32768
	ds_read_b128 v[184:187], v192 offset:33792
	ds_read_b128 v[194:197], v192 offset:34816
	ds_read_b128 v[198:201], v192 offset:35840
	ds_read_b128 v[202:205], v192 offset:36864
	ds_read_b128 v[206:209], v192 offset:37888
	ds_read_b128 v[210:213], v192 offset:38912
	ds_read_b128 v[214:217], v192 offset:39936
	global_load_lds_dwordx4 v152, s[22:23]
	s_mov_b32 m0, s37
	s_nop 0
	global_load_lds_dwordx4 v156, s[22:23]
	s_waitcnt vmcnt(8) lgkmcnt(0)
	s_barrier
	s_setprio 1
	v_mfma_f32_16x16x32_bf16 v[124:127], v[128:131], v[180:183], v[124:127]
	v_mfma_f32_16x16x32_bf16 v[120:123], v[136:139], v[180:183], v[120:123]
	v_mfma_f32_16x16x32_bf16 v[108:111], v[128:131], v[194:197], v[108:111]
	v_mfma_f32_16x16x32_bf16 v[104:107], v[136:139], v[194:197], v[104:107]
	v_mfma_f32_16x16x32_bf16 v[92:95], v[128:131], v[202:205], v[92:95]
	v_mfma_f32_16x16x32_bf16 v[88:91], v[136:139], v[202:205], v[88:91]
	v_mfma_f32_16x16x32_bf16 v[76:79], v[128:131], v[210:213], v[76:79]
	v_mfma_f32_16x16x32_bf16 v[72:75], v[136:139], v[210:213], v[72:75]
	v_mfma_f32_16x16x32_bf16 v[124:127], v[132:135], v[184:187], v[124:127]
	v_mfma_f32_16x16x32_bf16 v[120:123], v[140:143], v[184:187], v[120:123]
	v_mfma_f32_16x16x32_bf16 v[108:111], v[132:135], v[198:201], v[108:111]
	v_mfma_f32_16x16x32_bf16 v[104:107], v[140:143], v[198:201], v[104:107]
	v_mfma_f32_16x16x32_bf16 v[92:95], v[132:135], v[206:209], v[92:95]
	v_mfma_f32_16x16x32_bf16 v[88:91], v[140:143], v[206:209], v[88:91]
	v_mfma_f32_16x16x32_bf16 v[76:79], v[132:135], v[214:217], v[76:79]
	v_mfma_f32_16x16x32_bf16 v[72:75], v[140:143], v[214:217], v[72:75]
	v_mfma_f32_16x16x32_bf16 v[116:119], v[144:147], v[180:183], v[116:119]
	v_mfma_f32_16x16x32_bf16 v[112:115], v[172:175], v[180:183], v[112:115]
	v_mfma_f32_16x16x32_bf16 v[100:103], v[144:147], v[194:197], v[100:103]
	v_mfma_f32_16x16x32_bf16 v[96:99], v[172:175], v[194:197], v[96:99]
	v_mfma_f32_16x16x32_bf16 v[84:87], v[144:147], v[202:205], v[84:87]
	v_mfma_f32_16x16x32_bf16 v[80:83], v[172:175], v[202:205], v[80:83]
	v_mfma_f32_16x16x32_bf16 v[68:71], v[144:147], v[210:213], v[68:71]
	v_mfma_f32_16x16x32_bf16 v[64:67], v[172:175], v[210:213], v[64:67]
	v_mfma_f32_16x16x32_bf16 v[116:119], v[148:151], v[184:187], v[116:119]
	v_mfma_f32_16x16x32_bf16 v[112:115], v[176:179], v[184:187], v[112:115]
	v_mfma_f32_16x16x32_bf16 v[100:103], v[148:151], v[198:201], v[100:103]
	v_mfma_f32_16x16x32_bf16 v[96:99], v[176:179], v[198:201], v[96:99]
	v_mfma_f32_16x16x32_bf16 v[84:87], v[148:151], v[206:209], v[84:87]
	v_mfma_f32_16x16x32_bf16 v[80:83], v[176:179], v[206:209], v[80:83]
	v_mfma_f32_16x16x32_bf16 v[68:71], v[148:151], v[214:217], v[68:71]
	v_mfma_f32_16x16x32_bf16 v[64:67], v[176:179], v[214:217], v[64:67]
	s_setprio 0
	s_barrier
	s_add_i32 s22, s69, s33
	v_lshl_add_u64 v[218:219], v[218:219], 0, s[16:17]
	s_mov_b32 m0, s22
	ds_read_b128 v[180:183], v192 offset:49152
	ds_read_b128 v[184:187], v192 offset:50176
	ds_read_b128 v[194:197], v192 offset:51200
	ds_read_b128 v[198:201], v192 offset:52224
	ds_read_b128 v[202:205], v192 offset:53248
	ds_read_b128 v[206:209], v192 offset:54272
	ds_read_b128 v[210:213], v192 offset:55296
	ds_read_b128 v[214:217], v192 offset:56320
	global_load_lds_dwordx4 v[218:219], off
	s_add_i32 m0, s22, 0x2000
	s_add_u32 s22, s26, 0xb0080
	v_lshl_add_u64 v[218:219], v[220:221], 0, s[16:17]
	s_addc_u32 s23, s27, 0
	s_add_i32 s26, s70, s33
	global_load_lds_dwordx4 v[218:219], off
	s_mov_b32 m0, s26
	s_nop 0
	global_load_lds_dwordx4 v154, s[22:23]
	v_lshl_add_u64 v[218:219], s[22:23], 0, v[158:159]
	s_add_i32 m0, s26, 0x2000
	s_nop 0
	global_load_lds_dwordx4 v158, s[22:23]
	v_lshl_add_u64 v[218:219], v[222:223], 0, s[16:17]
	s_mov_b32 m0, s39
	s_nop 0
	global_load_lds_dwordx4 v[218:219], off
	v_lshl_add_u64 v[218:219], v[224:225], 0, s[16:17]
	s_mov_b32 m0, s40
	s_nop 0
	global_load_lds_dwordx4 v[218:219], off
	s_waitcnt vmcnt(8) lgkmcnt(0)
	s_barrier
	s_setprio 1
	v_mfma_f32_16x16x32_bf16 v[60:63], v[128:131], v[180:183], v[60:63]
	v_mfma_f32_16x16x32_bf16 v[56:59], v[136:139], v[180:183], v[56:59]
	v_mfma_f32_16x16x32_bf16 v[44:47], v[128:131], v[194:197], v[44:47]
	v_mfma_f32_16x16x32_bf16 v[40:43], v[136:139], v[194:197], v[40:43]
	v_mfma_f32_16x16x32_bf16 v[28:31], v[128:131], v[202:205], v[28:31]
	v_mfma_f32_16x16x32_bf16 v[24:27], v[136:139], v[202:205], v[24:27]
	v_mfma_f32_16x16x32_bf16 v[12:15], v[128:131], v[210:213], v[12:15]
	v_mfma_f32_16x16x32_bf16 v[8:11], v[136:139], v[210:213], v[8:11]
	v_mfma_f32_16x16x32_bf16 v[60:63], v[132:135], v[184:187], v[60:63]
	v_mfma_f32_16x16x32_bf16 v[56:59], v[140:143], v[184:187], v[56:59]
	v_mfma_f32_16x16x32_bf16 v[44:47], v[132:135], v[198:201], v[44:47]
	v_mfma_f32_16x16x32_bf16 v[40:43], v[140:143], v[198:201], v[40:43]
	v_mfma_f32_16x16x32_bf16 v[28:31], v[132:135], v[206:209], v[28:31]
	v_mfma_f32_16x16x32_bf16 v[24:27], v[140:143], v[206:209], v[24:27]
	v_mfma_f32_16x16x32_bf16 v[12:15], v[132:135], v[214:217], v[12:15]
	v_mfma_f32_16x16x32_bf16 v[8:11], v[140:143], v[214:217], v[8:11]
	v_mfma_f32_16x16x32_bf16 v[52:55], v[144:147], v[180:183], v[52:55]
	v_mfma_f32_16x16x32_bf16 v[48:51], v[172:175], v[180:183], v[48:51]
	v_mfma_f32_16x16x32_bf16 v[36:39], v[144:147], v[194:197], v[36:39]
	v_mfma_f32_16x16x32_bf16 v[32:35], v[172:175], v[194:197], v[32:35]
	v_mfma_f32_16x16x32_bf16 v[20:23], v[144:147], v[202:205], v[20:23]
	v_mfma_f32_16x16x32_bf16 v[16:19], v[172:175], v[202:205], v[16:19]
	v_mfma_f32_16x16x32_bf16 v[4:7], v[144:147], v[210:213], v[4:7]
	v_mfma_f32_16x16x32_bf16 v[0:3], v[172:175], v[210:213], v[0:3]
	v_mfma_f32_16x16x32_bf16 v[52:55], v[148:151], v[184:187], v[52:55]
	v_mfma_f32_16x16x32_bf16 v[48:51], v[176:179], v[184:187], v[48:51]
	v_mfma_f32_16x16x32_bf16 v[36:39], v[148:151], v[198:201], v[36:39]
	v_mfma_f32_16x16x32_bf16 v[32:35], v[176:179], v[198:201], v[32:35]
	v_mfma_f32_16x16x32_bf16 v[20:23], v[148:151], v[206:209], v[20:23]
	v_mfma_f32_16x16x32_bf16 v[16:19], v[176:179], v[206:209], v[16:19]
	v_mfma_f32_16x16x32_bf16 v[4:7], v[148:151], v[214:217], v[4:7]
	v_mfma_f32_16x16x32_bf16 v[0:3], v[176:179], v[214:217], v[0:3]
	s_setprio 0
	s_barrier
	s_add_i32 s68, s68, 2
	s_add_u32 s66, s66, 0x100
	s_addc_u32 s67, s67, 0
	s_cmp_gt_u32 s68, 41
	s_mov_b64 s[22:23], s[24:25]
	s_cbranch_scc0 .LBB0_1952
	s_and_b64 vcc, exec, s[18:19]
	s_cbranch_vccz .LBB0_1955
	s_barrier

; #define PG8_STAGE(bufoff, gbase, voff) do { _Pragma("unroll") for (int _i = 0; _i < 2; ++_i) \
;         __builtin_amdgcn_global_load_lds((const unsigned*)((const char*)(gbase) + (voff)[_i]), (PG8_LAS unsigned*)(lds + (bufoff) + ldsw + _i * 8192), 16, 0, 0); } while (0)
; #define PG8_LDA(dst, b, h) do { _Pragma("unroll") for (int m = 0; m < 4; ++m) _Pragma("unroll") for (int k = 0; k < 2; ++k) dst[m][k] = *(const PG8_LAS bf16x8*)(lds + PG8_SA(b, h) + aoff + m * 2048 + k * 1024); } while (0)
; #define PG8_LDB(dst, b, h) do { _Pragma("unroll") for (int n = 0; n < 2; ++n) _Pragma("unroll") for (int k = 0; k < 2; ++k) dst[n][k] = *(const PG8_LAS bf16x8*)(lds + PG8_SB(b, h) + boff + n * 2048 + k * 1024); } while (0)
; #define PG8_MMA(ai, bj, At, Bt) do { __builtin_amdgcn_s_setprio(1); _Pragma("unroll") for (int m = 0; m < 4; ++m) _Pragma("unroll") for (int n = 0; n < 2; ++n) _Pragma("unroll") for (int k = 0; k < 2; ++k) \
;         acc[ai][bj][m][n] = __builtin_amdgcn_mfma_f32_16x16x32_bf16(Bt[n][k], At[m][k], acc[ai][bj][m][n], 0, 0, 0); __builtin_amdgcn_s_setprio(0); } while (0)
; #define PG8_WAIT_V(n) asm volatile("s_waitcnt vmcnt(" #n ")" ::: "memory")
; #define PG8_WAIT_L(n) asm volatile("s_waitcnt lgkmcnt(" #n ")" ::: "memory")
; template <class Epi, class Sched, bool ALIGN_EPI = false, bool SP2 = false>
; __device__ __forceinline__ void gemm_phase(PG8_LAS unsigned char* lds, const Gemm g, const Sched& S, const Epi& E, const int wid) {
;     ...
;             const bool last = (t == nt - 2);
;             const char* a1 = cA + (size_t)(t + 1) * kstep;
;             const char* a2 = last ? nA : cA + (size_t)(t + 2) * kstep; const char* b2 = last ? nB : cB + (size_t)(t + 2) * kstep;
;             const char* a3 = a2 + kstep; const char* b3 = b2 + kstep;
;             if (last && has_next) S.a_ready(nxt);
;             if constexpr (SP2) {
;             PG8_LDB(B0, 0, 0); PG8_LDB(B1, 0, 1); PG8_SCHED; PG8_LDA(At, 0, 0); PG8_STAGE(PG8_SA(1, 1), a1 + hstepA, voffA);
;             PG8_WAIT_V(8); PG8_WAIT_L(0); PG8_BAR; PG8_MMA(0, 0, At, B0); PG8_MMA(0, 1, At, B1); PG8_BAR; PG8_SCHED;
;             PG8_LDA(At, 0, 1); PG8_STAGE(PG8_SB(0, 0), b2, voffB); PG8_STAGE(PG8_SB(0, 1), b2 + hstepB, voffB); PG8_STAGE(PG8_SA(0, 0), a2, voffA);
;             PG8_WAIT_V(8); PG8_WAIT_L(0); PG8_BAR; PG8_MMA(1, 0, At, B0); PG8_MMA(1, 1, At, B1); PG8_BAR; PG8_SCHED;
.LBB0_2049:
	ds_read_b128 v[146:149], v179
	ds_read_b128 v[150:153], v179 offset:1024
	ds_read_b128 v[154:157], v179 offset:2048
	ds_read_b128 v[158:161], v179 offset:3072
	ds_read_b128 v[162:165], v180
	ds_read_b128 v[166:169], v180 offset:1024
	ds_read_b128 v[184:187], v180 offset:2048
	ds_read_b128 v[188:191], v180 offset:3072
	s_add_u32 s12, s8, 0xfffc0080
	s_addc_u32 s13, s9, -1
	s_cmp_eq_u32 s71, 12
	s_cselect_b32 s39, s7, s13
	s_cselect_b32 s38, s11, s12
	s_cselect_b32 s13, s29, s41
	s_cselect_b32 s12, s31, s40
	s_add_i32 m0, s46, 0xc000
	ds_read_b128 v[192:195], v181
	ds_read_b128 v[196:199], v181 offset:1024
	ds_read_b128 v[200:203], v181 offset:2048
	ds_read_b128 v[204:207], v181 offset:3072
	ds_read_b128 v[208:211], v181 offset:4096
	ds_read_b128 v[212:215], v181 offset:5120
	ds_read_b128 v[216:219], v181 offset:6144
	ds_read_b128 v[220:223], v181 offset:7168
	global_load_lds_dwordx4 v138, s[8:9]
	s_add_i32 m0, s46, 0xe000
	s_nop 0
	global_load_lds_dwordx4 v140, s[8:9]
	s_waitcnt vmcnt(8) lgkmcnt(0)
	s_barrier
	s_setprio 1
	v_mfma_f32_16x16x32_bf16 v[124:127], v[146:149], v[192:195], v[124:127]
	v_mfma_f32_16x16x32_bf16 v[120:123], v[154:157], v[192:195], v[120:123]
	v_mfma_f32_16x16x32_bf16 v[108:111], v[146:149], v[200:203], v[108:111]
	v_mfma_f32_16x16x32_bf16 v[104:107], v[154:157], v[200:203], v[104:107]
	v_mfma_f32_16x16x32_bf16 v[92:95], v[146:149], v[208:211], v[92:95]
	v_mfma_f32_16x16x32_bf16 v[88:91], v[154:157], v[208:211], v[88:91]
	v_mfma_f32_16x16x32_bf16 v[76:79], v[146:149], v[216:219], v[76:79]
	v_mfma_f32_16x16x32_bf16 v[72:75], v[154:157], v[216:219], v[72:75]
	v_mfma_f32_16x16x32_bf16 v[124:127], v[150:153], v[196:199], v[124:127]
	v_mfma_f32_16x16x32_bf16 v[120:123], v[158:161], v[196:199], v[120:123]
	v_mfma_f32_16x16x32_bf16 v[108:111], v[150:153], v[204:207], v[108:111]
	v_mfma_f32_16x16x32_bf16 v[104:107], v[158:161], v[204:207], v[104:107]
	v_mfma_f32_16x16x32_bf16 v[92:95], v[150:153], v[212:215], v[92:95]
	v_mfma_f32_16x16x32_bf16 v[88:91], v[158:161], v[212:215], v[88:91]
	v_mfma_f32_16x16x32_bf16 v[76:79], v[150:153], v[220:223], v[76:79]
	v_mfma_f32_16x16x32_bf16 v[72:75], v[158:161], v[220:223], v[72:75]
	v_mfma_f32_16x16x32_bf16 v[116:119], v[162:165], v[192:195], v[116:119]
	v_mfma_f32_16x16x32_bf16 v[112:115], v[184:187], v[192:195], v[112:115]
	v_mfma_f32_16x16x32_bf16 v[100:103], v[162:165], v[200:203], v[100:103]
	v_mfma_f32_16x16x32_bf16 v[96:99], v[184:187], v[200:203], v[96:99]
	v_mfma_f32_16x16x32_bf16 v[84:87], v[162:165], v[208:211], v[84:87]
	v_mfma_f32_16x16x32_bf16 v[80:83], v[184:187], v[208:211], v[80:83]
	v_mfma_f32_16x16x32_bf16 v[68:71], v[162:165], v[216:219], v[68:71]
	v_mfma_f32_16x16x32_bf16 v[64:67], v[184:187], v[216:219], v[64:67]
	v_mfma_f32_16x16x32_bf16 v[116:119], v[166:169], v[196:199], v[116:119]
	v_mfma_f32_16x16x32_bf16 v[112:115], v[188:191], v[196:199], v[112:115]
	v_mfma_f32_16x16x32_bf16 v[100:103], v[166:169], v[204:207], v[100:103]
	v_mfma_f32_16x16x32_bf16 v[96:99], v[188:191], v[204:207], v[96:99]
	v_mfma_f32_16x16x32_bf16 v[84:87], v[166:169], v[212:215], v[84:87]
	v_mfma_f32_16x16x32_bf16 v[80:83], v[188:191], v[212:215], v[80:83]
	v_mfma_f32_16x16x32_bf16 v[68:71], v[166:169], v[220:223], v[68:71]
	v_mfma_f32_16x16x32_bf16 v[64:67], v[188:191], v[220:223], v[64:67]
	s_setprio 0
	s_barrier
	s_add_i32 s72, s69, s45
	v_lshl_add_u64 v[170:171], s[12:13], 0, v[130:131]
	s_mov_b32 m0, s72
	ds_read_b128 v[192:195], v181 offset:16384
	ds_read_b128 v[196:199], v181 offset:17408
	ds_read_b128 v[200:203], v181 offset:18432
	ds_read_b128 v[204:207], v181 offset:19456
	ds_read_b128 v[208:211], v181 offset:20480
	ds_read_b128 v[212:215], v181 offset:21504
	ds_read_b128 v[216:219], v181 offset:22528
	ds_read_b128 v[220:223], v181 offset:23552
	global_load_lds_dwordx4 v130, s[12:13]
	s_add_i32 m0, s72, 0x2000
	s_add_u32 s72, s12, 0x40000
	v_lshl_add_u64 v[224:225], s[12:13], 0, v[134:135]
	s_addc_u32 s73, s13, 0
	s_add_i32 s74, s70, s45
	global_load_lds_dwordx4 v134, s[12:13]
	s_mov_b32 m0, s74
	v_lshl_add_u64 v[228:229], s[38:39], 0, v[132:133]
	global_load_lds_dwordx4 v130, s[72:73]
	s_add_i32 m0, s74, 0x2000
	s_nop 0
	global_load_lds_dwordx4 v134, s[72:73]
	v_lshl_add_u64 v[226:227], s[38:39], 0, v[128:129]
	s_mov_b32 m0, s46
	s_nop 0
	global_load_lds_dwordx4 v128, s[38:39]
	s_mov_b32 m0, s47
	s_nop 0
	global_load_lds_dwordx4 v132, s[38:39]
	s_waitcnt vmcnt(8) lgkmcnt(0)
	s_barrier
	s_setprio 1
	v_mfma_f32_16x16x32_bf16 v[60:63], v[146:149], v[192:195], v[60:63]
	v_mfma_f32_16x16x32_bf16 v[56:59], v[154:157], v[192:195], v[56:59]
	v_mfma_f32_16x16x32_bf16 v[44:47], v[146:149], v[200:203], v[44:47]
	v_mfma_f32_16x16x32_bf16 v[40:43], v[154:157], v[200:203], v[40:43]
	v_mfma_f32_16x16x32_bf16 v[28:31], v[146:149], v[208:211], v[28:31]
	v_mfma_f32_16x16x32_bf16 v[24:27], v[154:157], v[208:211], v[24:27]
	v_mfma_f32_16x16x32_bf16 v[12:15], v[146:149], v[216:219], v[12:15]
	v_mfma_f32_16x16x32_bf16 v[8:11], v[154:157], v[216:219], v[8:11]
	v_mfma_f32_16x16x32_bf16 v[60:63], v[150:153], v[196:199], v[60:63]
	v_mfma_f32_16x16x32_bf16 v[56:59], v[158:161], v[196:199], v[56:59]
	v_mfma_f32_16x16x32_bf16 v[44:47], v[150:153], v[204:207], v[44:47]
	v_mfma_f32_16x16x32_bf16 v[40:43], v[158:161], v[204:207], v[40:43]
	v_mfma_f32_16x16x32_bf16 v[28:31], v[150:153], v[212:215], v[28:31]
	v_mfma_f32_16x16x32_bf16 v[24:27], v[158:161], v[212:215], v[24:27]
	v_mfma_f32_16x16x32_bf16 v[12:15], v[150:153], v[220:223], v[12:15]
	v_mfma_f32_16x16x32_bf16 v[8:11], v[158:161], v[220:223], v[8:11]
	v_mfma_f32_16x16x32_bf16 v[52:55], v[162:165], v[192:195], v[52:55]
	v_mfma_f32_16x16x32_bf16 v[48:51], v[184:187], v[192:195], v[48:51]
	v_mfma_f32_16x16x32_bf16 v[36:39], v[162:165], v[200:203], v[36:39]
	v_mfma_f32_16x16x32_bf16 v[32:35], v[184:187], v[200:203], v[32:35]
	v_mfma_f32_16x16x32_bf16 v[20:23], v[162:165], v[208:211], v[20:23]
	v_mfma_f32_16x16x32_bf16 v[16:19], v[184:187], v[208:211], v[16:19]
	v_mfma_f32_16x16x32_bf16 v[4:7], v[162:165], v[216:219], v[4:7]
	v_mfma_f32_16x16x32_bf16 v[0:3], v[184:187], v[216:219], v[0:3]
	v_mfma_f32_16x16x32_bf16 v[52:55], v[166:169], v[196:199], v[52:55]
	v_mfma_f32_16x16x32_bf16 v[48:51], v[188:191], v[196:199], v[48:51]
	v_mfma_f32_16x16x32_bf16 v[36:39], v[166:169], v[204:207], v[36:39]
	v_mfma_f32_16x16x32_bf16 v[32:35], v[188:191], v[204:207], v[32:35]
	v_mfma_f32_16x16x32_bf16 v[20:23], v[166:169], v[212:215], v[20:23]
	v_mfma_f32_16x16x32_bf16 v[16:19], v[188:191], v[212:215], v[16:19]
	v_mfma_f32_16x16x32_bf16 v[4:7], v[166:169], v[220:223], v[4:7]
	v_mfma_f32_16x16x32_bf16 v[0:3], v[188:191], v[220:223], v[0:3]
	s_setprio 0
	s_barrier
; #define PG8_STAGE(bufoff, gbase, voff) do { _Pragma("unroll") for (int _i = 0; _i < 2; ++_i) \
;         __builtin_amdgcn_global_load_lds((const unsigned*)((const char*)(gbase) + (voff)[_i]), (PG8_LAS unsigned*)(lds + (bufoff) + ldsw + _i * 8192), 16, 0, 0); } while (0)
; #define PG8_LDA(dst, b, h) do { _Pragma("unroll") for (int m = 0; m < 4; ++m) _Pragma("unroll") for (int k = 0; k < 2; ++k) dst[m][k] = *(const PG8_LAS bf16x8*)(lds + PG8_SA(b, h) + aoff + m * 2048 + k * 1024); } while (0)
; #define PG8_LDB(dst, b, h) do { _Pragma("unroll") for (int n = 0; n < 2; ++n) _Pragma("unroll") for (int k = 0; k < 2; ++k) dst[n][k] = *(const PG8_LAS bf16x8*)(lds + PG8_SB(b, h) + boff + n * 2048 + k * 1024); } while (0)
; #define PG8_MMA(ai, bj, At, Bt) do { __builtin_amdgcn_s_setprio(1); _Pragma("unroll") for (int m = 0; m < 4; ++m) _Pragma("unroll") for (int n = 0; n < 2; ++n) _Pragma("unroll") for (int k = 0; k < 2; ++k) \
;         acc[ai][bj][m][n] = __builtin_amdgcn_mfma_f32_16x16x32_bf16(Bt[n][k], At[m][k], acc[ai][bj][m][n], 0, 0, 0); __builtin_amdgcn_s_setprio(0); } while (0)
; #define PG8_WAIT_V(n) asm volatile("s_waitcnt vmcnt(" #n ")" ::: "memory")
; #define PG8_WAIT_L(n) asm volatile("s_waitcnt lgkmcnt(" #n ")" ::: "memory")
; #define PG8_BAR __builtin_amdgcn_s_barrier()
; #define PG8_SCHED __builtin_amdgcn_sched_barrier(0)
; template <class Epi, class Sched, bool ALIGN_EPI = false, bool SP2 = false>
; __device__ __forceinline__ void gemm_phase(PG8_LAS unsigned char* lds, const Gemm g, const Sched& S, const Epi& E, const int wid) {
;     ...
;             PG8_LDB(B0, 1, 0); PG8_LDB(B1, 1, 1); PG8_SCHED; PG8_LDA(At, 1, 0); PG8_STAGE(PG8_SA(0, 1), a2 + hstepA, voffA);
;             PG8_WAIT_V(8); PG8_WAIT_L(0); PG8_BAR; PG8_MMA(0, 0, At, B0); PG8_MMA(0, 1, At, B1); PG8_BAR; PG8_SCHED;
;             PG8_LDA(At, 1, 1); PG8_STAGE(PG8_SB(1, 0), b3, voffB); PG8_STAGE(PG8_SB(1, 1), b3 + hstepB, voffB); PG8_STAGE(PG8_SA(1, 0), a3, voffA);
;             PG8_WAIT_V(8); PG8_WAIT_L(0); PG8_BAR; PG8_MMA(1, 0, At, B0); PG8_MMA(1, 1, At, B1); PG8_BAR; PG8_SCHED;
;     ...
;         if constexpr (ALIGN_EPI) { if (wr == 0) PG8_BAR; }
	s_add_i32 s72, 0, 0x18000
	s_add_i32 s73, 0, 0x1c000
	v_add_u32_e32 v158, s72, v174
	v_add_u32_e32 v188, s73, v174
	ds_read_b128 v[146:149], v158
	ds_read_b128 v[150:153], v158 offset:1024
	ds_read_b128 v[154:157], v158 offset:2048
	ds_read_b128 v[158:161], v158 offset:3072
	ds_read_b128 v[162:165], v188
	ds_read_b128 v[166:169], v188 offset:1024
	ds_read_b128 v[184:187], v188 offset:2048
	ds_read_b128 v[188:191], v188 offset:3072
	s_add_u32 s38, s38, 0x40000
	s_addc_u32 s39, s39, 0
	s_mov_b32 m0, s48
	ds_read_b128 v[192:195], v181 offset:32768
	ds_read_b128 v[196:199], v181 offset:33792
	ds_read_b128 v[200:203], v181 offset:34816
	ds_read_b128 v[204:207], v181 offset:35840
	ds_read_b128 v[208:211], v181 offset:36864
	ds_read_b128 v[212:215], v181 offset:37888
	ds_read_b128 v[216:219], v181 offset:38912
	ds_read_b128 v[220:223], v181 offset:39936
	global_load_lds_dwordx4 v128, s[38:39]
	s_mov_b32 m0, s49
	s_nop 0
	global_load_lds_dwordx4 v132, s[38:39]
	s_waitcnt vmcnt(8) lgkmcnt(0)
	s_barrier
	s_setprio 1
	v_mfma_f32_16x16x32_bf16 v[124:127], v[146:149], v[192:195], v[124:127]
	v_mfma_f32_16x16x32_bf16 v[120:123], v[154:157], v[192:195], v[120:123]
	v_mfma_f32_16x16x32_bf16 v[108:111], v[146:149], v[200:203], v[108:111]
	v_mfma_f32_16x16x32_bf16 v[104:107], v[154:157], v[200:203], v[104:107]
	v_mfma_f32_16x16x32_bf16 v[92:95], v[146:149], v[208:211], v[92:95]
	v_mfma_f32_16x16x32_bf16 v[88:91], v[154:157], v[208:211], v[88:91]
	v_mfma_f32_16x16x32_bf16 v[76:79], v[146:149], v[216:219], v[76:79]
	v_mfma_f32_16x16x32_bf16 v[72:75], v[154:157], v[216:219], v[72:75]
	v_mfma_f32_16x16x32_bf16 v[124:127], v[150:153], v[196:199], v[124:127]
	v_mfma_f32_16x16x32_bf16 v[120:123], v[158:161], v[196:199], v[120:123]
	v_mfma_f32_16x16x32_bf16 v[108:111], v[150:153], v[204:207], v[108:111]
	v_mfma_f32_16x16x32_bf16 v[104:107], v[158:161], v[204:207], v[104:107]
	v_mfma_f32_16x16x32_bf16 v[92:95], v[150:153], v[212:215], v[92:95]
	v_mfma_f32_16x16x32_bf16 v[88:91], v[158:161], v[212:215], v[88:91]
	v_mfma_f32_16x16x32_bf16 v[76:79], v[150:153], v[220:223], v[76:79]
	v_mfma_f32_16x16x32_bf16 v[72:75], v[158:161], v[220:223], v[72:75]
	v_mfma_f32_16x16x32_bf16 v[116:119], v[162:165], v[192:195], v[116:119]
	v_mfma_f32_16x16x32_bf16 v[112:115], v[184:187], v[192:195], v[112:115]
	v_mfma_f32_16x16x32_bf16 v[100:103], v[162:165], v[200:203], v[100:103]
	v_mfma_f32_16x16x32_bf16 v[96:99], v[184:187], v[200:203], v[96:99]
	v_mfma_f32_16x16x32_bf16 v[84:87], v[162:165], v[208:211], v[84:87]
	v_mfma_f32_16x16x32_bf16 v[80:83], v[184:187], v[208:211], v[80:83]
	v_mfma_f32_16x16x32_bf16 v[68:71], v[162:165], v[216:219], v[68:71]
	v_mfma_f32_16x16x32_bf16 v[64:67], v[184:187], v[216:219], v[64:67]
	v_mfma_f32_16x16x32_bf16 v[116:119], v[166:169], v[196:199], v[116:119]
	v_mfma_f32_16x16x32_bf16 v[112:115], v[188:191], v[196:199], v[112:115]
	v_mfma_f32_16x16x32_bf16 v[100:103], v[166:169], v[204:207], v[100:103]
	v_mfma_f32_16x16x32_bf16 v[96:99], v[188:191], v[204:207], v[96:99]
	v_mfma_f32_16x16x32_bf16 v[84:87], v[166:169], v[212:215], v[84:87]
	v_mfma_f32_16x16x32_bf16 v[80:83], v[188:191], v[212:215], v[80:83]
	v_mfma_f32_16x16x32_bf16 v[68:71], v[166:169], v[220:223], v[68:71]
	v_mfma_f32_16x16x32_bf16 v[64:67], v[188:191], v[220:223], v[64:67]
	s_setprio 0
	s_barrier
	s_add_i32 s38, s72, s45
	v_lshl_add_u64 v[170:171], v[170:171], 0, s[18:19]
	s_mov_b32 m0, s38
	ds_read_b128 v[192:195], v181 offset:49152
	ds_read_b128 v[196:199], v181 offset:50176
	ds_read_b128 v[200:203], v181 offset:51200
	ds_read_b128 v[204:207], v181 offset:52224
	ds_read_b128 v[208:211], v181 offset:53248
	ds_read_b128 v[212:215], v181 offset:54272
	ds_read_b128 v[216:219], v181 offset:55296
	ds_read_b128 v[220:223], v181 offset:56320
	global_load_lds_dwordx4 v[170:171], off
	s_add_i32 m0, s38, 0x2000
	s_add_u32 s12, s12, 0x40080
	v_lshl_add_u64 v[170:171], v[224:225], 0, s[18:19]
	s_addc_u32 s13, s13, 0
	s_add_i32 s38, s73, s45
	global_load_lds_dwordx4 v[170:171], off
	s_mov_b32 m0, s38
	s_nop 0
	global_load_lds_dwordx4 v130, s[12:13]
	v_lshl_add_u64 v[170:171], s[12:13], 0, v[134:135]
	s_add_i32 m0, s38, 0x2000
	s_nop 0
	global_load_lds_dwordx4 v134, s[12:13]
	v_lshl_add_u64 v[170:171], v[226:227], 0, s[18:19]
	s_mov_b32 m0, s65
	s_nop 0
	global_load_lds_dwordx4 v[170:171], off
	v_lshl_add_u64 v[170:171], v[228:229], 0, s[18:19]
	s_mov_b32 m0, s66
	s_nop 0
	global_load_lds_dwordx4 v[170:171], off
	s_waitcnt vmcnt(8) lgkmcnt(0)
	s_barrier
	s_setprio 1
	v_mfma_f32_16x16x32_bf16 v[60:63], v[146:149], v[192:195], v[60:63]
	v_mfma_f32_16x16x32_bf16 v[56:59], v[154:157], v[192:195], v[56:59]
	v_mfma_f32_16x16x32_bf16 v[44:47], v[146:149], v[200:203], v[44:47]
	v_mfma_f32_16x16x32_bf16 v[40:43], v[154:157], v[200:203], v[40:43]
	v_mfma_f32_16x16x32_bf16 v[28:31], v[146:149], v[208:211], v[28:31]
	v_mfma_f32_16x16x32_bf16 v[24:27], v[154:157], v[208:211], v[24:27]
	v_mfma_f32_16x16x32_bf16 v[12:15], v[146:149], v[216:219], v[12:15]
	v_mfma_f32_16x16x32_bf16 v[8:11], v[154:157], v[216:219], v[8:11]
	v_mfma_f32_16x16x32_bf16 v[60:63], v[150:153], v[196:199], v[60:63]
	v_mfma_f32_16x16x32_bf16 v[56:59], v[158:161], v[196:199], v[56:59]
	v_mfma_f32_16x16x32_bf16 v[44:47], v[150:153], v[204:207], v[44:47]
	v_mfma_f32_16x16x32_bf16 v[40:43], v[158:161], v[204:207], v[40:43]
	v_mfma_f32_16x16x32_bf16 v[28:31], v[150:153], v[212:215], v[28:31]
	v_mfma_f32_16x16x32_bf16 v[24:27], v[158:161], v[212:215], v[24:27]
	v_mfma_f32_16x16x32_bf16 v[12:15], v[150:153], v[220:223], v[12:15]
	v_mfma_f32_16x16x32_bf16 v[8:11], v[158:161], v[220:223], v[8:11]
	v_mfma_f32_16x16x32_bf16 v[52:55], v[162:165], v[192:195], v[52:55]
	v_mfma_f32_16x16x32_bf16 v[48:51], v[184:187], v[192:195], v[48:51]
	v_mfma_f32_16x16x32_bf16 v[36:39], v[162:165], v[200:203], v[36:39]
	v_mfma_f32_16x16x32_bf16 v[32:35], v[184:187], v[200:203], v[32:35]
	v_mfma_f32_16x16x32_bf16 v[20:23], v[162:165], v[208:211], v[20:23]
	v_mfma_f32_16x16x32_bf16 v[16:19], v[184:187], v[208:211], v[16:19]
	v_mfma_f32_16x16x32_bf16 v[4:7], v[162:165], v[216:219], v[4:7]
	v_mfma_f32_16x16x32_bf16 v[0:3], v[184:187], v[216:219], v[0:3]
	v_mfma_f32_16x16x32_bf16 v[52:55], v[166:169], v[196:199], v[52:55]
	v_mfma_f32_16x16x32_bf16 v[48:51], v[188:191], v[196:199], v[48:51]
	v_mfma_f32_16x16x32_bf16 v[36:39], v[166:169], v[204:207], v[36:39]
	v_mfma_f32_16x16x32_bf16 v[32:35], v[188:191], v[204:207], v[32:35]
	v_mfma_f32_16x16x32_bf16 v[20:23], v[166:169], v[212:215], v[20:23]
	v_mfma_f32_16x16x32_bf16 v[16:19], v[188:191], v[212:215], v[16:19]
	v_mfma_f32_16x16x32_bf16 v[4:7], v[166:169], v[220:223], v[4:7]
	v_mfma_f32_16x16x32_bf16 v[0:3], v[188:191], v[220:223], v[0:3]
	s_setprio 0
	s_barrier
	s_add_i32 s71, s71, 2
	s_add_u32 s8, s8, 0x100
	s_addc_u32 s9, s9, 0
	s_add_u32 s40, s40, 0x100
	s_addc_u32 s41, s41, 0
	s_cmp_gt_u32 s71, 13
	s_cbranch_scc0 .LBB0_2049
	s_and_b64 vcc, exec, s[20:21]
	s_cbranch_vccz .LBB0_2052
	s_barrier

; #define PG8_STAGE(bufoff, gbase, voff) do { _Pragma("unroll") for (int _i = 0; _i < 2; ++_i) \
;         __builtin_amdgcn_global_load_lds((const unsigned*)((const char*)(gbase) + (voff)[_i]), (PG8_LAS unsigned*)(lds + (bufoff) + ldsw + _i * 8192), 16, 0, 0); } while (0)
; #define PG8_LDA(dst, b, h) do { _Pragma("unroll") for (int m = 0; m < 4; ++m) _Pragma("unroll") for (int k = 0; k < 2; ++k) dst[m][k] = *(const PG8_LAS bf16x8*)(lds + PG8_SA(b, h) + aoff + m * 2048 + k * 1024); } while (0)
; #define PG8_LDB(dst, b, h) do { _Pragma("unroll") for (int n = 0; n < 2; ++n) _Pragma("unroll") for (int k = 0; k < 2; ++k) dst[n][k] = *(const PG8_LAS bf16x8*)(lds + PG8_SB(b, h) + boff + n * 2048 + k * 1024); } while (0)
; #define PG8_MMA(ai, bj, At, Bt) do { __builtin_amdgcn_s_setprio(1); _Pragma("unroll") for (int m = 0; m < 4; ++m) _Pragma("unroll") for (int n = 0; n < 2; ++n) _Pragma("unroll") for (int k = 0; k < 2; ++k) \
;         acc[ai][bj][m][n] = __builtin_amdgcn_mfma_f32_16x16x32_bf16(Bt[n][k], At[m][k], acc[ai][bj][m][n], 0, 0, 0); __builtin_amdgcn_s_setprio(0); } while (0)
; #define PG8_WAIT_V(n) asm volatile("s_waitcnt vmcnt(" #n ")" ::: "memory")
; #define PG8_WAIT_L(n) asm volatile("s_waitcnt lgkmcnt(" #n ")" ::: "memory")
; template <class Epi, class Sched, bool ALIGN_EPI = false, bool SP2 = false>
; __device__ __forceinline__ void gemm_phase(PG8_LAS unsigned char* lds, const Gemm g, const Sched& S, const Epi& E, const int wid) {
;     ...
;             const bool last = (t == nt - 2);
;             const char* a1 = cA + (size_t)(t + 1) * kstep;
;             const char* a2 = last ? nA : cA + (size_t)(t + 2) * kstep; const char* b2 = last ? nB : cB + (size_t)(t + 2) * kstep;
;             const char* a3 = a2 + kstep; const char* b3 = b2 + kstep;
;             if (last && has_next) S.a_ready(nxt);
;             if constexpr (SP2) {
;             PG8_LDB(B0, 0, 0); PG8_LDB(B1, 0, 1); PG8_SCHED; PG8_LDA(At, 0, 0); PG8_STAGE(PG8_SA(1, 1), a1 + hstepA, voffA);
;             PG8_WAIT_V(8); PG8_WAIT_L(0); PG8_BAR; PG8_MMA(0, 0, At, B0); PG8_MMA(0, 1, At, B1); PG8_BAR; PG8_SCHED;
;             PG8_LDA(At, 0, 1); PG8_STAGE(PG8_SB(0, 0), b2, voffB); PG8_STAGE(PG8_SB(0, 1), b2 + hstepB, voffB); PG8_STAGE(PG8_SA(0, 0), a2, voffA);
;             PG8_WAIT_V(8); PG8_WAIT_L(0); PG8_BAR; PG8_MMA(1, 0, At, B0); PG8_MMA(1, 1, At, B1); PG8_BAR; PG8_SCHED;
.LBB0_2280:
	s_add_u32 s37, s28, s36
	s_addc_u32 s44, s29, 0
	s_add_u32 s40, s37, 0x100
	s_addc_u32 s41, s44, 0
	s_and_b64 s[38:39], s[34:35], exec
	s_cselect_b32 s39, s19, s41
	s_cselect_b32 s38, s81, s40
	s_add_u32 s36, s26, s36
	s_addc_u32 s40, s27, 0
	s_add_u32 s36, s36, 0x100
	s_addc_u32 s40, s40, 0
	s_and_b64 s[34:35], s[34:35], exec
	s_cselect_b32 s41, s17, s40
	s_cselect_b32 s40, s82, s36
	s_add_u32 s46, s37, 0x80080
	ds_read_b128 v[142:145], v157
	ds_read_b128 v[146:149], v157 offset:1024
	ds_read_b128 v[150:153], v157 offset:2048
	ds_read_b128 v[162:165], v157 offset:3072
	ds_read_b128 v[166:169], v158
	ds_read_b128 v[170:173], v158 offset:1024
	ds_read_b128 v[174:177], v158 offset:2048
	ds_read_b128 v[178:181], v158 offset:3072
	s_addc_u32 s47, s44, 0
	s_add_i32 s93, s77, s0
	s_add_i32 m0, s70, 0xc000
	s_add_i32 s94, s70, 0xe000
	s_add_i32 s89, s93, 0x2000
	s_add_u32 s44, s40, 0x10000
	s_addc_u32 s45, s41, 0
	s_add_i32 s92, s78, s0
	s_add_i32 s91, s92, 0x2000
	s_add_i32 s88, 0, 0x18000
	s_add_i32 s87, 0, 0x1c000
	s_add_u32 s36, s38, 0x80000
	s_addc_u32 s37, s39, 0
	s_add_i32 s86, s88, s0
	s_add_i32 s84, s86, 0x2000
	s_add_u32 s34, s40, 0x10080
	s_addc_u32 s35, s41, 0
	s_add_i32 s85, s87, s0
	s_add_i32 s83, s85, 0x2000
	ds_read_b128 v[182:185], v159
	ds_read_b128 v[186:189], v159 offset:1024
	ds_read_b128 v[190:193], v159 offset:2048
	ds_read_b128 v[194:197], v159 offset:3072
	ds_read_b128 v[198:201], v159 offset:4096
	ds_read_b128 v[202:205], v159 offset:5120
	ds_read_b128 v[206:209], v159 offset:6144
	ds_read_b128 v[210:213], v159 offset:7168
	global_load_lds_dwordx4 v134, s[46:47]
	s_mov_b32 m0, s94
	s_nop 0
	global_load_lds_dwordx4 v130, s[46:47]
	s_waitcnt vmcnt(8) lgkmcnt(0)
	s_barrier
	s_setprio 1
	v_mfma_f32_16x16x32_bf16 v[124:127], v[142:145], v[182:185], v[124:127]
	v_mfma_f32_16x16x32_bf16 v[120:123], v[150:153], v[182:185], v[120:123]
	v_mfma_f32_16x16x32_bf16 v[116:119], v[142:145], v[190:193], v[116:119]
	v_mfma_f32_16x16x32_bf16 v[112:115], v[150:153], v[190:193], v[112:115]
	v_mfma_f32_16x16x32_bf16 v[100:103], v[142:145], v[198:201], v[100:103]
	v_mfma_f32_16x16x32_bf16 v[96:99], v[150:153], v[198:201], v[96:99]
	v_mfma_f32_16x16x32_bf16 v[84:87], v[142:145], v[206:209], v[84:87]
	v_mfma_f32_16x16x32_bf16 v[80:83], v[150:153], v[206:209], v[80:83]
	v_mfma_f32_16x16x32_bf16 v[124:127], v[146:149], v[186:189], v[124:127]
	v_mfma_f32_16x16x32_bf16 v[120:123], v[162:165], v[186:189], v[120:123]
	v_mfma_f32_16x16x32_bf16 v[116:119], v[146:149], v[194:197], v[116:119]
	v_mfma_f32_16x16x32_bf16 v[112:115], v[162:165], v[194:197], v[112:115]
	v_mfma_f32_16x16x32_bf16 v[100:103], v[146:149], v[202:205], v[100:103]
	v_mfma_f32_16x16x32_bf16 v[96:99], v[162:165], v[202:205], v[96:99]
	v_mfma_f32_16x16x32_bf16 v[84:87], v[146:149], v[210:213], v[84:87]
	v_mfma_f32_16x16x32_bf16 v[80:83], v[162:165], v[210:213], v[80:83]
	v_mfma_f32_16x16x32_bf16 v[108:111], v[166:169], v[182:185], v[108:111]
	v_mfma_f32_16x16x32_bf16 v[104:107], v[174:177], v[182:185], v[104:107]
	v_mfma_f32_16x16x32_bf16 v[92:95], v[166:169], v[190:193], v[92:95]
	v_mfma_f32_16x16x32_bf16 v[88:91], v[174:177], v[190:193], v[88:91]
	v_mfma_f32_16x16x32_bf16 v[76:79], v[166:169], v[198:201], v[76:79]
	v_mfma_f32_16x16x32_bf16 v[72:75], v[174:177], v[198:201], v[72:75]
	v_mfma_f32_16x16x32_bf16 v[68:71], v[166:169], v[206:209], v[68:71]
	v_mfma_f32_16x16x32_bf16 v[64:67], v[174:177], v[206:209], v[64:67]
	v_mfma_f32_16x16x32_bf16 v[108:111], v[170:173], v[186:189], v[108:111]
	v_mfma_f32_16x16x32_bf16 v[104:107], v[178:181], v[186:189], v[104:107]
	v_mfma_f32_16x16x32_bf16 v[92:95], v[170:173], v[194:197], v[92:95]
	v_mfma_f32_16x16x32_bf16 v[88:91], v[178:181], v[194:197], v[88:91]
	v_mfma_f32_16x16x32_bf16 v[76:79], v[170:173], v[202:205], v[76:79]
	v_mfma_f32_16x16x32_bf16 v[72:75], v[178:181], v[202:205], v[72:75]
	v_mfma_f32_16x16x32_bf16 v[68:71], v[170:173], v[210:213], v[68:71]
	v_mfma_f32_16x16x32_bf16 v[64:67], v[178:181], v[210:213], v[64:67]
	s_setprio 0
	s_barrier
	s_mov_b32 m0, s93
	v_lshl_add_u64 v[214:215], s[40:41], 0, v[132:133]
	ds_read_b128 v[182:185], v159 offset:16384
	ds_read_b128 v[186:189], v159 offset:17408
	ds_read_b128 v[190:193], v159 offset:18432
	ds_read_b128 v[194:197], v159 offset:19456
	ds_read_b128 v[198:201], v159 offset:20480
	ds_read_b128 v[202:205], v159 offset:21504
	ds_read_b128 v[206:209], v159 offset:22528
	ds_read_b128 v[210:213], v159 offset:23552
	global_load_lds_dwordx4 v132, s[40:41]
	v_lshl_add_u64 v[216:217], s[40:41], 0, v[128:129]
	s_mov_b32 m0, s89
	s_nop 0
	global_load_lds_dwordx4 v128, s[40:41]
	s_mov_b32 m0, s92
	v_lshl_add_u64 v[220:221], s[38:39], 0, v[130:131]
	global_load_lds_dwordx4 v132, s[44:45]
	s_mov_b32 m0, s91
	s_nop 0
	global_load_lds_dwordx4 v128, s[44:45]
	v_lshl_add_u64 v[218:219], s[38:39], 0, v[134:135]
	s_mov_b32 m0, s70
	s_nop 0
	global_load_lds_dwordx4 v134, s[38:39]
	s_mov_b32 m0, s71
	s_nop 0
	global_load_lds_dwordx4 v130, s[38:39]
	s_waitcnt vmcnt(8) lgkmcnt(0)
	s_barrier
; #define PG8_STAGE(bufoff, gbase, voff) do { _Pragma("unroll") for (int _i = 0; _i < 2; ++_i) \
;         __builtin_amdgcn_global_load_lds((const unsigned*)((const char*)(gbase) + (voff)[_i]), (PG8_LAS unsigned*)(lds + (bufoff) + ldsw + _i * 8192), 16, 0, 0); } while (0)
; #define PG8_LDA(dst, b, h) do { _Pragma("unroll") for (int m = 0; m < 4; ++m) _Pragma("unroll") for (int k = 0; k < 2; ++k) dst[m][k] = *(const PG8_LAS bf16x8*)(lds + PG8_SA(b, h) + aoff + m * 2048 + k * 1024); } while (0)
; #define PG8_LDB(dst, b, h) do { _Pragma("unroll") for (int n = 0; n < 2; ++n) _Pragma("unroll") for (int k = 0; k < 2; ++k) dst[n][k] = *(const PG8_LAS bf16x8*)(lds + PG8_SB(b, h) + boff + n * 2048 + k * 1024); } while (0)
; #define PG8_MMA(ai, bj, At, Bt) do { __builtin_amdgcn_s_setprio(1); _Pragma("unroll") for (int m = 0; m < 4; ++m) _Pragma("unroll") for (int n = 0; n < 2; ++n) _Pragma("unroll") for (int k = 0; k < 2; ++k) \
;         acc[ai][bj][m][n] = __builtin_amdgcn_mfma_f32_16x16x32_bf16(Bt[n][k], At[m][k], acc[ai][bj][m][n], 0, 0, 0); __builtin_amdgcn_s_setprio(0); } while (0)
; #define PG8_WAIT_V(n) asm volatile("s_waitcnt vmcnt(" #n ")" ::: "memory")
; #define PG8_WAIT_L(n) asm volatile("s_waitcnt lgkmcnt(" #n ")" ::: "memory")
; #define PG8_BAR __builtin_amdgcn_s_barrier()
; #define PG8_SCHED __builtin_amdgcn_sched_barrier(0)
; template <class Epi, class Sched, bool ALIGN_EPI = false, bool SP2 = false>
; __device__ __forceinline__ void gemm_phase(PG8_LAS unsigned char* lds, const Gemm g, const Sched& S, const Epi& E, const int wid) {
;     ...
;             PG8_WAIT_V(8); PG8_WAIT_L(0); PG8_BAR; PG8_MMA(1, 0, At, B0); PG8_MMA(1, 1, At, B1); PG8_BAR; PG8_SCHED;
;             PG8_LDB(B0, 1, 0); PG8_LDB(B1, 1, 1); PG8_SCHED; PG8_LDA(At, 1, 0); PG8_STAGE(PG8_SA(0, 1), a2 + hstepA, voffA);
;             PG8_WAIT_V(8); PG8_WAIT_L(0); PG8_BAR; PG8_MMA(0, 0, At, B0); PG8_MMA(0, 1, At, B1); PG8_BAR; PG8_SCHED;
	s_setprio 1
	v_mfma_f32_16x16x32_bf16 v[60:63], v[142:145], v[182:185], v[60:63]
	v_mfma_f32_16x16x32_bf16 v[56:59], v[150:153], v[182:185], v[56:59]
	v_mfma_f32_16x16x32_bf16 v[52:55], v[142:145], v[190:193], v[52:55]
	v_mfma_f32_16x16x32_bf16 v[48:51], v[150:153], v[190:193], v[48:51]
	v_mfma_f32_16x16x32_bf16 v[36:39], v[142:145], v[198:201], v[36:39]
	v_mfma_f32_16x16x32_bf16 v[32:35], v[150:153], v[198:201], v[32:35]
	v_mfma_f32_16x16x32_bf16 v[20:23], v[142:145], v[206:209], v[20:23]
	v_mfma_f32_16x16x32_bf16 v[16:19], v[150:153], v[206:209], v[16:19]
	v_mfma_f32_16x16x32_bf16 v[60:63], v[146:149], v[186:189], v[60:63]
	v_mfma_f32_16x16x32_bf16 v[56:59], v[162:165], v[186:189], v[56:59]
	v_mfma_f32_16x16x32_bf16 v[52:55], v[146:149], v[194:197], v[52:55]
	v_mfma_f32_16x16x32_bf16 v[48:51], v[162:165], v[194:197], v[48:51]
	v_mfma_f32_16x16x32_bf16 v[36:39], v[146:149], v[202:205], v[36:39]
	v_mfma_f32_16x16x32_bf16 v[32:35], v[162:165], v[202:205], v[32:35]
	v_mfma_f32_16x16x32_bf16 v[20:23], v[146:149], v[210:213], v[20:23]
	v_mfma_f32_16x16x32_bf16 v[16:19], v[162:165], v[210:213], v[16:19]
	v_mfma_f32_16x16x32_bf16 v[44:47], v[166:169], v[182:185], v[44:47]
	v_mfma_f32_16x16x32_bf16 v[40:43], v[174:177], v[182:185], v[40:43]
	v_mfma_f32_16x16x32_bf16 v[28:31], v[166:169], v[190:193], v[28:31]
	v_mfma_f32_16x16x32_bf16 v[24:27], v[174:177], v[190:193], v[24:27]
	v_mfma_f32_16x16x32_bf16 v[12:15], v[166:169], v[198:201], v[12:15]
	v_mfma_f32_16x16x32_bf16 v[8:11], v[174:177], v[198:201], v[8:11]
	v_mfma_f32_16x16x32_bf16 v[4:7], v[166:169], v[206:209], v[4:7]
	v_mfma_f32_16x16x32_bf16 v[0:3], v[174:177], v[206:209], v[0:3]
	v_mfma_f32_16x16x32_bf16 v[44:47], v[170:173], v[186:189], v[44:47]
	v_mfma_f32_16x16x32_bf16 v[40:43], v[178:181], v[186:189], v[40:43]
	v_mfma_f32_16x16x32_bf16 v[28:31], v[170:173], v[194:197], v[28:31]
	v_mfma_f32_16x16x32_bf16 v[24:27], v[178:181], v[194:197], v[24:27]
	v_mfma_f32_16x16x32_bf16 v[12:15], v[170:173], v[202:205], v[12:15]
	v_mfma_f32_16x16x32_bf16 v[8:11], v[178:181], v[202:205], v[8:11]
	v_mfma_f32_16x16x32_bf16 v[4:7], v[170:173], v[210:213], v[4:7]
	v_mfma_f32_16x16x32_bf16 v[0:3], v[178:181], v[210:213], v[0:3]
	s_setprio 0
	s_barrier
	v_add_u32_e32 v161, s88, v156
	ds_read_b128 v[142:145], v161
	ds_read_b128 v[146:149], v161 offset:1024
	ds_read_b128 v[150:153], v161 offset:2048
	ds_read_b128 v[162:165], v161 offset:3072
	v_add_u32_e32 v161, s87, v156
	ds_read_b128 v[166:169], v161
	ds_read_b128 v[170:173], v161 offset:1024
	ds_read_b128 v[174:177], v161 offset:2048
	ds_read_b128 v[178:181], v161 offset:3072
	s_mov_b32 m0, s72
	ds_read_b128 v[182:185], v159 offset:32768
	ds_read_b128 v[186:189], v159 offset:33792
	ds_read_b128 v[190:193], v159 offset:34816
	ds_read_b128 v[194:197], v159 offset:35840
	ds_read_b128 v[198:201], v159 offset:36864
	ds_read_b128 v[202:205], v159 offset:37888
	ds_read_b128 v[206:209], v159 offset:38912
	ds_read_b128 v[210:213], v159 offset:39936
	global_load_lds_dwordx4 v134, s[36:37]
	s_mov_b32 m0, s73
	s_nop 0
	global_load_lds_dwordx4 v130, s[36:37]
	s_waitcnt vmcnt(8) lgkmcnt(0)
	s_barrier
	s_setprio 1
	v_mfma_f32_16x16x32_bf16 v[124:127], v[142:145], v[182:185], v[124:127]
	v_mfma_f32_16x16x32_bf16 v[120:123], v[150:153], v[182:185], v[120:123]
	v_mfma_f32_16x16x32_bf16 v[116:119], v[142:145], v[190:193], v[116:119]
	v_mfma_f32_16x16x32_bf16 v[112:115], v[150:153], v[190:193], v[112:115]
	v_mfma_f32_16x16x32_bf16 v[100:103], v[142:145], v[198:201], v[100:103]
	v_mfma_f32_16x16x32_bf16 v[96:99], v[150:153], v[198:201], v[96:99]
	v_mfma_f32_16x16x32_bf16 v[84:87], v[142:145], v[206:209], v[84:87]
	v_mfma_f32_16x16x32_bf16 v[80:83], v[150:153], v[206:209], v[80:83]
	v_mfma_f32_16x16x32_bf16 v[124:127], v[146:149], v[186:189], v[124:127]
	v_mfma_f32_16x16x32_bf16 v[120:123], v[162:165], v[186:189], v[120:123]
	v_mfma_f32_16x16x32_bf16 v[116:119], v[146:149], v[194:197], v[116:119]
	v_mfma_f32_16x16x32_bf16 v[112:115], v[162:165], v[194:197], v[112:115]
	v_mfma_f32_16x16x32_bf16 v[100:103], v[146:149], v[202:205], v[100:103]
	v_mfma_f32_16x16x32_bf16 v[96:99], v[162:165], v[202:205], v[96:99]
	v_mfma_f32_16x16x32_bf16 v[84:87], v[146:149], v[210:213], v[84:87]
	v_mfma_f32_16x16x32_bf16 v[80:83], v[162:165], v[210:213], v[80:83]
	v_mfma_f32_16x16x32_bf16 v[108:111], v[166:169], v[182:185], v[108:111]
	v_mfma_f32_16x16x32_bf16 v[104:107], v[174:177], v[182:185], v[104:107]
	v_mfma_f32_16x16x32_bf16 v[92:95], v[166:169], v[190:193], v[92:95]
	v_mfma_f32_16x16x32_bf16 v[88:91], v[174:177], v[190:193], v[88:91]
	v_mfma_f32_16x16x32_bf16 v[76:79], v[166:169], v[198:201], v[76:79]
	v_mfma_f32_16x16x32_bf16 v[72:75], v[174:177], v[198:201], v[72:75]
	v_mfma_f32_16x16x32_bf16 v[68:71], v[166:169], v[206:209], v[68:71]
	v_mfma_f32_16x16x32_bf16 v[64:67], v[174:177], v[206:209], v[64:67]
	v_mfma_f32_16x16x32_bf16 v[108:111], v[170:173], v[186:189], v[108:111]
	v_mfma_f32_16x16x32_bf16 v[104:107], v[178:181], v[186:189], v[104:107]
	v_mfma_f32_16x16x32_bf16 v[92:95], v[170:173], v[194:197], v[92:95]
	v_mfma_f32_16x16x32_bf16 v[88:91], v[178:181], v[194:197], v[88:91]
	v_mfma_f32_16x16x32_bf16 v[76:79], v[170:173], v[202:205], v[76:79]
	v_mfma_f32_16x16x32_bf16 v[72:75], v[178:181], v[202:205], v[72:75]
	v_mfma_f32_16x16x32_bf16 v[68:71], v[170:173], v[210:213], v[68:71]
	v_mfma_f32_16x16x32_bf16 v[64:67], v[178:181], v[210:213], v[64:67]
	s_setprio 0
	s_barrier
; #define PG8_STAGE(bufoff, gbase, voff) do { _Pragma("unroll") for (int _i = 0; _i < 2; ++_i) \
;         __builtin_amdgcn_global_load_lds((const unsigned*)((const char*)(gbase) + (voff)[_i]), (PG8_LAS unsigned*)(lds + (bufoff) + ldsw + _i * 8192), 16, 0, 0); } while (0)
; #define PG8_LDA(dst, b, h) do { _Pragma("unroll") for (int m = 0; m < 4; ++m) _Pragma("unroll") for (int k = 0; k < 2; ++k) dst[m][k] = *(const PG8_LAS bf16x8*)(lds + PG8_SA(b, h) + aoff + m * 2048 + k * 1024); } while (0)
; #define PG8_MMA(ai, bj, At, Bt) do { __builtin_amdgcn_s_setprio(1); _Pragma("unroll") for (int m = 0; m < 4; ++m) _Pragma("unroll") for (int n = 0; n < 2; ++n) _Pragma("unroll") for (int k = 0; k < 2; ++k) \
;         acc[ai][bj][m][n] = __builtin_amdgcn_mfma_f32_16x16x32_bf16(Bt[n][k], At[m][k], acc[ai][bj][m][n], 0, 0, 0); __builtin_amdgcn_s_setprio(0); } while (0)
; #define PG8_WAIT_V(n) asm volatile("s_waitcnt vmcnt(" #n ")" ::: "memory")
; #define PG8_WAIT_L(n) asm volatile("s_waitcnt lgkmcnt(" #n ")" ::: "memory")
; #define PG8_BAR __builtin_amdgcn_s_barrier()
; #define PG8_SCHED __builtin_amdgcn_sched_barrier(0)
; template <class Epi, class Sched, bool ALIGN_EPI = false, bool SP2 = false>
; __device__ __forceinline__ void gemm_phase(PG8_LAS unsigned char* lds, const Gemm g, const Sched& S, const Epi& E, const int wid) {
;     ...
;             PG8_LDA(At, 1, 1); PG8_STAGE(PG8_SB(1, 0), b3, voffB); PG8_STAGE(PG8_SB(1, 1), b3 + hstepB, voffB); PG8_STAGE(PG8_SA(1, 0), a3, voffA);
;             PG8_WAIT_V(8); PG8_WAIT_L(0); PG8_BAR; PG8_MMA(1, 0, At, B0); PG8_MMA(1, 1, At, B1); PG8_BAR; PG8_SCHED;
;     ...
;         if constexpr (ALIGN_EPI) { if (wr == 0) PG8_BAR; }
	s_mov_b32 m0, s86
	v_lshl_add_u64 v[214:215], v[214:215], 0, s[12:13]
	ds_read_b128 v[182:185], v159 offset:49152
	ds_read_b128 v[186:189], v159 offset:50176
	ds_read_b128 v[190:193], v159 offset:51200
	ds_read_b128 v[194:197], v159 offset:52224
	ds_read_b128 v[198:201], v159 offset:53248
	ds_read_b128 v[202:205], v159 offset:54272
	ds_read_b128 v[206:209], v159 offset:55296
	ds_read_b128 v[210:213], v159 offset:56320
	global_load_lds_dwordx4 v[214:215], off
	v_lshl_add_u64 v[214:215], v[216:217], 0, s[12:13]
	s_mov_b32 m0, s84
	s_nop 0
	global_load_lds_dwordx4 v[214:215], off
	s_mov_b32 m0, s85
	s_nop 0
	global_load_lds_dwordx4 v132, s[34:35]
	v_lshl_add_u64 v[214:215], s[34:35], 0, v[128:129]
	s_mov_b32 m0, s83
	s_nop 0
	global_load_lds_dwordx4 v128, s[34:35]
	v_lshl_add_u64 v[214:215], v[218:219], 0, s[12:13]
	s_mov_b32 m0, s74
	s_nop 0
	global_load_lds_dwordx4 v[214:215], off
	v_lshl_add_u64 v[214:215], v[220:221], 0, s[12:13]
	s_mov_b32 m0, s75
	s_nop 0
	global_load_lds_dwordx4 v[214:215], off
	s_waitcnt vmcnt(8) lgkmcnt(0)
	s_barrier
	s_setprio 1
	v_mfma_f32_16x16x32_bf16 v[60:63], v[142:145], v[182:185], v[60:63]
	v_mfma_f32_16x16x32_bf16 v[56:59], v[150:153], v[182:185], v[56:59]
	v_mfma_f32_16x16x32_bf16 v[52:55], v[142:145], v[190:193], v[52:55]
	v_mfma_f32_16x16x32_bf16 v[48:51], v[150:153], v[190:193], v[48:51]
	v_mfma_f32_16x16x32_bf16 v[36:39], v[142:145], v[198:201], v[36:39]
	v_mfma_f32_16x16x32_bf16 v[32:35], v[150:153], v[198:201], v[32:35]
	v_mfma_f32_16x16x32_bf16 v[20:23], v[142:145], v[206:209], v[20:23]
	v_mfma_f32_16x16x32_bf16 v[16:19], v[150:153], v[206:209], v[16:19]
	v_mfma_f32_16x16x32_bf16 v[60:63], v[146:149], v[186:189], v[60:63]
	v_mfma_f32_16x16x32_bf16 v[56:59], v[162:165], v[186:189], v[56:59]
	v_mfma_f32_16x16x32_bf16 v[52:55], v[146:149], v[194:197], v[52:55]
	v_mfma_f32_16x16x32_bf16 v[48:51], v[162:165], v[194:197], v[48:51]
	v_mfma_f32_16x16x32_bf16 v[36:39], v[146:149], v[202:205], v[36:39]
	v_mfma_f32_16x16x32_bf16 v[32:35], v[162:165], v[202:205], v[32:35]
	v_mfma_f32_16x16x32_bf16 v[20:23], v[146:149], v[210:213], v[20:23]
	v_mfma_f32_16x16x32_bf16 v[16:19], v[162:165], v[210:213], v[16:19]
	v_mfma_f32_16x16x32_bf16 v[44:47], v[166:169], v[182:185], v[44:47]
	v_mfma_f32_16x16x32_bf16 v[40:43], v[174:177], v[182:185], v[40:43]
	v_mfma_f32_16x16x32_bf16 v[28:31], v[166:169], v[190:193], v[28:31]
	v_mfma_f32_16x16x32_bf16 v[24:27], v[174:177], v[190:193], v[24:27]
	v_mfma_f32_16x16x32_bf16 v[12:15], v[166:169], v[198:201], v[12:15]
	v_mfma_f32_16x16x32_bf16 v[8:11], v[174:177], v[198:201], v[8:11]
	v_mfma_f32_16x16x32_bf16 v[4:7], v[166:169], v[206:209], v[4:7]
	v_mfma_f32_16x16x32_bf16 v[0:3], v[174:177], v[206:209], v[0:3]
	v_mfma_f32_16x16x32_bf16 v[44:47], v[170:173], v[186:189], v[44:47]
	v_mfma_f32_16x16x32_bf16 v[40:43], v[178:181], v[186:189], v[40:43]
	v_mfma_f32_16x16x32_bf16 v[28:31], v[170:173], v[194:197], v[28:31]
	v_mfma_f32_16x16x32_bf16 v[24:27], v[178:181], v[194:197], v[24:27]
	v_mfma_f32_16x16x32_bf16 v[12:15], v[170:173], v[202:205], v[12:15]
	v_mfma_f32_16x16x32_bf16 v[8:11], v[178:181], v[202:205], v[8:11]
	v_mfma_f32_16x16x32_bf16 v[4:7], v[170:173], v[210:213], v[4:7]
	v_mfma_f32_16x16x32_bf16 v[0:3], v[178:181], v[210:213], v[0:3]
	s_setprio 0
	s_barrier
	s_movk_i32 s36, 0x100
	s_andn2_b64 vcc, exec, s[30:31]
	s_mov_b64 s[34:35], -1
	s_mov_b64 s[30:31], 0
	s_cbranch_vccz .LBB0_2280
	s_and_b64 vcc, exec, s[14:15]
	s_cbranch_vccz .LBB0_2283
	s_barrier

; #define PG8_STAGE(bufoff, gbase, voff) do { _Pragma("unroll") for (int _i = 0; _i < 2; ++_i) \
;         __builtin_amdgcn_global_load_lds((const unsigned*)((const char*)(gbase) + (voff)[_i]), (PG8_LAS unsigned*)(lds + (bufoff) + ldsw + _i * 8192), 16, 0, 0); } while (0)
; #define PG8_LDA(dst, b, h) do { _Pragma("unroll") for (int m = 0; m < 4; ++m) _Pragma("unroll") for (int k = 0; k < 2; ++k) dst[m][k] = *(const PG8_LAS bf16x8*)(lds + PG8_SA(b, h) + aoff + m * 2048 + k * 1024); } while (0)
; #define PG8_LDB(dst, b, h) do { _Pragma("unroll") for (int n = 0; n < 2; ++n) _Pragma("unroll") for (int k = 0; k < 2; ++k) dst[n][k] = *(const PG8_LAS bf16x8*)(lds + PG8_SB(b, h) + boff + n * 2048 + k * 1024); } while (0)
; #define PG8_MMA(ai, bj, At, Bt) do { __builtin_amdgcn_s_setprio(1); _Pragma("unroll") for (int m = 0; m < 4; ++m) _Pragma("unroll") for (int n = 0; n < 2; ++n) _Pragma("unroll") for (int k = 0; k < 2; ++k) \
;         acc[ai][bj][m][n] = __builtin_amdgcn_mfma_f32_16x16x32_bf16(Bt[n][k], At[m][k], acc[ai][bj][m][n], 0, 0, 0); __builtin_amdgcn_s_setprio(0); } while (0)
; #define PG8_WAIT_V(n) asm volatile("s_waitcnt vmcnt(" #n ")" ::: "memory")
; #define PG8_WAIT_L(n) asm volatile("s_waitcnt lgkmcnt(" #n ")" ::: "memory")
; template <class Epi, class Sched, bool ALIGN_EPI = false, bool SP2 = false>
; __device__ __forceinline__ void gemm_phase(PG8_LAS unsigned char* lds, const Gemm g, const Sched& S, const Epi& E, const int wid) {
;     ...
;             const bool last = (t == nt - 2);
;             const char* a1 = cA + (size_t)(t + 1) * kstep;
;             const char* a2 = last ? nA : cA + (size_t)(t + 2) * kstep; const char* b2 = last ? nB : cB + (size_t)(t + 2) * kstep;
;             const char* a3 = a2 + kstep; const char* b3 = b2 + kstep;
;             if (last && has_next) S.a_ready(nxt);
;             if constexpr (SP2) {
;             PG8_LDB(B0, 0, 0); PG8_LDB(B1, 0, 1); PG8_SCHED; PG8_LDA(At, 0, 0); PG8_STAGE(PG8_SA(1, 1), a1 + hstepA, voffA);
;             PG8_WAIT_V(8); PG8_WAIT_L(0); PG8_BAR; PG8_MMA(0, 0, At, B0); PG8_MMA(0, 1, At, B1); PG8_BAR; PG8_SCHED;
;             PG8_LDA(At, 0, 1); PG8_STAGE(PG8_SB(0, 0), b2, voffB); PG8_STAGE(PG8_SB(0, 1), b2 + hstepB, voffB); PG8_STAGE(PG8_SA(0, 0), a2, voffA);
;             PG8_WAIT_V(8); PG8_WAIT_L(0); PG8_BAR; PG8_MMA(1, 0, At, B0); PG8_MMA(1, 1, At, B1); PG8_BAR; PG8_SCHED;
.LBB0_2725:
	ds_read_b128 v[128:131], v190
	ds_read_b128 v[132:135], v190 offset:1024
	ds_read_b128 v[136:139], v190 offset:2048
	ds_read_b128 v[140:143], v190 offset:3072
	ds_read_b128 v[144:147], v191
	ds_read_b128 v[148:151], v191 offset:1024
	ds_read_b128 v[172:175], v191 offset:2048
	ds_read_b128 v[176:179], v191 offset:3072
	s_add_u32 s34, s30, 0xfffc0080
	s_addc_u32 s35, s31, -1
	s_cmp_eq_u32 s60, 12
	s_cselect_b32 s37, s21, s35
	s_cselect_b32 s36, s27, s34
	s_cselect_b32 s35, s19, s59
	s_cselect_b32 s34, s29, s58
	s_add_i32 m0, s40, 0xc000
	ds_read_b128 v[180:183], v192
	ds_read_b128 v[184:187], v192 offset:1024
	ds_read_b128 v[194:197], v192 offset:2048
	ds_read_b128 v[198:201], v192 offset:3072
	ds_read_b128 v[202:205], v192 offset:4096
	ds_read_b128 v[206:209], v192 offset:5120
	ds_read_b128 v[210:213], v192 offset:6144
	ds_read_b128 v[214:217], v192 offset:7168
	global_load_lds_dwordx4 v164, s[30:31]
	s_add_i32 m0, s40, 0xe000
	s_nop 0
	global_load_lds_dwordx4 v166, s[30:31]
	s_waitcnt vmcnt(8) lgkmcnt(0)
	s_barrier
	s_setprio 1
	v_mfma_f32_16x16x32_bf16 v[124:127], v[128:131], v[180:183], v[124:127]
	v_mfma_f32_16x16x32_bf16 v[120:123], v[136:139], v[180:183], v[120:123]
	v_mfma_f32_16x16x32_bf16 v[108:111], v[128:131], v[194:197], v[108:111]
	v_mfma_f32_16x16x32_bf16 v[104:107], v[136:139], v[194:197], v[104:107]
	v_mfma_f32_16x16x32_bf16 v[92:95], v[128:131], v[202:205], v[92:95]
	v_mfma_f32_16x16x32_bf16 v[88:91], v[136:139], v[202:205], v[88:91]
	v_mfma_f32_16x16x32_bf16 v[76:79], v[128:131], v[210:213], v[76:79]
	v_mfma_f32_16x16x32_bf16 v[72:75], v[136:139], v[210:213], v[72:75]
	v_mfma_f32_16x16x32_bf16 v[124:127], v[132:135], v[184:187], v[124:127]
	v_mfma_f32_16x16x32_bf16 v[120:123], v[140:143], v[184:187], v[120:123]
	v_mfma_f32_16x16x32_bf16 v[108:111], v[132:135], v[198:201], v[108:111]
	v_mfma_f32_16x16x32_bf16 v[104:107], v[140:143], v[198:201], v[104:107]
	v_mfma_f32_16x16x32_bf16 v[92:95], v[132:135], v[206:209], v[92:95]
	v_mfma_f32_16x16x32_bf16 v[88:91], v[140:143], v[206:209], v[88:91]
	v_mfma_f32_16x16x32_bf16 v[76:79], v[132:135], v[214:217], v[76:79]
	v_mfma_f32_16x16x32_bf16 v[72:75], v[140:143], v[214:217], v[72:75]
	v_mfma_f32_16x16x32_bf16 v[116:119], v[144:147], v[180:183], v[116:119]
	v_mfma_f32_16x16x32_bf16 v[112:115], v[172:175], v[180:183], v[112:115]
	v_mfma_f32_16x16x32_bf16 v[100:103], v[144:147], v[194:197], v[100:103]
	v_mfma_f32_16x16x32_bf16 v[96:99], v[172:175], v[194:197], v[96:99]
	v_mfma_f32_16x16x32_bf16 v[84:87], v[144:147], v[202:205], v[84:87]
	v_mfma_f32_16x16x32_bf16 v[80:83], v[172:175], v[202:205], v[80:83]
	v_mfma_f32_16x16x32_bf16 v[68:71], v[144:147], v[210:213], v[68:71]
	v_mfma_f32_16x16x32_bf16 v[64:67], v[172:175], v[210:213], v[64:67]
	v_mfma_f32_16x16x32_bf16 v[116:119], v[148:151], v[184:187], v[116:119]
	v_mfma_f32_16x16x32_bf16 v[112:115], v[176:179], v[184:187], v[112:115]
	v_mfma_f32_16x16x32_bf16 v[100:103], v[148:151], v[198:201], v[100:103]
	v_mfma_f32_16x16x32_bf16 v[96:99], v[176:179], v[198:201], v[96:99]
	v_mfma_f32_16x16x32_bf16 v[84:87], v[148:151], v[206:209], v[84:87]
	v_mfma_f32_16x16x32_bf16 v[80:83], v[176:179], v[206:209], v[80:83]
	v_mfma_f32_16x16x32_bf16 v[68:71], v[148:151], v[214:217], v[68:71]
	v_mfma_f32_16x16x32_bf16 v[64:67], v[176:179], v[214:217], v[64:67]
	s_setprio 0
	s_barrier
	s_add_i32 s61, s49, s39
	v_lshl_add_u64 v[218:219], s[34:35], 0, v[154:155]
	s_mov_b32 m0, s61
	ds_read_b128 v[180:183], v192 offset:16384
	ds_read_b128 v[184:187], v192 offset:17408
	ds_read_b128 v[194:197], v192 offset:18432
	ds_read_b128 v[198:201], v192 offset:19456
	ds_read_b128 v[202:205], v192 offset:20480
	ds_read_b128 v[206:209], v192 offset:21504
	ds_read_b128 v[210:213], v192 offset:22528
	ds_read_b128 v[214:217], v192 offset:23552
	global_load_lds_dwordx4 v154, s[34:35]
	s_add_i32 m0, s61, 0x2000
	s_add_u32 s62, s34, 0x40000
	v_lshl_add_u64 v[220:221], s[34:35], 0, v[158:159]
	s_addc_u32 s63, s35, 0
	s_add_i32 s61, s56, s39
	global_load_lds_dwordx4 v158, s[34:35]
	s_mov_b32 m0, s61
	v_lshl_add_u64 v[224:225], s[36:37], 0, v[156:157]
	global_load_lds_dwordx4 v154, s[62:63]
	s_add_i32 m0, s61, 0x2000
	s_nop 0
	global_load_lds_dwordx4 v158, s[62:63]
	v_lshl_add_u64 v[222:223], s[36:37], 0, v[152:153]
	s_mov_b32 m0, s40
	s_nop 0
	global_load_lds_dwordx4 v152, s[36:37]
	s_mov_b32 m0, s41
	s_nop 0
	global_load_lds_dwordx4 v156, s[36:37]
	s_waitcnt vmcnt(8) lgkmcnt(0)
	s_barrier
	s_setprio 1
	v_mfma_f32_16x16x32_bf16 v[60:63], v[128:131], v[180:183], v[60:63]
	v_mfma_f32_16x16x32_bf16 v[56:59], v[136:139], v[180:183], v[56:59]
	v_mfma_f32_16x16x32_bf16 v[44:47], v[128:131], v[194:197], v[44:47]
	v_mfma_f32_16x16x32_bf16 v[40:43], v[136:139], v[194:197], v[40:43]
	v_mfma_f32_16x16x32_bf16 v[28:31], v[128:131], v[202:205], v[28:31]
	v_mfma_f32_16x16x32_bf16 v[24:27], v[136:139], v[202:205], v[24:27]
	v_mfma_f32_16x16x32_bf16 v[12:15], v[128:131], v[210:213], v[12:15]
	v_mfma_f32_16x16x32_bf16 v[8:11], v[136:139], v[210:213], v[8:11]
	v_mfma_f32_16x16x32_bf16 v[60:63], v[132:135], v[184:187], v[60:63]
	v_mfma_f32_16x16x32_bf16 v[56:59], v[140:143], v[184:187], v[56:59]
	v_mfma_f32_16x16x32_bf16 v[44:47], v[132:135], v[198:201], v[44:47]
	v_mfma_f32_16x16x32_bf16 v[40:43], v[140:143], v[198:201], v[40:43]
	v_mfma_f32_16x16x32_bf16 v[28:31], v[132:135], v[206:209], v[28:31]
	v_mfma_f32_16x16x32_bf16 v[24:27], v[140:143], v[206:209], v[24:27]
	v_mfma_f32_16x16x32_bf16 v[12:15], v[132:135], v[214:217], v[12:15]
	v_mfma_f32_16x16x32_bf16 v[8:11], v[140:143], v[214:217], v[8:11]
	v_mfma_f32_16x16x32_bf16 v[52:55], v[144:147], v[180:183], v[52:55]
	v_mfma_f32_16x16x32_bf16 v[48:51], v[172:175], v[180:183], v[48:51]
	v_mfma_f32_16x16x32_bf16 v[36:39], v[144:147], v[194:197], v[36:39]
	v_mfma_f32_16x16x32_bf16 v[32:35], v[172:175], v[194:197], v[32:35]
	v_mfma_f32_16x16x32_bf16 v[20:23], v[144:147], v[202:205], v[20:23]
	v_mfma_f32_16x16x32_bf16 v[16:19], v[172:175], v[202:205], v[16:19]
	v_mfma_f32_16x16x32_bf16 v[4:7], v[144:147], v[210:213], v[4:7]
	v_mfma_f32_16x16x32_bf16 v[0:3], v[172:175], v[210:213], v[0:3]
	v_mfma_f32_16x16x32_bf16 v[52:55], v[148:151], v[184:187], v[52:55]
	v_mfma_f32_16x16x32_bf16 v[48:51], v[176:179], v[184:187], v[48:51]
	v_mfma_f32_16x16x32_bf16 v[36:39], v[148:151], v[198:201], v[36:39]
	v_mfma_f32_16x16x32_bf16 v[32:35], v[176:179], v[198:201], v[32:35]
	v_mfma_f32_16x16x32_bf16 v[20:23], v[148:151], v[206:209], v[20:23]
	v_mfma_f32_16x16x32_bf16 v[16:19], v[176:179], v[206:209], v[16:19]
	v_mfma_f32_16x16x32_bf16 v[4:7], v[148:151], v[214:217], v[4:7]
	v_mfma_f32_16x16x32_bf16 v[0:3], v[176:179], v[214:217], v[0:3]
	s_setprio 0
	s_barrier
; #define PG8_STAGE(bufoff, gbase, voff) do { _Pragma("unroll") for (int _i = 0; _i < 2; ++_i) \
;         __builtin_amdgcn_global_load_lds((const unsigned*)((const char*)(gbase) + (voff)[_i]), (PG8_LAS unsigned*)(lds + (bufoff) + ldsw + _i * 8192), 16, 0, 0); } while (0)
; #define PG8_LDA(dst, b, h) do { _Pragma("unroll") for (int m = 0; m < 4; ++m) _Pragma("unroll") for (int k = 0; k < 2; ++k) dst[m][k] = *(const PG8_LAS bf16x8*)(lds + PG8_SA(b, h) + aoff + m * 2048 + k * 1024); } while (0)
; #define PG8_LDB(dst, b, h) do { _Pragma("unroll") for (int n = 0; n < 2; ++n) _Pragma("unroll") for (int k = 0; k < 2; ++k) dst[n][k] = *(const PG8_LAS bf16x8*)(lds + PG8_SB(b, h) + boff + n * 2048 + k * 1024); } while (0)
; #define PG8_MMA(ai, bj, At, Bt) do { __builtin_amdgcn_s_setprio(1); _Pragma("unroll") for (int m = 0; m < 4; ++m) _Pragma("unroll") for (int n = 0; n < 2; ++n) _Pragma("unroll") for (int k = 0; k < 2; ++k) \
;         acc[ai][bj][m][n] = __builtin_amdgcn_mfma_f32_16x16x32_bf16(Bt[n][k], At[m][k], acc[ai][bj][m][n], 0, 0, 0); __builtin_amdgcn_s_setprio(0); } while (0)
; #define PG8_WAIT_V(n) asm volatile("s_waitcnt vmcnt(" #n ")" ::: "memory")
; #define PG8_WAIT_L(n) asm volatile("s_waitcnt lgkmcnt(" #n ")" ::: "memory")
; #define PG8_BAR __builtin_amdgcn_s_barrier()
; #define PG8_SCHED __builtin_amdgcn_sched_barrier(0)
; template <class Epi, class Sched, bool ALIGN_EPI = false, bool SP2 = false>
; __device__ __forceinline__ void gemm_phase(PG8_LAS unsigned char* lds, const Gemm g, const Sched& S, const Epi& E, const int wid) {
;     ...
;             PG8_LDB(B0, 1, 0); PG8_LDB(B1, 1, 1); PG8_SCHED; PG8_LDA(At, 1, 0); PG8_STAGE(PG8_SA(0, 1), a2 + hstepA, voffA);
;             PG8_WAIT_V(8); PG8_WAIT_L(0); PG8_BAR; PG8_MMA(0, 0, At, B0); PG8_MMA(0, 1, At, B1); PG8_BAR; PG8_SCHED;
;             PG8_LDA(At, 1, 1); PG8_STAGE(PG8_SB(1, 0), b3, voffB); PG8_STAGE(PG8_SB(1, 1), b3 + hstepB, voffB); PG8_STAGE(PG8_SA(1, 0), a3, voffA);
;             PG8_WAIT_V(8); PG8_WAIT_L(0); PG8_BAR; PG8_MMA(1, 0, At, B0); PG8_MMA(1, 1, At, B1); PG8_BAR; PG8_SCHED;
;     ...
;         if constexpr (ALIGN_EPI) { if (wr == 0) PG8_BAR; }
	s_add_i32 s61, 0, 0x18000
	s_add_i32 s62, 0, 0x1c000
	v_add_u32_e32 v140, s61, v189
	v_add_u32_e32 v176, s62, v189
	ds_read_b128 v[128:131], v140
	ds_read_b128 v[132:135], v140 offset:1024
	ds_read_b128 v[136:139], v140 offset:2048
	ds_read_b128 v[140:143], v140 offset:3072
	ds_read_b128 v[144:147], v176
	ds_read_b128 v[148:151], v176 offset:1024
	ds_read_b128 v[172:175], v176 offset:2048
	ds_read_b128 v[176:179], v176 offset:3072
	s_add_u32 s36, s36, 0x40000
	s_addc_u32 s37, s37, 0
	s_mov_b32 m0, s42
	ds_read_b128 v[180:183], v192 offset:32768
	ds_read_b128 v[184:187], v192 offset:33792
	ds_read_b128 v[194:197], v192 offset:34816
	ds_read_b128 v[198:201], v192 offset:35840
	ds_read_b128 v[202:205], v192 offset:36864
	ds_read_b128 v[206:209], v192 offset:37888
	ds_read_b128 v[210:213], v192 offset:38912
	ds_read_b128 v[214:217], v192 offset:39936
	global_load_lds_dwordx4 v152, s[36:37]
	s_mov_b32 m0, s43
	s_nop 0
	global_load_lds_dwordx4 v156, s[36:37]
	s_waitcnt vmcnt(8) lgkmcnt(0)
	s_barrier
	s_setprio 1
	v_mfma_f32_16x16x32_bf16 v[124:127], v[128:131], v[180:183], v[124:127]
	v_mfma_f32_16x16x32_bf16 v[120:123], v[136:139], v[180:183], v[120:123]
	v_mfma_f32_16x16x32_bf16 v[108:111], v[128:131], v[194:197], v[108:111]
	v_mfma_f32_16x16x32_bf16 v[104:107], v[136:139], v[194:197], v[104:107]
	v_mfma_f32_16x16x32_bf16 v[92:95], v[128:131], v[202:205], v[92:95]
	v_mfma_f32_16x16x32_bf16 v[88:91], v[136:139], v[202:205], v[88:91]
	v_mfma_f32_16x16x32_bf16 v[76:79], v[128:131], v[210:213], v[76:79]
	v_mfma_f32_16x16x32_bf16 v[72:75], v[136:139], v[210:213], v[72:75]
	v_mfma_f32_16x16x32_bf16 v[124:127], v[132:135], v[184:187], v[124:127]
	v_mfma_f32_16x16x32_bf16 v[120:123], v[140:143], v[184:187], v[120:123]
	v_mfma_f32_16x16x32_bf16 v[108:111], v[132:135], v[198:201], v[108:111]
	v_mfma_f32_16x16x32_bf16 v[104:107], v[140:143], v[198:201], v[104:107]
	v_mfma_f32_16x16x32_bf16 v[92:95], v[132:135], v[206:209], v[92:95]
	v_mfma_f32_16x16x32_bf16 v[88:91], v[140:143], v[206:209], v[88:91]
	v_mfma_f32_16x16x32_bf16 v[76:79], v[132:135], v[214:217], v[76:79]
	v_mfma_f32_16x16x32_bf16 v[72:75], v[140:143], v[214:217], v[72:75]
	v_mfma_f32_16x16x32_bf16 v[116:119], v[144:147], v[180:183], v[116:119]
	v_mfma_f32_16x16x32_bf16 v[112:115], v[172:175], v[180:183], v[112:115]
	v_mfma_f32_16x16x32_bf16 v[100:103], v[144:147], v[194:197], v[100:103]
	v_mfma_f32_16x16x32_bf16 v[96:99], v[172:175], v[194:197], v[96:99]
	v_mfma_f32_16x16x32_bf16 v[84:87], v[144:147], v[202:205], v[84:87]
	v_mfma_f32_16x16x32_bf16 v[80:83], v[172:175], v[202:205], v[80:83]
	v_mfma_f32_16x16x32_bf16 v[68:71], v[144:147], v[210:213], v[68:71]
	v_mfma_f32_16x16x32_bf16 v[64:67], v[172:175], v[210:213], v[64:67]
	v_mfma_f32_16x16x32_bf16 v[116:119], v[148:151], v[184:187], v[116:119]
	v_mfma_f32_16x16x32_bf16 v[112:115], v[176:179], v[184:187], v[112:115]
	v_mfma_f32_16x16x32_bf16 v[100:103], v[148:151], v[198:201], v[100:103]
	v_mfma_f32_16x16x32_bf16 v[96:99], v[176:179], v[198:201], v[96:99]
	v_mfma_f32_16x16x32_bf16 v[84:87], v[148:151], v[206:209], v[84:87]
	v_mfma_f32_16x16x32_bf16 v[80:83], v[176:179], v[206:209], v[80:83]
	v_mfma_f32_16x16x32_bf16 v[68:71], v[148:151], v[214:217], v[68:71]
	v_mfma_f32_16x16x32_bf16 v[64:67], v[176:179], v[214:217], v[64:67]
	s_setprio 0
	s_barrier
	s_add_i32 s36, s61, s39
	v_lshl_add_u64 v[218:219], v[218:219], 0, s[14:15]
	s_mov_b32 m0, s36
	ds_read_b128 v[180:183], v192 offset:49152
	ds_read_b128 v[184:187], v192 offset:50176
	ds_read_b128 v[194:197], v192 offset:51200
	ds_read_b128 v[198:201], v192 offset:52224
	ds_read_b128 v[202:205], v192 offset:53248
	ds_read_b128 v[206:209], v192 offset:54272
	ds_read_b128 v[210:213], v192 offset:55296
	ds_read_b128 v[214:217], v192 offset:56320
	global_load_lds_dwordx4 v[218:219], off
	s_add_i32 m0, s36, 0x2000
	s_add_u32 s34, s34, 0x40080
	v_lshl_add_u64 v[218:219], v[220:221], 0, s[14:15]
	s_addc_u32 s35, s35, 0
	s_add_i32 s36, s62, s39
	global_load_lds_dwordx4 v[218:219], off
	s_mov_b32 m0, s36
	s_nop 0
	global_load_lds_dwordx4 v154, s[34:35]
	v_lshl_add_u64 v[218:219], s[34:35], 0, v[158:159]
	s_add_i32 m0, s36, 0x2000
	s_nop 0
	global_load_lds_dwordx4 v158, s[34:35]
	v_lshl_add_u64 v[218:219], v[222:223], 0, s[14:15]
	s_mov_b32 m0, s45
	s_nop 0
	global_load_lds_dwordx4 v[218:219], off
	v_lshl_add_u64 v[218:219], v[224:225], 0, s[14:15]
	s_mov_b32 m0, s46
	s_nop 0
	global_load_lds_dwordx4 v[218:219], off
	s_waitcnt vmcnt(8) lgkmcnt(0)
	s_barrier
	s_setprio 1
	v_mfma_f32_16x16x32_bf16 v[60:63], v[128:131], v[180:183], v[60:63]
	v_mfma_f32_16x16x32_bf16 v[56:59], v[136:139], v[180:183], v[56:59]
	v_mfma_f32_16x16x32_bf16 v[44:47], v[128:131], v[194:197], v[44:47]
	v_mfma_f32_16x16x32_bf16 v[40:43], v[136:139], v[194:197], v[40:43]
	v_mfma_f32_16x16x32_bf16 v[28:31], v[128:131], v[202:205], v[28:31]
	v_mfma_f32_16x16x32_bf16 v[24:27], v[136:139], v[202:205], v[24:27]
	v_mfma_f32_16x16x32_bf16 v[12:15], v[128:131], v[210:213], v[12:15]
	v_mfma_f32_16x16x32_bf16 v[8:11], v[136:139], v[210:213], v[8:11]
	v_mfma_f32_16x16x32_bf16 v[60:63], v[132:135], v[184:187], v[60:63]
	v_mfma_f32_16x16x32_bf16 v[56:59], v[140:143], v[184:187], v[56:59]
	v_mfma_f32_16x16x32_bf16 v[44:47], v[132:135], v[198:201], v[44:47]
	v_mfma_f32_16x16x32_bf16 v[40:43], v[140:143], v[198:201], v[40:43]
	v_mfma_f32_16x16x32_bf16 v[28:31], v[132:135], v[206:209], v[28:31]
	v_mfma_f32_16x16x32_bf16 v[24:27], v[140:143], v[206:209], v[24:27]
	v_mfma_f32_16x16x32_bf16 v[12:15], v[132:135], v[214:217], v[12:15]
	v_mfma_f32_16x16x32_bf16 v[8:11], v[140:143], v[214:217], v[8:11]
	v_mfma_f32_16x16x32_bf16 v[52:55], v[144:147], v[180:183], v[52:55]
	v_mfma_f32_16x16x32_bf16 v[48:51], v[172:175], v[180:183], v[48:51]
	v_mfma_f32_16x16x32_bf16 v[36:39], v[144:147], v[194:197], v[36:39]
	v_mfma_f32_16x16x32_bf16 v[32:35], v[172:175], v[194:197], v[32:35]
	v_mfma_f32_16x16x32_bf16 v[20:23], v[144:147], v[202:205], v[20:23]
	v_mfma_f32_16x16x32_bf16 v[16:19], v[172:175], v[202:205], v[16:19]
	v_mfma_f32_16x16x32_bf16 v[4:7], v[144:147], v[210:213], v[4:7]
	v_mfma_f32_16x16x32_bf16 v[0:3], v[172:175], v[210:213], v[0:3]
	v_mfma_f32_16x16x32_bf16 v[52:55], v[148:151], v[184:187], v[52:55]
	v_mfma_f32_16x16x32_bf16 v[48:51], v[176:179], v[184:187], v[48:51]
	v_mfma_f32_16x16x32_bf16 v[36:39], v[148:151], v[198:201], v[36:39]
	v_mfma_f32_16x16x32_bf16 v[32:35], v[176:179], v[198:201], v[32:35]
	v_mfma_f32_16x16x32_bf16 v[20:23], v[148:151], v[206:209], v[20:23]
	v_mfma_f32_16x16x32_bf16 v[16:19], v[176:179], v[206:209], v[16:19]
	v_mfma_f32_16x16x32_bf16 v[4:7], v[148:151], v[214:217], v[4:7]
	v_mfma_f32_16x16x32_bf16 v[0:3], v[176:179], v[214:217], v[0:3]
	s_setprio 0
	s_barrier
	s_add_i32 s60, s60, 2
	s_add_u32 s30, s30, 0x100
	s_addc_u32 s31, s31, 0
	s_add_u32 s58, s58, 0x100
	s_addc_u32 s59, s59, 0
	s_cmp_gt_u32 s60, 13
	s_cbranch_scc0 .LBB0_2725
	s_and_b64 vcc, exec, s[16:17]
	s_cbranch_vccz .LBB0_2728
	s_barrier

; #define PG8_STAGE(bufoff, gbase, voff) do { _Pragma("unroll") for (int _i = 0; _i < 2; ++_i) \
;         __builtin_amdgcn_global_load_lds((const unsigned*)((const char*)(gbase) + (voff)[_i]), (PG8_LAS unsigned*)(lds + (bufoff) + ldsw + _i * 8192), 16, 0, 0); } while (0)
; #define PG8_LDA(dst, b, h) do { _Pragma("unroll") for (int m = 0; m < 4; ++m) _Pragma("unroll") for (int k = 0; k < 2; ++k) dst[m][k] = *(const PG8_LAS bf16x8*)(lds + PG8_SA(b, h) + aoff + m * 2048 + k * 1024); } while (0)
; #define PG8_LDB(dst, b, h) do { _Pragma("unroll") for (int n = 0; n < 2; ++n) _Pragma("unroll") for (int k = 0; k < 2; ++k) dst[n][k] = *(const PG8_LAS bf16x8*)(lds + PG8_SB(b, h) + boff + n * 2048 + k * 1024); } while (0)
; #define PG8_MMA(ai, bj, At, Bt) do { __builtin_amdgcn_s_setprio(1); _Pragma("unroll") for (int m = 0; m < 4; ++m) _Pragma("unroll") for (int n = 0; n < 2; ++n) _Pragma("unroll") for (int k = 0; k < 2; ++k) \
;         acc[ai][bj][m][n] = __builtin_amdgcn_mfma_f32_16x16x32_bf16(Bt[n][k], At[m][k], acc[ai][bj][m][n], 0, 0, 0); __builtin_amdgcn_s_setprio(0); } while (0)
; #define PG8_WAIT_V(n) asm volatile("s_waitcnt vmcnt(" #n ")" ::: "memory")
; #define PG8_WAIT_L(n) asm volatile("s_waitcnt lgkmcnt(" #n ")" ::: "memory")
; template <class Epi, class Sched, bool ALIGN_EPI = false, bool SP2 = false>
; __device__ __forceinline__ void gemm_phase(PG8_LAS unsigned char* lds, const Gemm g, const Sched& S, const Epi& E, const int wid) {
;     ...
;             const bool last = (t == nt - 2);
;             const char* a1 = cA + (size_t)(t + 1) * kstep;
;             const char* a2 = last ? nA : cA + (size_t)(t + 2) * kstep; const char* b2 = last ? nB : cB + (size_t)(t + 2) * kstep;
;             const char* a3 = a2 + kstep; const char* b3 = b2 + kstep;
;             if (last && has_next) S.a_ready(nxt);
;             if constexpr (SP2) {
;             PG8_LDB(B0, 0, 0); PG8_LDB(B1, 0, 1); PG8_SCHED; PG8_LDA(At, 0, 0); PG8_STAGE(PG8_SA(1, 1), a1 + hstepA, voffA);
;             PG8_WAIT_V(8); PG8_WAIT_L(0); PG8_BAR; PG8_MMA(0, 0, At, B0); PG8_MMA(0, 1, At, B1); PG8_BAR; PG8_SCHED;
;             PG8_LDA(At, 0, 1); PG8_STAGE(PG8_SB(0, 0), b2, voffB); PG8_STAGE(PG8_SB(0, 1), b2 + hstepB, voffB); PG8_STAGE(PG8_SA(0, 0), a2, voffA);
;             PG8_WAIT_V(8); PG8_WAIT_L(0); PG8_BAR; PG8_MMA(1, 0, At, B0); PG8_MMA(1, 1, At, B1); PG8_BAR; PG8_SCHED;
.LBB0_2812:
	ds_read_b128 v[148:151], v166
	ds_read_b128 v[152:155], v166 offset:1024
	ds_read_b128 v[156:159], v166 offset:2048
	ds_read_b128 v[160:163], v166 offset:3072
	ds_read_b128 v[172:175], v167
	ds_read_b128 v[176:179], v167 offset:1024
	ds_read_b128 v[180:183], v167 offset:2048
	ds_read_b128 v[184:187], v167 offset:3072
	s_add_u32 s26, s24, 0xfffc0080
	s_addc_u32 s27, s25, -1
	s_cmp_eq_u32 s57, 12
	s_cselect_b32 s29, s17, s27
	s_cselect_b32 s28, s47, s26
	s_cselect_b32 s27, s15, s56
	s_cselect_b32 s26, s48, s49
	s_add_i32 m0, s36, 0xc000
	ds_read_b128 v[188:191], v168
	ds_read_b128 v[192:195], v168 offset:1024
	ds_read_b128 v[196:199], v168 offset:2048
	ds_read_b128 v[200:203], v168 offset:3072
	ds_read_b128 v[204:207], v168 offset:4096
	ds_read_b128 v[208:211], v168 offset:5120
	ds_read_b128 v[212:215], v168 offset:6144
	ds_read_b128 v[216:219], v168 offset:7168
	global_load_lds_dwordx4 v140, s[24:25]
	s_add_i32 m0, s36, 0xe000
	s_nop 0
	global_load_lds_dwordx4 v142, s[24:25]
	s_waitcnt vmcnt(8) lgkmcnt(0)
	s_barrier
	s_setprio 1
	v_mfma_f32_16x16x32_bf16 v[124:127], v[148:151], v[188:191], v[124:127]
	v_mfma_f32_16x16x32_bf16 v[116:119], v[156:159], v[188:191], v[116:119]
	v_mfma_f32_16x16x32_bf16 v[108:111], v[148:151], v[196:199], v[108:111]
	v_mfma_f32_16x16x32_bf16 v[100:103], v[156:159], v[196:199], v[100:103]
	v_mfma_f32_16x16x32_bf16 v[92:95], v[148:151], v[204:207], v[92:95]
	v_mfma_f32_16x16x32_bf16 v[84:87], v[156:159], v[204:207], v[84:87]
	v_mfma_f32_16x16x32_bf16 v[76:79], v[148:151], v[212:215], v[76:79]
	v_mfma_f32_16x16x32_bf16 v[68:71], v[156:159], v[212:215], v[68:71]
	v_mfma_f32_16x16x32_bf16 v[124:127], v[152:155], v[192:195], v[124:127]
	v_mfma_f32_16x16x32_bf16 v[116:119], v[160:163], v[192:195], v[116:119]
	v_mfma_f32_16x16x32_bf16 v[108:111], v[152:155], v[200:203], v[108:111]
	v_mfma_f32_16x16x32_bf16 v[100:103], v[160:163], v[200:203], v[100:103]
	v_mfma_f32_16x16x32_bf16 v[92:95], v[152:155], v[208:211], v[92:95]
	v_mfma_f32_16x16x32_bf16 v[84:87], v[160:163], v[208:211], v[84:87]
	v_mfma_f32_16x16x32_bf16 v[76:79], v[152:155], v[216:219], v[76:79]
	v_mfma_f32_16x16x32_bf16 v[68:71], v[160:163], v[216:219], v[68:71]
	v_mfma_f32_16x16x32_bf16 v[120:123], v[172:175], v[188:191], v[120:123]
	v_mfma_f32_16x16x32_bf16 v[112:115], v[180:183], v[188:191], v[112:115]
	v_mfma_f32_16x16x32_bf16 v[104:107], v[172:175], v[196:199], v[104:107]
	v_mfma_f32_16x16x32_bf16 v[96:99], v[180:183], v[196:199], v[96:99]
	v_mfma_f32_16x16x32_bf16 v[88:91], v[172:175], v[204:207], v[88:91]
	v_mfma_f32_16x16x32_bf16 v[80:83], v[180:183], v[204:207], v[80:83]
	v_mfma_f32_16x16x32_bf16 v[72:75], v[172:175], v[212:215], v[72:75]
	v_mfma_f32_16x16x32_bf16 v[64:67], v[180:183], v[212:215], v[64:67]
	v_mfma_f32_16x16x32_bf16 v[120:123], v[176:179], v[192:195], v[120:123]
	v_mfma_f32_16x16x32_bf16 v[112:115], v[184:187], v[192:195], v[112:115]
	v_mfma_f32_16x16x32_bf16 v[104:107], v[176:179], v[200:203], v[104:107]
	v_mfma_f32_16x16x32_bf16 v[96:99], v[184:187], v[200:203], v[96:99]
	v_mfma_f32_16x16x32_bf16 v[88:91], v[176:179], v[208:211], v[88:91]
	v_mfma_f32_16x16x32_bf16 v[80:83], v[184:187], v[208:211], v[80:83]
	v_mfma_f32_16x16x32_bf16 v[72:75], v[176:179], v[216:219], v[72:75]
	v_mfma_f32_16x16x32_bf16 v[64:67], v[184:187], v[216:219], v[64:67]
	s_setprio 0
	s_barrier
	s_add_i32 s58, s43, s33
	v_lshl_add_u64 v[220:221], s[26:27], 0, v[132:133]
	s_mov_b32 m0, s58
	ds_read_b128 v[188:191], v168 offset:16384
	ds_read_b128 v[192:195], v168 offset:17408
	ds_read_b128 v[196:199], v168 offset:18432
	ds_read_b128 v[200:203], v168 offset:19456
	ds_read_b128 v[204:207], v168 offset:20480
	ds_read_b128 v[208:211], v168 offset:21504
	ds_read_b128 v[212:215], v168 offset:22528
	ds_read_b128 v[216:219], v168 offset:23552
	global_load_lds_dwordx4 v132, s[26:27]
	s_add_i32 m0, s58, 0x2000
	s_add_u32 s58, s26, 0x40000
	v_lshl_add_u64 v[222:223], s[26:27], 0, v[128:129]
	s_addc_u32 s59, s27, 0
	s_add_i32 s60, s44, s33
	global_load_lds_dwordx4 v128, s[26:27]
	s_mov_b32 m0, s60
	v_lshl_add_u64 v[226:227], s[28:29], 0, v[130:131]
	global_load_lds_dwordx4 v132, s[58:59]
	s_add_i32 m0, s60, 0x2000
	s_nop 0
	global_load_lds_dwordx4 v128, s[58:59]
	v_lshl_add_u64 v[224:225], s[28:29], 0, v[134:135]
	s_mov_b32 m0, s36
	s_nop 0
	global_load_lds_dwordx4 v134, s[28:29]
	s_mov_b32 m0, s37
	s_nop 0
	global_load_lds_dwordx4 v130, s[28:29]
	s_waitcnt vmcnt(8) lgkmcnt(0)
	s_barrier
	s_setprio 1
	v_mfma_f32_16x16x32_bf16 v[60:63], v[148:151], v[188:191], v[60:63]
	v_mfma_f32_16x16x32_bf16 v[52:55], v[156:159], v[188:191], v[52:55]
	v_mfma_f32_16x16x32_bf16 v[44:47], v[148:151], v[196:199], v[44:47]
	v_mfma_f32_16x16x32_bf16 v[36:39], v[156:159], v[196:199], v[36:39]
	v_mfma_f32_16x16x32_bf16 v[28:31], v[148:151], v[204:207], v[28:31]
	v_mfma_f32_16x16x32_bf16 v[20:23], v[156:159], v[204:207], v[20:23]
	v_mfma_f32_16x16x32_bf16 v[12:15], v[148:151], v[212:215], v[12:15]
	v_mfma_f32_16x16x32_bf16 v[4:7], v[156:159], v[212:215], v[4:7]
	v_mfma_f32_16x16x32_bf16 v[60:63], v[152:155], v[192:195], v[60:63]
	v_mfma_f32_16x16x32_bf16 v[52:55], v[160:163], v[192:195], v[52:55]
	v_mfma_f32_16x16x32_bf16 v[44:47], v[152:155], v[200:203], v[44:47]
	v_mfma_f32_16x16x32_bf16 v[36:39], v[160:163], v[200:203], v[36:39]
	v_mfma_f32_16x16x32_bf16 v[28:31], v[152:155], v[208:211], v[28:31]
	v_mfma_f32_16x16x32_bf16 v[20:23], v[160:163], v[208:211], v[20:23]
	v_mfma_f32_16x16x32_bf16 v[12:15], v[152:155], v[216:219], v[12:15]
	v_mfma_f32_16x16x32_bf16 v[4:7], v[160:163], v[216:219], v[4:7]
	v_mfma_f32_16x16x32_bf16 v[56:59], v[172:175], v[188:191], v[56:59]
	v_mfma_f32_16x16x32_bf16 v[48:51], v[180:183], v[188:191], v[48:51]
	v_mfma_f32_16x16x32_bf16 v[40:43], v[172:175], v[196:199], v[40:43]
	v_mfma_f32_16x16x32_bf16 v[32:35], v[180:183], v[196:199], v[32:35]
	v_mfma_f32_16x16x32_bf16 v[24:27], v[172:175], v[204:207], v[24:27]
	v_mfma_f32_16x16x32_bf16 v[16:19], v[180:183], v[204:207], v[16:19]
	v_mfma_f32_16x16x32_bf16 v[8:11], v[172:175], v[212:215], v[8:11]
	v_mfma_f32_16x16x32_bf16 v[0:3], v[180:183], v[212:215], v[0:3]
	v_mfma_f32_16x16x32_bf16 v[56:59], v[176:179], v[192:195], v[56:59]
	v_mfma_f32_16x16x32_bf16 v[48:51], v[184:187], v[192:195], v[48:51]
	v_mfma_f32_16x16x32_bf16 v[40:43], v[176:179], v[200:203], v[40:43]
	v_mfma_f32_16x16x32_bf16 v[32:35], v[184:187], v[200:203], v[32:35]
	v_mfma_f32_16x16x32_bf16 v[24:27], v[176:179], v[208:211], v[24:27]
	v_mfma_f32_16x16x32_bf16 v[16:19], v[184:187], v[208:211], v[16:19]
	v_mfma_f32_16x16x32_bf16 v[8:11], v[176:179], v[216:219], v[8:11]
	v_mfma_f32_16x16x32_bf16 v[0:3], v[184:187], v[216:219], v[0:3]
	s_setprio 0
	s_barrier
; #define PG8_STAGE(bufoff, gbase, voff) do { _Pragma("unroll") for (int _i = 0; _i < 2; ++_i) \
;         __builtin_amdgcn_global_load_lds((const unsigned*)((const char*)(gbase) + (voff)[_i]), (PG8_LAS unsigned*)(lds + (bufoff) + ldsw + _i * 8192), 16, 0, 0); } while (0)
; #define PG8_LDA(dst, b, h) do { _Pragma("unroll") for (int m = 0; m < 4; ++m) _Pragma("unroll") for (int k = 0; k < 2; ++k) dst[m][k] = *(const PG8_LAS bf16x8*)(lds + PG8_SA(b, h) + aoff + m * 2048 + k * 1024); } while (0)
; #define PG8_LDB(dst, b, h) do { _Pragma("unroll") for (int n = 0; n < 2; ++n) _Pragma("unroll") for (int k = 0; k < 2; ++k) dst[n][k] = *(const PG8_LAS bf16x8*)(lds + PG8_SB(b, h) + boff + n * 2048 + k * 1024); } while (0)
; #define PG8_MMA(ai, bj, At, Bt) do { __builtin_amdgcn_s_setprio(1); _Pragma("unroll") for (int m = 0; m < 4; ++m) _Pragma("unroll") for (int n = 0; n < 2; ++n) _Pragma("unroll") for (int k = 0; k < 2; ++k) \
;         acc[ai][bj][m][n] = __builtin_amdgcn_mfma_f32_16x16x32_bf16(Bt[n][k], At[m][k], acc[ai][bj][m][n], 0, 0, 0); __builtin_amdgcn_s_setprio(0); } while (0)
; #define PG8_WAIT_V(n) asm volatile("s_waitcnt vmcnt(" #n ")" ::: "memory")
; #define PG8_WAIT_L(n) asm volatile("s_waitcnt lgkmcnt(" #n ")" ::: "memory")
; #define PG8_BAR __builtin_amdgcn_s_barrier()
; #define PG8_SCHED __builtin_amdgcn_sched_barrier(0)
; template <class Epi, class Sched, bool ALIGN_EPI = false, bool SP2 = false>
; __device__ __forceinline__ void gemm_phase(PG8_LAS unsigned char* lds, const Gemm g, const Sched& S, const Epi& E, const int wid) {
;     ...
;             PG8_LDB(B0, 1, 0); PG8_LDB(B1, 1, 1); PG8_SCHED; PG8_LDA(At, 1, 0); PG8_STAGE(PG8_SA(0, 1), a2 + hstepA, voffA);
;             PG8_WAIT_V(8); PG8_WAIT_L(0); PG8_BAR; PG8_MMA(0, 0, At, B0); PG8_MMA(0, 1, At, B1); PG8_BAR; PG8_SCHED;
;             PG8_LDA(At, 1, 1); PG8_STAGE(PG8_SB(1, 0), b3, voffB); PG8_STAGE(PG8_SB(1, 1), b3 + hstepB, voffB); PG8_STAGE(PG8_SA(1, 0), a3, voffA);
;             PG8_WAIT_V(8); PG8_WAIT_L(0); PG8_BAR; PG8_MMA(1, 0, At, B0); PG8_MMA(1, 1, At, B1); PG8_BAR; PG8_SCHED;
;     ...
;         if constexpr (ALIGN_EPI) { if (wr == 0) PG8_BAR; }
	s_add_i32 s58, 0, 0x18000
	s_add_i32 s59, 0, 0x1c000
	v_add_u32_e32 v160, s58, v165
	v_add_u32_e32 v171, s59, v165
	ds_read_b128 v[148:151], v160
	ds_read_b128 v[152:155], v160 offset:1024
	ds_read_b128 v[156:159], v160 offset:2048
	ds_read_b128 v[160:163], v160 offset:3072
	ds_read_b128 v[172:175], v171
	ds_read_b128 v[176:179], v171 offset:1024
	ds_read_b128 v[180:183], v171 offset:2048
	ds_read_b128 v[184:187], v171 offset:3072
	s_add_u32 s28, s28, 0x40000
	s_addc_u32 s29, s29, 0
	s_mov_b32 m0, s38
	ds_read_b128 v[188:191], v168 offset:32768
	ds_read_b128 v[192:195], v168 offset:33792
	ds_read_b128 v[196:199], v168 offset:34816
	ds_read_b128 v[200:203], v168 offset:35840
	ds_read_b128 v[204:207], v168 offset:36864
	ds_read_b128 v[208:211], v168 offset:37888
	ds_read_b128 v[212:215], v168 offset:38912
	ds_read_b128 v[216:219], v168 offset:39936
	global_load_lds_dwordx4 v134, s[28:29]
	s_mov_b32 m0, s39
	s_nop 0
	global_load_lds_dwordx4 v130, s[28:29]
	s_waitcnt vmcnt(8) lgkmcnt(0)
	s_barrier
	s_setprio 1
	v_mfma_f32_16x16x32_bf16 v[124:127], v[148:151], v[188:191], v[124:127]
	v_mfma_f32_16x16x32_bf16 v[116:119], v[156:159], v[188:191], v[116:119]
	v_mfma_f32_16x16x32_bf16 v[108:111], v[148:151], v[196:199], v[108:111]
	v_mfma_f32_16x16x32_bf16 v[100:103], v[156:159], v[196:199], v[100:103]
	v_mfma_f32_16x16x32_bf16 v[92:95], v[148:151], v[204:207], v[92:95]
	v_mfma_f32_16x16x32_bf16 v[84:87], v[156:159], v[204:207], v[84:87]
	v_mfma_f32_16x16x32_bf16 v[76:79], v[148:151], v[212:215], v[76:79]
	v_mfma_f32_16x16x32_bf16 v[68:71], v[156:159], v[212:215], v[68:71]
	v_mfma_f32_16x16x32_bf16 v[124:127], v[152:155], v[192:195], v[124:127]
	v_mfma_f32_16x16x32_bf16 v[116:119], v[160:163], v[192:195], v[116:119]
	v_mfma_f32_16x16x32_bf16 v[108:111], v[152:155], v[200:203], v[108:111]
	v_mfma_f32_16x16x32_bf16 v[100:103], v[160:163], v[200:203], v[100:103]
	v_mfma_f32_16x16x32_bf16 v[92:95], v[152:155], v[208:211], v[92:95]
	v_mfma_f32_16x16x32_bf16 v[84:87], v[160:163], v[208:211], v[84:87]
	v_mfma_f32_16x16x32_bf16 v[76:79], v[152:155], v[216:219], v[76:79]
	v_mfma_f32_16x16x32_bf16 v[68:71], v[160:163], v[216:219], v[68:71]
	v_mfma_f32_16x16x32_bf16 v[120:123], v[172:175], v[188:191], v[120:123]
	v_mfma_f32_16x16x32_bf16 v[112:115], v[180:183], v[188:191], v[112:115]
	v_mfma_f32_16x16x32_bf16 v[104:107], v[172:175], v[196:199], v[104:107]
	v_mfma_f32_16x16x32_bf16 v[96:99], v[180:183], v[196:199], v[96:99]
	v_mfma_f32_16x16x32_bf16 v[88:91], v[172:175], v[204:207], v[88:91]
	v_mfma_f32_16x16x32_bf16 v[80:83], v[180:183], v[204:207], v[80:83]
	v_mfma_f32_16x16x32_bf16 v[72:75], v[172:175], v[212:215], v[72:75]
	v_mfma_f32_16x16x32_bf16 v[64:67], v[180:183], v[212:215], v[64:67]
	v_mfma_f32_16x16x32_bf16 v[120:123], v[176:179], v[192:195], v[120:123]
	v_mfma_f32_16x16x32_bf16 v[112:115], v[184:187], v[192:195], v[112:115]
	v_mfma_f32_16x16x32_bf16 v[104:107], v[176:179], v[200:203], v[104:107]
	v_mfma_f32_16x16x32_bf16 v[96:99], v[184:187], v[200:203], v[96:99]
	v_mfma_f32_16x16x32_bf16 v[88:91], v[176:179], v[208:211], v[88:91]
	v_mfma_f32_16x16x32_bf16 v[80:83], v[184:187], v[208:211], v[80:83]
	v_mfma_f32_16x16x32_bf16 v[72:75], v[176:179], v[216:219], v[72:75]
	v_mfma_f32_16x16x32_bf16 v[64:67], v[184:187], v[216:219], v[64:67]
	s_setprio 0
	s_barrier
	s_add_i32 s28, s58, s33
	v_lshl_add_u64 v[220:221], v[220:221], 0, s[10:11]
	s_mov_b32 m0, s28
	ds_read_b128 v[188:191], v168 offset:49152
	ds_read_b128 v[192:195], v168 offset:50176
	ds_read_b128 v[196:199], v168 offset:51200
	ds_read_b128 v[200:203], v168 offset:52224
	ds_read_b128 v[204:207], v168 offset:53248
	ds_read_b128 v[208:211], v168 offset:54272
	ds_read_b128 v[212:215], v168 offset:55296
	ds_read_b128 v[216:219], v168 offset:56320
	global_load_lds_dwordx4 v[220:221], off
	s_add_i32 m0, s28, 0x2000
	s_add_u32 s26, s26, 0x40080
	v_lshl_add_u64 v[220:221], v[222:223], 0, s[10:11]
	s_addc_u32 s27, s27, 0
	s_add_i32 s28, s59, s33
	global_load_lds_dwordx4 v[220:221], off
	s_mov_b32 m0, s28
	s_nop 0
	global_load_lds_dwordx4 v132, s[26:27]
	v_lshl_add_u64 v[220:221], s[26:27], 0, v[128:129]
	s_add_i32 m0, s28, 0x2000
	s_nop 0
	global_load_lds_dwordx4 v128, s[26:27]
	v_lshl_add_u64 v[220:221], v[224:225], 0, s[10:11]
	s_mov_b32 m0, s40
	s_nop 0
	global_load_lds_dwordx4 v[220:221], off
	v_lshl_add_u64 v[220:221], v[226:227], 0, s[10:11]
	s_mov_b32 m0, s41
	s_nop 0
	global_load_lds_dwordx4 v[220:221], off
	s_waitcnt vmcnt(8) lgkmcnt(0)
	s_barrier
	s_setprio 1
	v_mfma_f32_16x16x32_bf16 v[60:63], v[148:151], v[188:191], v[60:63]
	v_mfma_f32_16x16x32_bf16 v[52:55], v[156:159], v[188:191], v[52:55]
	v_mfma_f32_16x16x32_bf16 v[44:47], v[148:151], v[196:199], v[44:47]
	v_mfma_f32_16x16x32_bf16 v[36:39], v[156:159], v[196:199], v[36:39]
	v_mfma_f32_16x16x32_bf16 v[28:31], v[148:151], v[204:207], v[28:31]
	v_mfma_f32_16x16x32_bf16 v[20:23], v[156:159], v[204:207], v[20:23]
	v_mfma_f32_16x16x32_bf16 v[12:15], v[148:151], v[212:215], v[12:15]
	v_mfma_f32_16x16x32_bf16 v[4:7], v[156:159], v[212:215], v[4:7]
	v_mfma_f32_16x16x32_bf16 v[60:63], v[152:155], v[192:195], v[60:63]
	v_mfma_f32_16x16x32_bf16 v[52:55], v[160:163], v[192:195], v[52:55]
	v_mfma_f32_16x16x32_bf16 v[44:47], v[152:155], v[200:203], v[44:47]
	v_mfma_f32_16x16x32_bf16 v[36:39], v[160:163], v[200:203], v[36:39]
	v_mfma_f32_16x16x32_bf16 v[28:31], v[152:155], v[208:211], v[28:31]
	v_mfma_f32_16x16x32_bf16 v[20:23], v[160:163], v[208:211], v[20:23]
	v_mfma_f32_16x16x32_bf16 v[12:15], v[152:155], v[216:219], v[12:15]
	v_mfma_f32_16x16x32_bf16 v[4:7], v[160:163], v[216:219], v[4:7]
	v_mfma_f32_16x16x32_bf16 v[56:59], v[172:175], v[188:191], v[56:59]
	v_mfma_f32_16x16x32_bf16 v[48:51], v[180:183], v[188:191], v[48:51]
	v_mfma_f32_16x16x32_bf16 v[40:43], v[172:175], v[196:199], v[40:43]
	v_mfma_f32_16x16x32_bf16 v[32:35], v[180:183], v[196:199], v[32:35]
	v_mfma_f32_16x16x32_bf16 v[24:27], v[172:175], v[204:207], v[24:27]
	v_mfma_f32_16x16x32_bf16 v[16:19], v[180:183], v[204:207], v[16:19]
	v_mfma_f32_16x16x32_bf16 v[8:11], v[172:175], v[212:215], v[8:11]
	v_mfma_f32_16x16x32_bf16 v[0:3], v[180:183], v[212:215], v[0:3]
	v_mfma_f32_16x16x32_bf16 v[56:59], v[176:179], v[192:195], v[56:59]
	v_mfma_f32_16x16x32_bf16 v[48:51], v[184:187], v[192:195], v[48:51]
	v_mfma_f32_16x16x32_bf16 v[40:43], v[176:179], v[200:203], v[40:43]
	v_mfma_f32_16x16x32_bf16 v[32:35], v[184:187], v[200:203], v[32:35]
	v_mfma_f32_16x16x32_bf16 v[24:27], v[176:179], v[208:211], v[24:27]
	v_mfma_f32_16x16x32_bf16 v[16:19], v[184:187], v[208:211], v[16:19]
	v_mfma_f32_16x16x32_bf16 v[8:11], v[176:179], v[216:219], v[8:11]
	v_mfma_f32_16x16x32_bf16 v[0:3], v[184:187], v[216:219], v[0:3]
	s_setprio 0
	s_barrier
	s_add_i32 s57, s57, 2
	s_add_u32 s24, s24, 0x100
	s_addc_u32 s25, s25, 0
	s_add_u32 s49, s49, 0x100
	s_addc_u32 s56, s56, 0
	s_cmp_gt_u32 s57, 13
	s_cbranch_scc0 .LBB0_2812
	s_and_b64 vcc, exec, s[12:13]
	s_cbranch_vccz .LBB0_2815
	s_barrier

; #define PG8_STAGE(bufoff, gbase, voff) do { _Pragma("unroll") for (int _i = 0; _i < 2; ++_i) \
;         __builtin_amdgcn_global_load_lds((const unsigned*)((const char*)(gbase) + (voff)[_i]), (PG8_LAS unsigned*)(lds + (bufoff) + ldsw + _i * 8192), 16, 0, 0); } while (0)
; #define PG8_LDA(dst, b, h) do { _Pragma("unroll") for (int m = 0; m < 4; ++m) _Pragma("unroll") for (int k = 0; k < 2; ++k) dst[m][k] = *(const PG8_LAS bf16x8*)(lds + PG8_SA(b, h) + aoff + m * 2048 + k * 1024); } while (0)
; #define PG8_LDB(dst, b, h) do { _Pragma("unroll") for (int n = 0; n < 2; ++n) _Pragma("unroll") for (int k = 0; k < 2; ++k) dst[n][k] = *(const PG8_LAS bf16x8*)(lds + PG8_SB(b, h) + boff + n * 2048 + k * 1024); } while (0)
; #define PG8_MMA(ai, bj, At, Bt) do { __builtin_amdgcn_s_setprio(1); _Pragma("unroll") for (int m = 0; m < 4; ++m) _Pragma("unroll") for (int n = 0; n < 2; ++n) _Pragma("unroll") for (int k = 0; k < 2; ++k) \
;         acc[ai][bj][m][n] = __builtin_amdgcn_mfma_f32_16x16x32_bf16(Bt[n][k], At[m][k], acc[ai][bj][m][n], 0, 0, 0); __builtin_amdgcn_s_setprio(0); } while (0)
; #define PG8_WAIT_V(n) asm volatile("s_waitcnt vmcnt(" #n ")" ::: "memory")
; #define PG8_WAIT_L(n) asm volatile("s_waitcnt lgkmcnt(" #n ")" ::: "memory")
; template <class Epi, class Sched, bool ALIGN_EPI = false, bool SP2 = false>
; __device__ __forceinline__ void gemm_phase(PG8_LAS unsigned char* lds, const Gemm g, const Sched& S, const Epi& E, const int wid) {
;     ...
;             const bool last = (t == nt - 2);
;             const char* a1 = cA + (size_t)(t + 1) * kstep;
;             const char* a2 = last ? nA : cA + (size_t)(t + 2) * kstep; const char* b2 = last ? nB : cB + (size_t)(t + 2) * kstep;
;             const char* a3 = a2 + kstep; const char* b3 = b2 + kstep;
;             if (last && has_next) S.a_ready(nxt);
;             if constexpr (SP2) {
;             PG8_LDB(B0, 0, 0); PG8_LDB(B1, 0, 1); PG8_SCHED; PG8_LDA(At, 0, 0); PG8_STAGE(PG8_SA(1, 1), a1 + hstepA, voffA);
;             PG8_WAIT_V(8); PG8_WAIT_L(0); PG8_BAR; PG8_MMA(0, 0, At, B0); PG8_MMA(0, 1, At, B1); PG8_BAR; PG8_SCHED;
;             PG8_LDA(At, 0, 1); PG8_STAGE(PG8_SB(0, 0), b2, voffB); PG8_STAGE(PG8_SB(0, 1), b2 + hstepB, voffB); PG8_STAGE(PG8_SA(0, 0), a2, voffA);
;             PG8_WAIT_V(8); PG8_WAIT_L(0); PG8_BAR; PG8_MMA(1, 0, At, B0); PG8_MMA(1, 1, At, B1); PG8_BAR; PG8_SCHED;
.LBB0_2897:
	ds_read_b128 v[128:131], v190
	ds_read_b128 v[132:135], v190 offset:1024
	ds_read_b128 v[136:139], v190 offset:2048
	ds_read_b128 v[140:143], v190 offset:3072
	ds_read_b128 v[144:147], v191
	ds_read_b128 v[148:151], v191 offset:1024
	ds_read_b128 v[172:175], v191 offset:2048
	ds_read_b128 v[176:179], v191 offset:3072
	s_add_u32 s24, s22, 0x100
	s_addc_u32 s25, s23, 0
	s_cmp_eq_u32 s58, 40
	s_cselect_b32 s29, s7, s25
	s_cselect_b32 s28, s6, s24
	s_cselect_b32 s27, s21, s57
	s_cselect_b32 s26, s20, s56
	s_add_i32 m0, s34, 0xc000
	ds_read_b128 v[180:183], v192
	ds_read_b128 v[184:187], v192 offset:1024
	ds_read_b128 v[194:197], v192 offset:2048
	ds_read_b128 v[198:201], v192 offset:3072
	ds_read_b128 v[202:205], v192 offset:4096
	ds_read_b128 v[206:209], v192 offset:5120
	ds_read_b128 v[210:213], v192 offset:6144
	ds_read_b128 v[214:217], v192 offset:7168
	global_load_lds_dwordx4 v164, s[22:23]
	s_add_i32 m0, s34, 0xe000
	s_nop 0
	global_load_lds_dwordx4 v166, s[22:23]
	s_waitcnt vmcnt(8) lgkmcnt(0)
	s_barrier
	s_setprio 1
	v_mfma_f32_16x16x32_bf16 v[124:127], v[128:131], v[180:183], v[124:127]
	v_mfma_f32_16x16x32_bf16 v[120:123], v[136:139], v[180:183], v[120:123]
	v_mfma_f32_16x16x32_bf16 v[108:111], v[128:131], v[194:197], v[108:111]
	v_mfma_f32_16x16x32_bf16 v[104:107], v[136:139], v[194:197], v[104:107]
	v_mfma_f32_16x16x32_bf16 v[92:95], v[128:131], v[202:205], v[92:95]
	v_mfma_f32_16x16x32_bf16 v[88:91], v[136:139], v[202:205], v[88:91]
	v_mfma_f32_16x16x32_bf16 v[76:79], v[128:131], v[210:213], v[76:79]
	v_mfma_f32_16x16x32_bf16 v[72:75], v[136:139], v[210:213], v[72:75]
	v_mfma_f32_16x16x32_bf16 v[124:127], v[132:135], v[184:187], v[124:127]
	v_mfma_f32_16x16x32_bf16 v[120:123], v[140:143], v[184:187], v[120:123]
	v_mfma_f32_16x16x32_bf16 v[108:111], v[132:135], v[198:201], v[108:111]
	v_mfma_f32_16x16x32_bf16 v[104:107], v[140:143], v[198:201], v[104:107]
	v_mfma_f32_16x16x32_bf16 v[92:95], v[132:135], v[206:209], v[92:95]
	v_mfma_f32_16x16x32_bf16 v[88:91], v[140:143], v[206:209], v[88:91]
	v_mfma_f32_16x16x32_bf16 v[76:79], v[132:135], v[214:217], v[76:79]
	v_mfma_f32_16x16x32_bf16 v[72:75], v[140:143], v[214:217], v[72:75]
	v_mfma_f32_16x16x32_bf16 v[116:119], v[144:147], v[180:183], v[116:119]
	v_mfma_f32_16x16x32_bf16 v[112:115], v[172:175], v[180:183], v[112:115]
	v_mfma_f32_16x16x32_bf16 v[100:103], v[144:147], v[194:197], v[100:103]
	v_mfma_f32_16x16x32_bf16 v[96:99], v[172:175], v[194:197], v[96:99]
	v_mfma_f32_16x16x32_bf16 v[84:87], v[144:147], v[202:205], v[84:87]
	v_mfma_f32_16x16x32_bf16 v[80:83], v[172:175], v[202:205], v[80:83]
	v_mfma_f32_16x16x32_bf16 v[68:71], v[144:147], v[210:213], v[68:71]
	v_mfma_f32_16x16x32_bf16 v[64:67], v[172:175], v[210:213], v[64:67]
	v_mfma_f32_16x16x32_bf16 v[116:119], v[148:151], v[184:187], v[116:119]
	v_mfma_f32_16x16x32_bf16 v[112:115], v[176:179], v[184:187], v[112:115]
	v_mfma_f32_16x16x32_bf16 v[100:103], v[148:151], v[198:201], v[100:103]
	v_mfma_f32_16x16x32_bf16 v[96:99], v[176:179], v[198:201], v[96:99]
	v_mfma_f32_16x16x32_bf16 v[84:87], v[148:151], v[206:209], v[84:87]
	v_mfma_f32_16x16x32_bf16 v[80:83], v[176:179], v[206:209], v[80:83]
	v_mfma_f32_16x16x32_bf16 v[68:71], v[148:151], v[214:217], v[68:71]
	v_mfma_f32_16x16x32_bf16 v[64:67], v[176:179], v[214:217], v[64:67]
	s_setprio 0
	s_barrier
	s_add_i32 s22, s43, s33
	v_lshl_add_u64 v[218:219], s[26:27], 0, v[154:155]
	s_mov_b32 m0, s22
	ds_read_b128 v[180:183], v192 offset:16384
	ds_read_b128 v[184:187], v192 offset:17408
	ds_read_b128 v[194:197], v192 offset:18432
	ds_read_b128 v[198:201], v192 offset:19456
	ds_read_b128 v[202:205], v192 offset:20480
	ds_read_b128 v[206:209], v192 offset:21504
	ds_read_b128 v[210:213], v192 offset:22528
	ds_read_b128 v[214:217], v192 offset:23552
	global_load_lds_dwordx4 v154, s[26:27]
	s_add_i32 m0, s22, 0x2000
	s_add_u32 s22, s26, 0xb0000
	v_lshl_add_u64 v[220:221], s[26:27], 0, v[158:159]
	s_addc_u32 s23, s27, 0
	s_add_i32 s59, s44, s33
	global_load_lds_dwordx4 v158, s[26:27]
	s_mov_b32 m0, s59
	v_lshl_add_u64 v[224:225], s[28:29], 0, v[156:157]
	global_load_lds_dwordx4 v154, s[22:23]
	s_add_i32 m0, s59, 0x2000
	s_nop 0
	global_load_lds_dwordx4 v158, s[22:23]
	v_lshl_add_u64 v[222:223], s[28:29], 0, v[152:153]
	s_mov_b32 m0, s34
	s_nop 0
	global_load_lds_dwordx4 v152, s[28:29]
	s_mov_b32 m0, s35
	s_nop 0
	global_load_lds_dwordx4 v156, s[28:29]
	s_waitcnt vmcnt(8) lgkmcnt(0)
	s_barrier
	s_setprio 1
	v_mfma_f32_16x16x32_bf16 v[60:63], v[128:131], v[180:183], v[60:63]
	v_mfma_f32_16x16x32_bf16 v[56:59], v[136:139], v[180:183], v[56:59]
	v_mfma_f32_16x16x32_bf16 v[44:47], v[128:131], v[194:197], v[44:47]
	v_mfma_f32_16x16x32_bf16 v[40:43], v[136:139], v[194:197], v[40:43]
	v_mfma_f32_16x16x32_bf16 v[28:31], v[128:131], v[202:205], v[28:31]
	v_mfma_f32_16x16x32_bf16 v[24:27], v[136:139], v[202:205], v[24:27]
	v_mfma_f32_16x16x32_bf16 v[12:15], v[128:131], v[210:213], v[12:15]
	v_mfma_f32_16x16x32_bf16 v[8:11], v[136:139], v[210:213], v[8:11]
	v_mfma_f32_16x16x32_bf16 v[60:63], v[132:135], v[184:187], v[60:63]
	v_mfma_f32_16x16x32_bf16 v[56:59], v[140:143], v[184:187], v[56:59]
	v_mfma_f32_16x16x32_bf16 v[44:47], v[132:135], v[198:201], v[44:47]
	v_mfma_f32_16x16x32_bf16 v[40:43], v[140:143], v[198:201], v[40:43]
	v_mfma_f32_16x16x32_bf16 v[28:31], v[132:135], v[206:209], v[28:31]
	v_mfma_f32_16x16x32_bf16 v[24:27], v[140:143], v[206:209], v[24:27]
	v_mfma_f32_16x16x32_bf16 v[12:15], v[132:135], v[214:217], v[12:15]
	v_mfma_f32_16x16x32_bf16 v[8:11], v[140:143], v[214:217], v[8:11]
	v_mfma_f32_16x16x32_bf16 v[52:55], v[144:147], v[180:183], v[52:55]
	v_mfma_f32_16x16x32_bf16 v[48:51], v[172:175], v[180:183], v[48:51]
	v_mfma_f32_16x16x32_bf16 v[36:39], v[144:147], v[194:197], v[36:39]
	v_mfma_f32_16x16x32_bf16 v[32:35], v[172:175], v[194:197], v[32:35]
	v_mfma_f32_16x16x32_bf16 v[20:23], v[144:147], v[202:205], v[20:23]
	v_mfma_f32_16x16x32_bf16 v[16:19], v[172:175], v[202:205], v[16:19]
	v_mfma_f32_16x16x32_bf16 v[4:7], v[144:147], v[210:213], v[4:7]
	v_mfma_f32_16x16x32_bf16 v[0:3], v[172:175], v[210:213], v[0:3]
	v_mfma_f32_16x16x32_bf16 v[52:55], v[148:151], v[184:187], v[52:55]
	v_mfma_f32_16x16x32_bf16 v[48:51], v[176:179], v[184:187], v[48:51]
	v_mfma_f32_16x16x32_bf16 v[36:39], v[148:151], v[198:201], v[36:39]
	v_mfma_f32_16x16x32_bf16 v[32:35], v[176:179], v[198:201], v[32:35]
	v_mfma_f32_16x16x32_bf16 v[20:23], v[148:151], v[206:209], v[20:23]
	v_mfma_f32_16x16x32_bf16 v[16:19], v[176:179], v[206:209], v[16:19]
	v_mfma_f32_16x16x32_bf16 v[4:7], v[148:151], v[214:217], v[4:7]
	v_mfma_f32_16x16x32_bf16 v[0:3], v[176:179], v[214:217], v[0:3]
	s_setprio 0
	s_barrier
; #define PG8_STAGE(bufoff, gbase, voff) do { _Pragma("unroll") for (int _i = 0; _i < 2; ++_i) \
;         __builtin_amdgcn_global_load_lds((const unsigned*)((const char*)(gbase) + (voff)[_i]), (PG8_LAS unsigned*)(lds + (bufoff) + ldsw + _i * 8192), 16, 0, 0); } while (0)
; #define PG8_LDA(dst, b, h) do { _Pragma("unroll") for (int m = 0; m < 4; ++m) _Pragma("unroll") for (int k = 0; k < 2; ++k) dst[m][k] = *(const PG8_LAS bf16x8*)(lds + PG8_SA(b, h) + aoff + m * 2048 + k * 1024); } while (0)
; #define PG8_LDB(dst, b, h) do { _Pragma("unroll") for (int n = 0; n < 2; ++n) _Pragma("unroll") for (int k = 0; k < 2; ++k) dst[n][k] = *(const PG8_LAS bf16x8*)(lds + PG8_SB(b, h) + boff + n * 2048 + k * 1024); } while (0)
; #define PG8_MMA(ai, bj, At, Bt) do { __builtin_amdgcn_s_setprio(1); _Pragma("unroll") for (int m = 0; m < 4; ++m) _Pragma("unroll") for (int n = 0; n < 2; ++n) _Pragma("unroll") for (int k = 0; k < 2; ++k) \
;         acc[ai][bj][m][n] = __builtin_amdgcn_mfma_f32_16x16x32_bf16(Bt[n][k], At[m][k], acc[ai][bj][m][n], 0, 0, 0); __builtin_amdgcn_s_setprio(0); } while (0)
; #define PG8_WAIT_V(n) asm volatile("s_waitcnt vmcnt(" #n ")" ::: "memory")
; #define PG8_WAIT_L(n) asm volatile("s_waitcnt lgkmcnt(" #n ")" ::: "memory")
; #define PG8_BAR __builtin_amdgcn_s_barrier()
; #define PG8_SCHED __builtin_amdgcn_sched_barrier(0)
; template <class Epi, class Sched, bool ALIGN_EPI = false, bool SP2 = false>
; __device__ __forceinline__ void gemm_phase(PG8_LAS unsigned char* lds, const Gemm g, const Sched& S, const Epi& E, const int wid) {
;     ...
;             PG8_LDB(B0, 1, 0); PG8_LDB(B1, 1, 1); PG8_SCHED; PG8_LDA(At, 1, 0); PG8_STAGE(PG8_SA(0, 1), a2 + hstepA, voffA);
;             PG8_WAIT_V(8); PG8_WAIT_L(0); PG8_BAR; PG8_MMA(0, 0, At, B0); PG8_MMA(0, 1, At, B1); PG8_BAR; PG8_SCHED;
;             PG8_LDA(At, 1, 1); PG8_STAGE(PG8_SB(1, 0), b3, voffB); PG8_STAGE(PG8_SB(1, 1), b3 + hstepB, voffB); PG8_STAGE(PG8_SA(1, 0), a3, voffA);
;             PG8_WAIT_V(8); PG8_WAIT_L(0); PG8_BAR; PG8_MMA(1, 0, At, B0); PG8_MMA(1, 1, At, B1); PG8_BAR; PG8_SCHED;
;     ...
;         if constexpr (ALIGN_EPI) { if (wr == 0) PG8_BAR; }
	s_add_i32 s59, 0, 0x18000
	s_add_i32 s60, 0, 0x1c000
	v_add_u32_e32 v140, s59, v189
	v_add_u32_e32 v176, s60, v189
	ds_read_b128 v[128:131], v140
	ds_read_b128 v[132:135], v140 offset:1024
	ds_read_b128 v[136:139], v140 offset:2048
	ds_read_b128 v[140:143], v140 offset:3072
	ds_read_b128 v[144:147], v176
	ds_read_b128 v[148:151], v176 offset:1024
	ds_read_b128 v[172:175], v176 offset:2048
	ds_read_b128 v[176:179], v176 offset:3072
	s_add_u32 s22, s28, 0xb0000
	s_addc_u32 s23, s29, 0
	s_mov_b32 m0, s36
	ds_read_b128 v[180:183], v192 offset:32768
	ds_read_b128 v[184:187], v192 offset:33792
	ds_read_b128 v[194:197], v192 offset:34816
	ds_read_b128 v[198:201], v192 offset:35840
	ds_read_b128 v[202:205], v192 offset:36864
	ds_read_b128 v[206:209], v192 offset:37888
	ds_read_b128 v[210:213], v192 offset:38912
	ds_read_b128 v[214:217], v192 offset:39936
	global_load_lds_dwordx4 v152, s[22:23]
	s_mov_b32 m0, s37
	s_nop 0
	global_load_lds_dwordx4 v156, s[22:23]
	s_waitcnt vmcnt(8) lgkmcnt(0)
	s_barrier
	s_setprio 1
	v_mfma_f32_16x16x32_bf16 v[124:127], v[128:131], v[180:183], v[124:127]
	v_mfma_f32_16x16x32_bf16 v[120:123], v[136:139], v[180:183], v[120:123]
	v_mfma_f32_16x16x32_bf16 v[108:111], v[128:131], v[194:197], v[108:111]
	v_mfma_f32_16x16x32_bf16 v[104:107], v[136:139], v[194:197], v[104:107]
	v_mfma_f32_16x16x32_bf16 v[92:95], v[128:131], v[202:205], v[92:95]
	v_mfma_f32_16x16x32_bf16 v[88:91], v[136:139], v[202:205], v[88:91]
	v_mfma_f32_16x16x32_bf16 v[76:79], v[128:131], v[210:213], v[76:79]
	v_mfma_f32_16x16x32_bf16 v[72:75], v[136:139], v[210:213], v[72:75]
	v_mfma_f32_16x16x32_bf16 v[124:127], v[132:135], v[184:187], v[124:127]
	v_mfma_f32_16x16x32_bf16 v[120:123], v[140:143], v[184:187], v[120:123]
	v_mfma_f32_16x16x32_bf16 v[108:111], v[132:135], v[198:201], v[108:111]
	v_mfma_f32_16x16x32_bf16 v[104:107], v[140:143], v[198:201], v[104:107]
	v_mfma_f32_16x16x32_bf16 v[92:95], v[132:135], v[206:209], v[92:95]
	v_mfma_f32_16x16x32_bf16 v[88:91], v[140:143], v[206:209], v[88:91]
	v_mfma_f32_16x16x32_bf16 v[76:79], v[132:135], v[214:217], v[76:79]
	v_mfma_f32_16x16x32_bf16 v[72:75], v[140:143], v[214:217], v[72:75]
	v_mfma_f32_16x16x32_bf16 v[116:119], v[144:147], v[180:183], v[116:119]
	v_mfma_f32_16x16x32_bf16 v[112:115], v[172:175], v[180:183], v[112:115]
	v_mfma_f32_16x16x32_bf16 v[100:103], v[144:147], v[194:197], v[100:103]
	v_mfma_f32_16x16x32_bf16 v[96:99], v[172:175], v[194:197], v[96:99]
	v_mfma_f32_16x16x32_bf16 v[84:87], v[144:147], v[202:205], v[84:87]
	v_mfma_f32_16x16x32_bf16 v[80:83], v[172:175], v[202:205], v[80:83]
	v_mfma_f32_16x16x32_bf16 v[68:71], v[144:147], v[210:213], v[68:71]
	v_mfma_f32_16x16x32_bf16 v[64:67], v[172:175], v[210:213], v[64:67]
	v_mfma_f32_16x16x32_bf16 v[116:119], v[148:151], v[184:187], v[116:119]
	v_mfma_f32_16x16x32_bf16 v[112:115], v[176:179], v[184:187], v[112:115]
	v_mfma_f32_16x16x32_bf16 v[100:103], v[148:151], v[198:201], v[100:103]
	v_mfma_f32_16x16x32_bf16 v[96:99], v[176:179], v[198:201], v[96:99]
	v_mfma_f32_16x16x32_bf16 v[84:87], v[148:151], v[206:209], v[84:87]
	v_mfma_f32_16x16x32_bf16 v[80:83], v[176:179], v[206:209], v[80:83]
	v_mfma_f32_16x16x32_bf16 v[68:71], v[148:151], v[214:217], v[68:71]
	v_mfma_f32_16x16x32_bf16 v[64:67], v[176:179], v[214:217], v[64:67]
	s_setprio 0
	s_barrier
	s_add_i32 s22, s59, s33
	v_lshl_add_u64 v[218:219], v[218:219], 0, s[16:17]
	s_mov_b32 m0, s22
	ds_read_b128 v[180:183], v192 offset:49152
	ds_read_b128 v[184:187], v192 offset:50176
	ds_read_b128 v[194:197], v192 offset:51200
	ds_read_b128 v[198:201], v192 offset:52224
	ds_read_b128 v[202:205], v192 offset:53248
	ds_read_b128 v[206:209], v192 offset:54272
	ds_read_b128 v[210:213], v192 offset:55296
	ds_read_b128 v[214:217], v192 offset:56320
	global_load_lds_dwordx4 v[218:219], off
	s_add_i32 m0, s22, 0x2000
	s_add_u32 s22, s26, 0xb0080
	v_lshl_add_u64 v[218:219], v[220:221], 0, s[16:17]
	s_addc_u32 s23, s27, 0
	s_add_i32 s26, s60, s33
	global_load_lds_dwordx4 v[218:219], off
	s_mov_b32 m0, s26
	s_nop 0
	global_load_lds_dwordx4 v154, s[22:23]
	v_lshl_add_u64 v[218:219], s[22:23], 0, v[158:159]
	s_add_i32 m0, s26, 0x2000
	s_nop 0
	global_load_lds_dwordx4 v158, s[22:23]
	v_lshl_add_u64 v[218:219], v[222:223], 0, s[16:17]
	s_mov_b32 m0, s39
	s_nop 0
	global_load_lds_dwordx4 v[218:219], off
	v_lshl_add_u64 v[218:219], v[224:225], 0, s[16:17]
	s_mov_b32 m0, s40
	s_nop 0
	global_load_lds_dwordx4 v[218:219], off
	s_waitcnt vmcnt(8) lgkmcnt(0)
	s_barrier
	s_setprio 1
	v_mfma_f32_16x16x32_bf16 v[60:63], v[128:131], v[180:183], v[60:63]
	v_mfma_f32_16x16x32_bf16 v[56:59], v[136:139], v[180:183], v[56:59]
	v_mfma_f32_16x16x32_bf16 v[44:47], v[128:131], v[194:197], v[44:47]
	v_mfma_f32_16x16x32_bf16 v[40:43], v[136:139], v[194:197], v[40:43]
	v_mfma_f32_16x16x32_bf16 v[28:31], v[128:131], v[202:205], v[28:31]
	v_mfma_f32_16x16x32_bf16 v[24:27], v[136:139], v[202:205], v[24:27]
	v_mfma_f32_16x16x32_bf16 v[12:15], v[128:131], v[210:213], v[12:15]
	v_mfma_f32_16x16x32_bf16 v[8:11], v[136:139], v[210:213], v[8:11]
	v_mfma_f32_16x16x32_bf16 v[60:63], v[132:135], v[184:187], v[60:63]
	v_mfma_f32_16x16x32_bf16 v[56:59], v[140:143], v[184:187], v[56:59]
	v_mfma_f32_16x16x32_bf16 v[44:47], v[132:135], v[198:201], v[44:47]
	v_mfma_f32_16x16x32_bf16 v[40:43], v[140:143], v[198:201], v[40:43]
	v_mfma_f32_16x16x32_bf16 v[28:31], v[132:135], v[206:209], v[28:31]
	v_mfma_f32_16x16x32_bf16 v[24:27], v[140:143], v[206:209], v[24:27]
	v_mfma_f32_16x16x32_bf16 v[12:15], v[132:135], v[214:217], v[12:15]
	v_mfma_f32_16x16x32_bf16 v[8:11], v[140:143], v[214:217], v[8:11]
	v_mfma_f32_16x16x32_bf16 v[52:55], v[144:147], v[180:183], v[52:55]
	v_mfma_f32_16x16x32_bf16 v[48:51], v[172:175], v[180:183], v[48:51]
	v_mfma_f32_16x16x32_bf16 v[36:39], v[144:147], v[194:197], v[36:39]
	v_mfma_f32_16x16x32_bf16 v[32:35], v[172:175], v[194:197], v[32:35]
	v_mfma_f32_16x16x32_bf16 v[20:23], v[144:147], v[202:205], v[20:23]
	v_mfma_f32_16x16x32_bf16 v[16:19], v[172:175], v[202:205], v[16:19]
	v_mfma_f32_16x16x32_bf16 v[4:7], v[144:147], v[210:213], v[4:7]
	v_mfma_f32_16x16x32_bf16 v[0:3], v[172:175], v[210:213], v[0:3]
	v_mfma_f32_16x16x32_bf16 v[52:55], v[148:151], v[184:187], v[52:55]
	v_mfma_f32_16x16x32_bf16 v[48:51], v[176:179], v[184:187], v[48:51]
	v_mfma_f32_16x16x32_bf16 v[36:39], v[148:151], v[198:201], v[36:39]
	v_mfma_f32_16x16x32_bf16 v[32:35], v[176:179], v[198:201], v[32:35]
	v_mfma_f32_16x16x32_bf16 v[20:23], v[148:151], v[206:209], v[20:23]
	v_mfma_f32_16x16x32_bf16 v[16:19], v[176:179], v[206:209], v[16:19]
	v_mfma_f32_16x16x32_bf16 v[4:7], v[148:151], v[214:217], v[4:7]
	v_mfma_f32_16x16x32_bf16 v[0:3], v[176:179], v[214:217], v[0:3]
	s_setprio 0
	s_barrier
	s_add_i32 s58, s58, 2
	s_add_u32 s56, s56, 0x100
	s_addc_u32 s57, s57, 0
	s_cmp_gt_u32 s58, 41
	s_mov_b64 s[22:23], s[24:25]
	s_cbranch_scc0 .LBB0_2897
	s_and_b64 vcc, exec, s[18:19]
	s_cbranch_vccz .LBB0_2900
	s_barrier
